# IEEE f32 division expansions replaced by v_rcp_f32 (1 ulp) in gate epilogues, rwkv prep, moe silu, chunk pass A; plus earlier load de-serialisation
# speedup vs baseline: 1.0172x; 1.0172x over previous
; #define LAS __attribute__((address_space(3)))
; DI float sigmoidf_(float x) { return 1.f / (1.f + __expf(-x)); }
; DI void phase_rwkvprep(const Args& a, int l, LAS unsigned char* lds, int tid, int gw, int NGW, int lane) {
;     ...
;             const f32x4 mr = *(const LAS f32x4*)(par + c0), mk = *(const LAS f32x4*)(par + C + c0), mv = *(const LAS f32x4*)(par + 2 * C + c0);
;             const f32x4 w0v = *(const LAS f32x4*)(par + 3 * C + c0), a0v = *(const LAS f32x4*)(par + 4 * C + c0), kkw = *(const LAS f32x4*)(par + 5 * C + c0), kaw = *(const LAS f32x4*)(par + 6 * C + c0), rkw = *(const LAS f32x4*)(par + 7 * C + c0);
;             const f32x4 v0v = *(const LAS f32x4*)(par + 8 * C + c0);
;             f32x4 ro, wo, ko, vo, go;
; #pragma unroll
;             for (int j = 0; j < 4; ++j) {
;                 const float rc = (j & 1) ? bfhi(j < 2 ? zr_.x : zr_.y) : bflo(j < 2 ? zr_.x : zr_.y), rp = (j & 1) ? bfhi(j < 2 ? pr_.x : pr_.y) : bflo(j < 2 ? pr_.x : pr_.y);
;                 const float kc = (j & 1) ? bfhi(j < 2 ? zk_.x : zk_.y) : bflo(j < 2 ? zk_.x : zk_.y), kp = (j & 1) ? bfhi(j < 2 ? pk_.x : pk_.y) : bflo(j < 2 ? pk_.x : pk_.y);
;                 const float vc = (j & 1) ? bfhi(j < 2 ? zv_.x : zv_.y) : bflo(j < 2 ? zv_.x : zv_.y), vp = (j & 1) ? bfhi(j < 2 ? pv_.x : pv_.y) : bflo(j < 2 ? pv_.x : pv_.y);
;                 const float vfj = (j & 1) ? bfhi(j < 2 ? vfw.x : vfw.y) : bflo(j < 2 ? vfw.x : vfw.y);
;                 const float r = rc + (rp - rc) * mr[j]; float k = kc + (kp - kc) * mk[j]; float v = vc + (vp - vc) * mv[j];
;                 const float xw = -(w0v[j] + aw[j]);
;                 const float sp = fmaxf(xw, 0.f) + __logf(1.f + __expf(-fabsf(xw)));
;                 const float wlog = -sp - 0.5f; const float dec = __expf(-__expf(wlog));
;                 const float aval = sigmoidf_(a0v[j] + aa[j]);
;                 if (l > 0) v = v + (vfj - v) * sigmoidf_(v0v[j] + avr[j]);
.LBB0_888:
	s_waitcnt vmcnt(9)
	v_lshlrev_b32_e32 v139, 16, v150
	v_lshlrev_b32_e32 v90, 16, v148
	v_lshl_add_u32 v209, v197, 2, 0
	v_sub_f32_e32 v139, v139, v90
	ds_read_b128 v[92:95], v209 offset:4096
	ds_read_b128 v[104:107], v209 offset:8192
	ds_read_b128 v[86:89], v209 offset:12288
	ds_read_b128 v[50:53], v209 offset:16384
	ds_read_b128 v[34:37], v209 offset:20480
	ds_read_b128 v[42:45], v209 offset:24576
	ds_read_b128 v[30:33], v209 offset:28672
	ds_read_b128 v[96:99], v209
	ds_read_b128 v[108:111], v209 offset:32768
	s_and_b64 vcc, exec, s[38:39]
	s_waitcnt lgkmcnt(7)
	v_fmac_f32_e32 v90, v139, v104
	s_cbranch_vccnz .LBB0_890
	s_waitcnt lgkmcnt(0)
	v_add_f32_e32 v100, v100, v108
	v_mul_f32_e32 v100, 0xbfb8aa3b, v100
	v_exp_f32_e32 v100, v100
	v_lshlrev_b32_e32 v104, 16, v146
	v_sub_f32_e32 v104, v104, v90
	v_add_f32_e32 v100, 1.0, v100
	v_rcp_f32_e32 v100, v100
	s_nop 0
	v_fmac_f32_e32 v90, v104, v100
.LBB0_890:
	v_and_b32_e32 v100, 0xffff0000, v148
	v_and_b32_e32 v104, 0xffff0000, v150
	v_sub_f32_e32 v104, v104, v100
	s_and_b64 vcc, exec, s[38:39]
	v_fmac_f32_e32 v100, v104, v105
	s_cbranch_vccnz .LBB0_892
	s_waitcnt lgkmcnt(0)
	v_add_f32_e32 v101, v101, v109
	v_mul_f32_e32 v101, 0xbfb8aa3b, v101
	v_exp_f32_e32 v101, v101
	v_and_b32_e32 v104, 0xffff0000, v146
	v_sub_f32_e32 v104, v104, v100
	v_add_f32_e32 v101, 1.0, v101
	v_rcp_f32_e32 v101, v101
	s_nop 0
	v_fmac_f32_e32 v100, v104, v101
.LBB0_892:
	v_lshlrev_b32_e32 v101, 16, v149
	v_lshlrev_b32_e32 v104, 16, v151
	v_sub_f32_e32 v104, v104, v101
	s_and_b64 vcc, exec, s[38:39]
	v_fmac_f32_e32 v101, v104, v106
	s_cbranch_vccnz .LBB0_894
	s_waitcnt lgkmcnt(0)
	v_add_f32_e32 v102, v102, v110
	v_mul_f32_e32 v102, 0xbfb8aa3b, v102
	v_exp_f32_e32 v102, v102
	v_lshlrev_b32_e32 v104, 16, v147
	v_sub_f32_e32 v104, v104, v101
	v_add_f32_e32 v102, 1.0, v102
	v_rcp_f32_e32 v102, v102
	s_nop 0
	v_fmac_f32_e32 v101, v104, v102
.LBB0_894:
	v_and_b32_e32 v102, 0xffff0000, v149
	v_and_b32_e32 v104, 0xffff0000, v151
	v_sub_f32_e32 v104, v104, v102
	s_and_b64 vcc, exec, s[38:39]
	v_fmac_f32_e32 v102, v104, v107
	s_cbranch_vccnz .LBB0_896
	s_waitcnt lgkmcnt(0)
	v_add_f32_e32 v103, v103, v111
	v_mul_f32_e32 v103, 0xbfb8aa3b, v103
	v_exp_f32_e32 v103, v103
	v_and_b32_e32 v104, 0xffff0000, v147
	v_sub_f32_e32 v104, v104, v102
	v_add_f32_e32 v103, 1.0, v103
	v_rcp_f32_e32 v103, v103
	s_nop 0
	v_fmac_f32_e32 v102, v104, v103
; DI unsigned pk2(float a, float b) { f32x2 v = {a, b}; bf16x2_t r = __builtin_convertvector(v, bf16x2_t); return __builtin_bit_cast(unsigned, r); }
; DI float sigmoidf_(float x) { return 1.f / (1.f + __expf(-x)); }
; DI void phase_rwkvprep(const Args& a, int l, LAS unsigned char* lds, int tid, int gw, int NGW, int lane) {
;     ...
;             for (int j = 0; j < 4; ++j) {
;                 const float rc = (j & 1) ? bfhi(j < 2 ? zr_.x : zr_.y) : bflo(j < 2 ? zr_.x : zr_.y), rp = (j & 1) ? bfhi(j < 2 ? pr_.x : pr_.y) : bflo(j < 2 ? pr_.x : pr_.y);
;                 const float kc = (j & 1) ? bfhi(j < 2 ? zk_.x : zk_.y) : bflo(j < 2 ? zk_.x : zk_.y), kp = (j & 1) ? bfhi(j < 2 ? pk_.x : pk_.y) : bflo(j < 2 ? pk_.x : pk_.y);
;                 const float vc = (j & 1) ? bfhi(j < 2 ? zv_.x : zv_.y) : bflo(j < 2 ? zv_.x : zv_.y), vp = (j & 1) ? bfhi(j < 2 ? pv_.x : pv_.y) : bflo(j < 2 ? pv_.x : pv_.y);
;                 const float vfj = (j & 1) ? bfhi(j < 2 ? vfw.x : vfw.y) : bflo(j < 2 ? vfw.x : vfw.y);
;                 const float r = rc + (rp - rc) * mr[j]; float k = kc + (kp - kc) * mk[j]; float v = vc + (vp - vc) * mv[j];
;                 const float xw = -(w0v[j] + aw[j]);
;                 const float sp = fmaxf(xw, 0.f) + __logf(1.f + __expf(-fabsf(xw)));
;                 const float wlog = -sp - 0.5f; const float dec = __expf(-__expf(wlog));
;                 const float aval = sigmoidf_(a0v[j] + aa[j]);
;                 if (l > 0) v = v + (vfj - v) * sigmoidf_(v0v[j] + avr[j]);
;                 const float kk = k * kkw[j]; ss += kk * kk;
;                 k = k * (1.f + (aval - 1.f) * kaw[j]);
;                 rks += r * k * rkw[j];
;                 kkv[ct][j] = kk; av[ct][j] = aval;
;                 ro[j] = r; wo[j] = dec; ko[j] = k; vo[j] = v; go[j] = ag[j]; }
;             const size_t o = (size_t)row * C + c0;
;             *(u32x2*)(Rr + o) = (u32x2){pk2(ro[0], ro[1]), pk2(ro[2], ro[3])}; *(f32x4*)(Ww + o) = wo; *(u32x2*)(Kk + o) = (u32x2){pk2(ko[0], ko[1]), pk2(ko[2], ko[3])};
;             const u32x2 vpk = {pk2(vo[0], vo[1]), pk2(vo[2], vo[3])}; *(u32x2*)(Vv + o) = vpk; *(u32x2*)(Gg + o) = (u32x2){pk2(go[0], go[1]), pk2(go[2], go[3])};
;             if (l == 0) *(u32x2*)(VF + o) = vpk; }
.LBB0_896:
	s_waitcnt lgkmcnt(6)
	v_add_f32_e32 v54, v54, v86
	s_mov_b32 s2, 0xbfb8aa3b
	v_max_f32_e64 v86, -v54, 0
	v_mul_f32_e64 v54, |v54|, s2
	v_exp_f32_e32 v54, v54
	v_lshlrev_b32_e32 v139, 16, v114
	v_lshlrev_b32_e32 v103, 16, v116
	v_lshlrev_b32_e32 v198, 16, v112
	v_lshlrev_b32_e32 v104, 16, v118
	v_sub_f32_e32 v103, v103, v139
	v_add_f32_e32 v54, 1.0, v54
	s_waitcnt lgkmcnt(1)
	v_fmac_f32_e32 v139, v103, v96
	v_sub_f32_e32 v96, v104, v198
	v_cmp_gt_f32_e32 vcc, s14, v54
	v_fmac_f32_e32 v198, v96, v92
	v_add_f32_e32 v46, v46, v50
	v_cndmask_b32_e64 v92, 0, 32, vcc
	v_ldexp_f32 v54, v54, v92
	v_log_f32_e32 v54, v54
	v_mul_f32_e32 v46, 0xbfb8aa3b, v46
	s_mov_b32 s3, 0x3f317217
	v_exp_f32_e32 v46, v46
	v_mul_f32_e32 v92, 0x3f317217, v54
	v_fma_f32 v92, v54, s3, -v92
	v_fmac_f32_e32 v92, 0x3377d1cf, v54
	s_mov_b32 s4, 0x7f800000
	v_fmac_f32_e32 v92, 0x3f317217, v54
	v_cmp_lt_f32_e64 s[48:49], |v54|, s4
	v_add_f32_e32 v46, 1.0, v46
	s_nop 0
	v_cndmask_b32_e64 v54, v54, v92, s[48:49]
	v_cndmask_b32_e32 v92, 0, v224, vcc
	v_sub_f32_e32 v54, v54, v92
	v_add_f32_e32 v54, v86, v54
	v_and_b32_e32 v199, 0xffff0000, v114
	v_and_b32_e32 v201, 0xffff0000, v112
	v_lshlrev_b32_e32 v202, 16, v115
	v_rcp_f32_e32 v146, v46
	s_nop 0
	v_add_f32_e32 v46, -1.0, v146
	v_fma_f32 v42, v42, v46, 1.0
	v_mul_f32_e32 v200, v198, v42
	v_and_b32_e32 v42, 0xffff0000, v116
	v_and_b32_e32 v46, 0xffff0000, v118
	v_sub_f32_e32 v42, v42, v199
	v_fmac_f32_e32 v199, v42, v97
	v_sub_f32_e32 v42, v46, v201
	v_fmac_f32_e32 v201, v42, v93
	v_add_f32_e32 v42, v55, v87
	v_max_f32_e64 v46, -v42, 0
	v_mul_f32_e64 v42, |v42|, s2
	v_exp_f32_e32 v42, v42
	v_lshlrev_b32_e32 v204, 16, v113
	v_and_b32_e32 v205, 0xffff0000, v115
	v_and_b32_e32 v207, 0xffff0000, v113
	v_add_f32_e32 v42, 1.0, v42
	v_cmp_gt_f32_e32 vcc, s14, v42
	v_sub_f32_e32 v54, -0.5, v54
	v_mul_f32_e32 v54, 0x3fb8aa3b, v54
	v_cndmask_b32_e64 v50, 0, 32, vcc
	v_ldexp_f32 v42, v42, v50
	v_log_f32_e32 v42, v42
	v_exp_f32_e32 v54, v54
	v_lshlrev_b64 v[152:153], 10, v[140:141]
	v_cvt_pk_bf16_f32 v38, v38, v39
	v_mul_f32_e32 v50, 0x3f317217, v42
	v_fma_f32 v50, v42, s3, -v50
	v_fmac_f32_e32 v50, 0x3377d1cf, v42
	v_fmac_f32_e32 v50, 0x3f317217, v42
	v_cmp_lt_f32_e64 s[48:49], |v42|, s4
	v_mul_f32_e32 v54, 0xbfb8aa3b, v54
	v_exp_f32_e32 v54, v54
	v_cndmask_b32_e64 v42, v42, v50, s[48:49]
	v_cndmask_b32_e32 v50, 0, v224, vcc
	v_sub_f32_e32 v42, v42, v50
	v_add_f32_e32 v42, v46, v42
	v_sub_f32_e32 v42, -0.5, v42
	v_mul_f32_e32 v42, 0x3fb8aa3b, v42
	v_exp_f32_e32 v42, v42
	v_cvt_pk_bf16_f32 v39, v40, v41
	v_mul_f32_e32 v42, 0xbfb8aa3b, v42
	v_exp_f32_e32 v55, v42
	v_add_f32_e32 v42, v47, v51
	v_mul_f32_e32 v42, 0xbfb8aa3b, v42
	v_exp_f32_e32 v42, v42
	s_nop 0
	v_add_f32_e32 v42, 1.0, v42
	v_rcp_f32_e32 v147, v42
	s_nop 0
	v_add_f32_e32 v42, -1.0, v147
	v_fma_f32 v42, v43, v42, 1.0
	v_mul_f32_e32 v203, v201, v42
	v_lshlrev_b32_e32 v42, 16, v117
	v_lshlrev_b32_e32 v43, 16, v119
	v_sub_f32_e32 v42, v42, v202
	v_fmac_f32_e32 v202, v42, v98
	v_sub_f32_e32 v42, v43, v204
	v_fmac_f32_e32 v204, v42, v94
	v_add_f32_e32 v42, v56, v88
	v_max_f32_e64 v43, -v42, 0
	v_mul_f32_e64 v42, |v42|, s2
	v_exp_f32_e32 v42, v42
	s_nop 0
	v_add_f32_e32 v42, 1.0, v42
	v_cmp_gt_f32_e32 vcc, s14, v42
	s_nop 1
	v_cndmask_b32_e64 v46, 0, 32, vcc
	v_ldexp_f32 v42, v42, v46
	v_log_f32_e32 v42, v42
	s_nop 0
	v_mul_f32_e32 v46, 0x3f317217, v42
	v_fma_f32 v46, v42, s3, -v46
	v_fmac_f32_e32 v46, 0x3377d1cf, v42
	v_fmac_f32_e32 v46, 0x3f317217, v42
	v_cmp_lt_f32_e64 s[48:49], |v42|, s4
	s_nop 1
	v_cndmask_b32_e64 v42, v42, v46, s[48:49]
	v_cndmask_b32_e32 v46, 0, v224, vcc
	v_sub_f32_e32 v42, v42, v46
	v_add_f32_e32 v42, v43, v42
	v_sub_f32_e32 v42, -0.5, v42
	v_mul_f32_e32 v42, 0x3fb8aa3b, v42
	v_exp_f32_e32 v42, v42
	s_nop 0
	v_mul_f32_e32 v42, 0xbfb8aa3b, v42
	v_exp_f32_e32 v56, v42
	v_add_f32_e32 v42, v48, v52
	v_mul_f32_e32 v42, 0xbfb8aa3b, v42
	v_exp_f32_e32 v42, v42
	s_nop 0
	v_add_f32_e32 v42, 1.0, v42
	v_rcp_f32_e32 v148, v42
	s_nop 0
	v_add_f32_e32 v42, -1.0, v148
	v_fma_f32 v42, v44, v42, 1.0
	v_mul_f32_e32 v206, v204, v42
	v_and_b32_e32 v42, 0xffff0000, v117
	v_and_b32_e32 v43, 0xffff0000, v119
	v_sub_f32_e32 v42, v42, v205
	v_fmac_f32_e32 v205, v42, v99
	v_sub_f32_e32 v42, v43, v207
	v_fmac_f32_e32 v207, v42, v95
	v_add_f32_e32 v42, v57, v89
	v_max_f32_e64 v43, -v42, 0
	v_mul_f32_e64 v42, |v42|, s2
	v_exp_f32_e32 v42, v42
	s_nop 0
	v_add_f32_e32 v42, 1.0, v42
	v_cmp_gt_f32_e32 vcc, s14, v42
	s_nop 1
	v_cndmask_b32_e64 v44, 0, 32, vcc
	v_ldexp_f32 v42, v42, v44
	v_log_f32_e32 v42, v42
	s_nop 0
	v_mul_f32_e32 v44, 0x3f317217, v42
	v_fma_f32 v44, v42, s3, -v44
	v_fmac_f32_e32 v44, 0x3377d1cf, v42
	v_fmac_f32_e32 v44, 0x3f317217, v42
	v_cmp_lt_f32_e64 s[48:49], |v42|, s4
	s_nop 1
	v_cndmask_b32_e64 v42, v42, v44, s[48:49]
	v_cndmask_b32_e32 v44, 0, v224, vcc
	v_sub_f32_e32 v42, v42, v44
	v_add_f32_e32 v42, v43, v42
	v_sub_f32_e32 v42, -0.5, v42
	v_mul_f32_e32 v42, 0x3fb8aa3b, v42
	v_exp_f32_e32 v42, v42
	s_nop 0
	v_mul_f32_e32 v42, 0xbfb8aa3b, v42
	v_exp_f32_e32 v57, v42
	v_add_f32_e32 v42, v49, v53
	v_mul_f32_e32 v42, 0xbfb8aa3b, v42
	v_exp_f32_e32 v42, v42
	s_nop 0
	v_add_f32_e32 v42, 1.0, v42
	v_readlane_b32 s0, v254, 1
	v_readlane_b32 s1, v254, 2
	v_rcp_f32_e32 v149, v42
	s_nop 0
	v_add_f32_e32 v42, -1.0, v149
	v_fma_f32 v42, v45, v42, 1.0
	v_mul_f32_e32 v208, v207, v42
	v_or_b32_e32 v42, v152, v197
	v_mov_b32_e32 v43, v153
	v_lshlrev_b64 v[150:151], 1, v[42:43]
	v_cvt_pk_bf16_f32 v44, v139, v199
	v_cvt_pk_bf16_f32 v45, v202, v205
	v_lshl_add_u64 v[46:47], s[58:59], 0, v[150:151]
	global_store_dwordx2 v[46:47], v[44:45], off
	v_lshl_add_u64 v[44:45], v[42:43], 2, s[64:65]
	v_lshl_add_u64 v[40:41], s[70:71], 0, v[150:151]
	global_store_dwordx4 v[44:45], v[54:57], off
	v_cvt_pk_bf16_f32 v44, v200, v203
	v_cvt_pk_bf16_f32 v45, v206, v208
	v_lshl_add_u64 v[46:47], s[52:53], 0, v[150:151]
	global_store_dwordx2 v[40:41], v[38:39], off
	v_cndmask_b32_e64 v38, 0, 1, s[0:1]
	global_store_dwordx2 v[46:47], v[44:45], off
	v_cvt_pk_bf16_f32 v44, v90, v100
	v_cvt_pk_bf16_f32 v45, v101, v102
	v_lshl_add_u64 v[46:47], s[66:67], 0, v[150:151]
	v_cmp_ne_u32_e64 s[48:49], 1, v38
	s_andn2_b64 vcc, exec, s[0:1]
	global_store_dwordx2 v[46:47], v[44:45], off
	s_cbranch_vccnz .LBB0_898
	v_lshl_add_u64 v[38:39], v[42:43], 1, s[54:55]
	global_store_dwordx2 v[38:39], v[44:45], off

; #define LAS __attribute__((address_space(3)))
; DI float sigmoidf_(float x) { return 1.f / (1.f + __expf(-x)); }
; DI void phase_rwkvprep(const Args& a, int l, LAS unsigned char* lds, int tid, int gw, int NGW, int lane) {
;     ...
;             const f32x4 mr = *(const LAS f32x4*)(par + c0), mk = *(const LAS f32x4*)(par + C + c0), mv = *(const LAS f32x4*)(par + 2 * C + c0);
;             const f32x4 w0v = *(const LAS f32x4*)(par + 3 * C + c0), a0v = *(const LAS f32x4*)(par + 4 * C + c0), kkw = *(const LAS f32x4*)(par + 5 * C + c0), kaw = *(const LAS f32x4*)(par + 6 * C + c0), rkw = *(const LAS f32x4*)(par + 7 * C + c0);
;             const f32x4 v0v = *(const LAS f32x4*)(par + 8 * C + c0);
;             f32x4 ro, wo, ko, vo, go;
; #pragma unroll
;             for (int j = 0; j < 4; ++j) {
;                 const float rc = (j & 1) ? bfhi(j < 2 ? zr_.x : zr_.y) : bflo(j < 2 ? zr_.x : zr_.y), rp = (j & 1) ? bfhi(j < 2 ? pr_.x : pr_.y) : bflo(j < 2 ? pr_.x : pr_.y);
;                 const float kc = (j & 1) ? bfhi(j < 2 ? zk_.x : zk_.y) : bflo(j < 2 ? zk_.x : zk_.y), kp = (j & 1) ? bfhi(j < 2 ? pk_.x : pk_.y) : bflo(j < 2 ? pk_.x : pk_.y);
;                 const float vc = (j & 1) ? bfhi(j < 2 ? zv_.x : zv_.y) : bflo(j < 2 ? zv_.x : zv_.y), vp = (j & 1) ? bfhi(j < 2 ? pv_.x : pv_.y) : bflo(j < 2 ? pv_.x : pv_.y);
;                 const float vfj = (j & 1) ? bfhi(j < 2 ? vfw.x : vfw.y) : bflo(j < 2 ? vfw.x : vfw.y);
;                 const float r = rc + (rp - rc) * mr[j]; float k = kc + (kp - kc) * mk[j]; float v = vc + (vp - vc) * mv[j];
;                 const float xw = -(w0v[j] + aw[j]);
;                 const float sp = fmaxf(xw, 0.f) + __logf(1.f + __expf(-fabsf(xw)));
;                 const float wlog = -sp - 0.5f; const float dec = __expf(-__expf(wlog));
;                 const float aval = sigmoidf_(a0v[j] + aa[j]);
;                 if (l > 0) v = v + (vfj - v) * sigmoidf_(v0v[j] + avr[j]);
.LBB0_907:
	s_waitcnt vmcnt(14)
	v_lshlrev_b32_e32 v164, 16, v188
	v_lshlrev_b32_e32 v90, 16, v182
	v_sub_f32_e32 v164, v164, v90
	ds_read_b128 v[82:85], v209 offset:4160
	ds_read_b128 v[112:115], v209 offset:8256
	ds_read_b128 v[78:81], v209 offset:12352
	ds_read_b128 v[70:73], v209 offset:16448
	ds_read_b128 v[42:45], v209 offset:20544
	ds_read_b128 v[62:65], v209 offset:24640
	ds_read_b128 v[38:41], v209 offset:28736
	ds_read_b128 v[104:107], v209 offset:64
	ds_read_b128 v[116:119], v209 offset:32832
	s_and_b64 vcc, exec, s[38:39]
	s_waitcnt lgkmcnt(7)
	v_fmac_f32_e32 v90, v164, v112
	s_cbranch_vccnz .LBB0_909
	s_waitcnt lgkmcnt(0)
	v_add_f32_e32 v108, v108, v116
	v_mul_f32_e32 v108, 0xbfb8aa3b, v108
	v_exp_f32_e32 v108, v108
	v_lshlrev_b32_e32 v112, 16, v154
	v_sub_f32_e32 v112, v112, v90
	v_add_f32_e32 v108, 1.0, v108
	v_rcp_f32_e32 v108, v108
	s_nop 0
	v_fmac_f32_e32 v90, v112, v108
.LBB0_909:
	v_and_b32_e32 v108, 0xffff0000, v182
	v_and_b32_e32 v112, 0xffff0000, v188
	v_sub_f32_e32 v112, v112, v108
	s_and_b64 vcc, exec, s[38:39]
	v_fmac_f32_e32 v108, v112, v113
	s_cbranch_vccnz .LBB0_911
	s_waitcnt lgkmcnt(0)
	v_add_f32_e32 v109, v109, v117
	v_mul_f32_e32 v109, 0xbfb8aa3b, v109
	v_exp_f32_e32 v109, v109
	v_and_b32_e32 v112, 0xffff0000, v154
	v_sub_f32_e32 v112, v112, v108
	v_add_f32_e32 v109, 1.0, v109
	v_rcp_f32_e32 v109, v109
	s_nop 0
	v_fmac_f32_e32 v108, v112, v109
.LBB0_911:
	v_lshlrev_b32_e32 v109, 16, v183
	v_lshlrev_b32_e32 v112, 16, v189
	v_sub_f32_e32 v112, v112, v109
	s_and_b64 vcc, exec, s[38:39]
	v_fmac_f32_e32 v109, v112, v114
	s_cbranch_vccnz .LBB0_913
	s_waitcnt lgkmcnt(0)
	v_add_f32_e32 v110, v110, v118
	v_mul_f32_e32 v110, 0xbfb8aa3b, v110
	v_exp_f32_e32 v110, v110
	v_lshlrev_b32_e32 v112, 16, v155
	v_sub_f32_e32 v112, v112, v109
	v_add_f32_e32 v110, 1.0, v110
	v_rcp_f32_e32 v110, v110
	s_nop 0
	v_fmac_f32_e32 v109, v112, v110
.LBB0_913:
	v_and_b32_e32 v110, 0xffff0000, v183
	v_and_b32_e32 v112, 0xffff0000, v189
	v_sub_f32_e32 v112, v112, v110
	s_and_b64 vcc, exec, s[38:39]
	v_fmac_f32_e32 v110, v112, v115
	s_cbranch_vccnz .LBB0_915
	s_waitcnt lgkmcnt(0)
	v_add_f32_e32 v111, v111, v119
	v_mul_f32_e32 v111, 0xbfb8aa3b, v111
	v_exp_f32_e32 v111, v111
	v_and_b32_e32 v112, 0xffff0000, v155
	v_sub_f32_e32 v112, v112, v110
	v_add_f32_e32 v111, 1.0, v111
	v_rcp_f32_e32 v111, v111
	s_nop 0
	v_fmac_f32_e32 v110, v112, v111
; DI unsigned pk2(float a, float b) { f32x2 v = {a, b}; bf16x2_t r = __builtin_convertvector(v, bf16x2_t); return __builtin_bit_cast(unsigned, r); }
; DI float sigmoidf_(float x) { return 1.f / (1.f + __expf(-x)); }
; DI void phase_rwkvprep(const Args& a, int l, LAS unsigned char* lds, int tid, int gw, int NGW, int lane) {
;     ...
;             for (int j = 0; j < 4; ++j) {
;                 const float rc = (j & 1) ? bfhi(j < 2 ? zr_.x : zr_.y) : bflo(j < 2 ? zr_.x : zr_.y), rp = (j & 1) ? bfhi(j < 2 ? pr_.x : pr_.y) : bflo(j < 2 ? pr_.x : pr_.y);
;                 const float kc = (j & 1) ? bfhi(j < 2 ? zk_.x : zk_.y) : bflo(j < 2 ? zk_.x : zk_.y), kp = (j & 1) ? bfhi(j < 2 ? pk_.x : pk_.y) : bflo(j < 2 ? pk_.x : pk_.y);
;                 const float vc = (j & 1) ? bfhi(j < 2 ? zv_.x : zv_.y) : bflo(j < 2 ? zv_.x : zv_.y), vp = (j & 1) ? bfhi(j < 2 ? pv_.x : pv_.y) : bflo(j < 2 ? pv_.x : pv_.y);
;                 const float vfj = (j & 1) ? bfhi(j < 2 ? vfw.x : vfw.y) : bflo(j < 2 ? vfw.x : vfw.y);
;                 const float r = rc + (rp - rc) * mr[j]; float k = kc + (kp - kc) * mk[j]; float v = vc + (vp - vc) * mv[j];
;                 const float xw = -(w0v[j] + aw[j]);
;                 const float sp = fmaxf(xw, 0.f) + __logf(1.f + __expf(-fabsf(xw)));
;                 const float wlog = -sp - 0.5f; const float dec = __expf(-__expf(wlog));
;                 const float aval = sigmoidf_(a0v[j] + aa[j]);
;                 if (l > 0) v = v + (vfj - v) * sigmoidf_(v0v[j] + avr[j]);
;                 const float kk = k * kkw[j]; ss += kk * kk;
;                 k = k * (1.f + (aval - 1.f) * kaw[j]);
;                 rks += r * k * rkw[j];
;                 kkv[ct][j] = kk; av[ct][j] = aval;
;                 ro[j] = r; wo[j] = dec; ko[j] = k; vo[j] = v; go[j] = ag[j]; }
;             const size_t o = (size_t)row * C + c0;
;             *(u32x2*)(Rr + o) = (u32x2){pk2(ro[0], ro[1]), pk2(ro[2], ro[3])}; *(f32x4*)(Ww + o) = wo; *(u32x2*)(Kk + o) = (u32x2){pk2(ko[0], ko[1]), pk2(ko[2], ko[3])};
;             const u32x2 vpk = {pk2(vo[0], vo[1]), pk2(vo[2], vo[3])}; *(u32x2*)(Vv + o) = vpk; *(u32x2*)(Gg + o) = (u32x2){pk2(go[0], go[1]), pk2(go[2], go[3])};
;             if (l == 0) *(u32x2*)(VF + o) = vpk; }
.LBB0_915:
	s_waitcnt lgkmcnt(6)
	v_add_f32_e32 v74, v74, v78
	s_mov_b32 s2, 0xbfb8aa3b
	v_max_f32_e64 v78, -v74, 0
	v_mul_f32_e64 v74, |v74|, s2
	v_exp_f32_e32 v74, v74
	v_lshlrev_b32_e32 v210, 16, v160
	v_lshlrev_b32_e32 v111, 16, v174
	v_lshlrev_b32_e32 v211, 16, v156
	v_lshlrev_b32_e32 v112, 16, v176
	v_sub_f32_e32 v111, v111, v210
	v_add_f32_e32 v74, 1.0, v74
	s_waitcnt lgkmcnt(1)
	v_fmac_f32_e32 v210, v111, v104
	v_sub_f32_e32 v104, v112, v211
	v_cmp_gt_f32_e32 vcc, s14, v74
	v_fmac_f32_e32 v211, v104, v82
	v_add_f32_e32 v66, v66, v70
	v_cndmask_b32_e64 v82, 0, 32, vcc
	v_ldexp_f32 v74, v74, v82
	v_log_f32_e32 v74, v74
	v_mul_f32_e32 v66, 0xbfb8aa3b, v66
	s_mov_b32 s3, 0x3f317217
	v_exp_f32_e32 v66, v66
	v_mul_f32_e32 v82, 0x3f317217, v74
	v_fma_f32 v82, v74, s3, -v82
	v_fmac_f32_e32 v82, 0x3377d1cf, v74
	v_fmac_f32_e32 v82, 0x3f317217, v74
	v_cmp_lt_f32_e64 s[50:51], |v74|, s4
	v_add_f32_e32 v66, 1.0, v66
	s_nop 0
	v_cndmask_b32_e64 v74, v74, v82, s[50:51]
	v_cndmask_b32_e32 v82, 0, v224, vcc
	v_sub_f32_e32 v74, v74, v82
	v_add_f32_e32 v74, v78, v74
	v_and_b32_e32 v212, 0xffff0000, v160
	v_and_b32_e32 v214, 0xffff0000, v156
	v_lshlrev_b32_e32 v215, 16, v161
	v_rcp_f32_e32 v154, v66
	s_nop 0
	v_add_f32_e32 v66, -1.0, v154
	v_fma_f32 v62, v62, v66, 1.0
	v_mul_f32_e32 v213, v211, v62
	v_and_b32_e32 v62, 0xffff0000, v174
	v_and_b32_e32 v66, 0xffff0000, v176
	v_sub_f32_e32 v62, v62, v212
	v_fmac_f32_e32 v212, v62, v105
	v_sub_f32_e32 v62, v66, v214
	v_fmac_f32_e32 v214, v62, v83
	v_add_f32_e32 v62, v75, v79
	v_max_f32_e64 v66, -v62, 0
	v_mul_f32_e64 v62, |v62|, s2
	v_exp_f32_e32 v62, v62
	v_lshlrev_b32_e32 v217, 16, v157
	v_and_b32_e32 v233, 0xffff0000, v161
	v_and_b32_e32 v235, 0xffff0000, v157
	v_add_f32_e32 v62, 1.0, v62
	v_cmp_gt_f32_e32 vcc, s14, v62
	v_sub_f32_e32 v74, -0.5, v74
	v_mul_f32_e32 v74, 0x3fb8aa3b, v74
	v_cndmask_b32_e64 v70, 0, 32, vcc
	v_ldexp_f32 v62, v62, v70
	v_log_f32_e32 v62, v62
	v_exp_f32_e32 v74, v74
	v_cvt_pk_bf16_f32 v58, v58, v59
	v_cvt_pk_bf16_f32 v59, v60, v61
	v_mul_f32_e32 v70, 0x3f317217, v62
	v_fma_f32 v70, v62, s3, -v70
	v_fmac_f32_e32 v70, 0x3377d1cf, v62
	v_fmac_f32_e32 v70, 0x3f317217, v62
	v_cmp_lt_f32_e64 s[50:51], |v62|, s4
	v_mul_f32_e32 v74, 0xbfb8aa3b, v74
	v_exp_f32_e32 v74, v74
	v_cndmask_b32_e64 v62, v62, v70, s[50:51]
	v_cndmask_b32_e32 v70, 0, v224, vcc
	v_sub_f32_e32 v62, v62, v70
	v_add_f32_e32 v62, v66, v62
	v_sub_f32_e32 v62, -0.5, v62
	v_mul_f32_e32 v62, 0x3fb8aa3b, v62
	v_exp_f32_e32 v62, v62
	s_nop 0
	v_mul_f32_e32 v62, 0xbfb8aa3b, v62
	v_exp_f32_e32 v75, v62
	v_add_f32_e32 v62, v67, v71
	v_mul_f32_e32 v62, 0xbfb8aa3b, v62
	v_exp_f32_e32 v62, v62
	s_nop 0
	v_add_f32_e32 v62, 1.0, v62
	v_rcp_f32_e32 v155, v62
	s_nop 0
	v_add_f32_e32 v62, -1.0, v155
	v_fma_f32 v62, v63, v62, 1.0
	v_mul_f32_e32 v216, v214, v62
	v_lshlrev_b32_e32 v62, 16, v175
	v_lshlrev_b32_e32 v63, 16, v177
	v_sub_f32_e32 v62, v62, v215
	v_fmac_f32_e32 v215, v62, v106
	v_sub_f32_e32 v62, v63, v217
	v_fmac_f32_e32 v217, v62, v84
	v_add_f32_e32 v62, v76, v80
	v_max_f32_e64 v63, -v62, 0
	v_mul_f32_e64 v62, |v62|, s2
	v_exp_f32_e32 v62, v62
	s_nop 0
	v_add_f32_e32 v62, 1.0, v62
	v_cmp_gt_f32_e32 vcc, s14, v62
	s_nop 1
	v_cndmask_b32_e64 v66, 0, 32, vcc
	v_ldexp_f32 v62, v62, v66
	v_log_f32_e32 v62, v62
	s_nop 0
	v_mul_f32_e32 v66, 0x3f317217, v62
	v_fma_f32 v66, v62, s3, -v66
	v_fmac_f32_e32 v66, 0x3377d1cf, v62
	v_fmac_f32_e32 v66, 0x3f317217, v62
	v_cmp_lt_f32_e64 s[50:51], |v62|, s4
	s_nop 1
	v_cndmask_b32_e64 v62, v62, v66, s[50:51]
	v_cndmask_b32_e32 v66, 0, v224, vcc
	v_sub_f32_e32 v62, v62, v66
	v_add_f32_e32 v62, v63, v62
	v_sub_f32_e32 v62, -0.5, v62
	v_mul_f32_e32 v62, 0x3fb8aa3b, v62
	v_exp_f32_e32 v62, v62
	s_nop 0
	v_mul_f32_e32 v62, 0xbfb8aa3b, v62
	v_exp_f32_e32 v76, v62
	v_add_f32_e32 v62, v68, v72
	v_mul_f32_e32 v62, 0xbfb8aa3b, v62
	v_exp_f32_e32 v62, v62
	s_nop 0
	v_add_f32_e32 v62, 1.0, v62
	v_rcp_f32_e32 v156, v62
	s_nop 0
	v_add_f32_e32 v62, -1.0, v156
	v_fma_f32 v62, v64, v62, 1.0
	v_mul_f32_e32 v234, v217, v62
	v_and_b32_e32 v62, 0xffff0000, v175
	v_and_b32_e32 v63, 0xffff0000, v177
	v_sub_f32_e32 v62, v62, v233
	v_fmac_f32_e32 v233, v62, v107
	v_sub_f32_e32 v62, v63, v235
	v_fmac_f32_e32 v235, v62, v85
	v_add_f32_e32 v62, v77, v81
	v_max_f32_e64 v63, -v62, 0
	v_mul_f32_e64 v62, |v62|, s2
	v_exp_f32_e32 v62, v62
	s_nop 0
	v_add_f32_e32 v62, 1.0, v62
	v_cmp_gt_f32_e32 vcc, s14, v62
	s_nop 1
	v_cndmask_b32_e64 v64, 0, 32, vcc
	v_ldexp_f32 v62, v62, v64
	v_log_f32_e32 v62, v62
	s_nop 0
	v_mul_f32_e32 v64, 0x3f317217, v62
	v_fma_f32 v64, v62, s3, -v64
	v_fmac_f32_e32 v64, 0x3377d1cf, v62
	v_fmac_f32_e32 v64, 0x3f317217, v62
	v_cmp_lt_f32_e64 s[50:51], |v62|, s4
	s_nop 1
	v_cndmask_b32_e64 v62, v62, v64, s[50:51]
	v_cndmask_b32_e32 v64, 0, v224, vcc
	v_sub_f32_e32 v62, v62, v64
	v_add_f32_e32 v62, v63, v62
	v_sub_f32_e32 v62, -0.5, v62
	v_mul_f32_e32 v62, 0x3fb8aa3b, v62
	v_exp_f32_e32 v62, v62
	s_nop 0
	v_mul_f32_e32 v62, 0xbfb8aa3b, v62
	v_exp_f32_e32 v77, v62
	v_add_f32_e32 v62, v69, v73
	v_mul_f32_e32 v62, 0xbfb8aa3b, v62
	v_exp_f32_e32 v62, v62
	s_nop 0
	v_add_f32_e32 v62, 1.0, v62
	v_rcp_f32_e32 v157, v62
	s_nop 0
	v_add_f32_e32 v62, -1.0, v157
	v_fma_f32 v62, v65, v62, 1.0
	v_mul_f32_e32 v236, v235, v62
	v_or3_b32 v62, v197, v152, 16
	v_mov_b32_e32 v63, v153
	v_lshlrev_b64 v[66:67], 1, v[62:63]
	v_cvt_pk_bf16_f32 v64, v210, v212
	v_cvt_pk_bf16_f32 v65, v215, v233
	v_lshl_add_u64 v[68:69], s[58:59], 0, v[66:67]
	global_store_dwordx2 v[68:69], v[64:65], off
	v_lshl_add_u64 v[64:65], v[62:63], 2, s[64:65]
	global_store_dwordx4 v[64:65], v[74:77], off
	v_cvt_pk_bf16_f32 v64, v213, v216
	v_cvt_pk_bf16_f32 v65, v234, v236
	v_lshl_add_u64 v[68:69], s[52:53], 0, v[66:67]
	global_store_dwordx2 v[68:69], v[64:65], off
	v_cvt_pk_bf16_f32 v64, v90, v108
	v_cvt_pk_bf16_f32 v65, v109, v110
	v_lshl_add_u64 v[68:69], s[66:67], 0, v[66:67]
	v_lshl_add_u64 v[60:61], s[70:71], 0, v[66:67]
	s_and_b64 vcc, exec, s[48:49]
	global_store_dwordx2 v[68:69], v[64:65], off
	global_store_dwordx2 v[60:61], v[58:59], off
	s_cbranch_vccnz .LBB0_917
	v_lshl_add_u64 v[58:59], v[62:63], 1, s[54:55]
	global_store_dwordx2 v[58:59], v[64:65], off

; #define LAS __attribute__((address_space(3)))
; DI float sigmoidf_(float x) { return 1.f / (1.f + __expf(-x)); }
; DI void phase_rwkvprep(const Args& a, int l, LAS unsigned char* lds, int tid, int gw, int NGW, int lane) {
;     ...
;             const f32x4 mr = *(const LAS f32x4*)(par + c0), mk = *(const LAS f32x4*)(par + C + c0), mv = *(const LAS f32x4*)(par + 2 * C + c0);
;             const f32x4 w0v = *(const LAS f32x4*)(par + 3 * C + c0), a0v = *(const LAS f32x4*)(par + 4 * C + c0), kkw = *(const LAS f32x4*)(par + 5 * C + c0), kaw = *(const LAS f32x4*)(par + 6 * C + c0), rkw = *(const LAS f32x4*)(par + 7 * C + c0);
;             const f32x4 v0v = *(const LAS f32x4*)(par + 8 * C + c0);
;             f32x4 ro, wo, ko, vo, go;
; #pragma unroll
;             for (int j = 0; j < 4; ++j) {
;                 const float rc = (j & 1) ? bfhi(j < 2 ? zr_.x : zr_.y) : bflo(j < 2 ? zr_.x : zr_.y), rp = (j & 1) ? bfhi(j < 2 ? pr_.x : pr_.y) : bflo(j < 2 ? pr_.x : pr_.y);
;                 const float kc = (j & 1) ? bfhi(j < 2 ? zk_.x : zk_.y) : bflo(j < 2 ? zk_.x : zk_.y), kp = (j & 1) ? bfhi(j < 2 ? pk_.x : pk_.y) : bflo(j < 2 ? pk_.x : pk_.y);
;                 const float vc = (j & 1) ? bfhi(j < 2 ? zv_.x : zv_.y) : bflo(j < 2 ? zv_.x : zv_.y), vp = (j & 1) ? bfhi(j < 2 ? pv_.x : pv_.y) : bflo(j < 2 ? pv_.x : pv_.y);
;                 const float vfj = (j & 1) ? bfhi(j < 2 ? vfw.x : vfw.y) : bflo(j < 2 ? vfw.x : vfw.y);
;                 const float r = rc + (rp - rc) * mr[j]; float k = kc + (kp - kc) * mk[j]; float v = vc + (vp - vc) * mv[j];
;                 const float xw = -(w0v[j] + aw[j]);
;                 const float sp = fmaxf(xw, 0.f) + __logf(1.f + __expf(-fabsf(xw)));
;                 const float wlog = -sp - 0.5f; const float dec = __expf(-__expf(wlog));
;                 const float aval = sigmoidf_(a0v[j] + aa[j]);
;                 if (l > 0) v = v + (vfj - v) * sigmoidf_(v0v[j] + avr[j]);
.LBB0_926:
	s_waitcnt vmcnt(14)
	v_lshlrev_b32_e32 v90, 16, v190
	v_lshlrev_b32_e32 v144, 16, v186
	v_sub_f32_e32 v90, v90, v144
	ds_read_b128 v[108:111], v209 offset:4224
	ds_read_b128 v[120:123], v209 offset:8320
	ds_read_b128 v[104:107], v209 offset:12416
	ds_read_b128 v[96:99], v209 offset:16512
	ds_read_b128 v[50:53], v209 offset:20608
	ds_read_b128 v[86:89], v209 offset:24704
	ds_read_b128 v[46:49], v209 offset:28800
	ds_read_b128 v[112:115], v209 offset:128
	ds_read_b128 v[124:127], v209 offset:32896
	s_and_b64 vcc, exec, s[38:39]
	s_waitcnt lgkmcnt(7)
	v_fmac_f32_e32 v144, v90, v120
	s_cbranch_vccnz .LBB0_928
	s_waitcnt lgkmcnt(0)
	v_add_f32_e32 v90, v116, v124
	v_mul_f32_e32 v90, 0xbfb8aa3b, v90
	v_exp_f32_e32 v90, v90
	v_lshlrev_b32_e32 v116, 16, v184
	v_sub_f32_e32 v116, v116, v144
	v_add_f32_e32 v90, 1.0, v90
	v_rcp_f32_e32 v90, v90
	s_nop 0
	v_fmac_f32_e32 v144, v116, v90
.LBB0_928:
	s_waitcnt lgkmcnt(0)
	v_and_b32_e32 v124, 0xffff0000, v186
	v_and_b32_e32 v90, 0xffff0000, v190
	v_sub_f32_e32 v90, v90, v124
	s_and_b64 vcc, exec, s[38:39]
	v_fmac_f32_e32 v124, v90, v121
	s_cbranch_vccnz .LBB0_930
	v_add_f32_e32 v90, v117, v125
	v_mul_f32_e32 v90, 0xbfb8aa3b, v90
	v_exp_f32_e32 v90, v90
	v_and_b32_e32 v116, 0xffff0000, v184
	v_sub_f32_e32 v116, v116, v124
	v_add_f32_e32 v90, 1.0, v90
	v_rcp_f32_e32 v90, v90
	s_nop 0
	v_fmac_f32_e32 v124, v116, v90
.LBB0_930:
	v_lshlrev_b32_e32 v125, 16, v187
	v_lshlrev_b32_e32 v90, 16, v191
	v_sub_f32_e32 v90, v90, v125
	s_and_b64 vcc, exec, s[38:39]
	v_fmac_f32_e32 v125, v90, v122
	s_cbranch_vccnz .LBB0_932
	v_add_f32_e32 v90, v118, v126
	v_mul_f32_e32 v90, 0xbfb8aa3b, v90
	v_exp_f32_e32 v90, v90
	v_lshlrev_b32_e32 v116, 16, v185
	v_sub_f32_e32 v116, v116, v125
	v_add_f32_e32 v90, 1.0, v90
	v_rcp_f32_e32 v90, v90
	s_nop 0
	v_fmac_f32_e32 v125, v116, v90
.LBB0_932:
	v_and_b32_e32 v126, 0xffff0000, v187
	v_and_b32_e32 v90, 0xffff0000, v191
	v_sub_f32_e32 v90, v90, v126
	s_and_b64 vcc, exec, s[38:39]
	v_fmac_f32_e32 v126, v90, v123
	s_cbranch_vccnz .LBB0_934
	v_add_f32_e32 v90, v119, v127
	v_mul_f32_e32 v90, 0xbfb8aa3b, v90
	v_exp_f32_e32 v90, v90
	v_and_b32_e32 v116, 0xffff0000, v185
	v_sub_f32_e32 v116, v116, v126
	v_add_f32_e32 v90, 1.0, v90
	v_rcp_f32_e32 v90, v90
	s_nop 0
	v_fmac_f32_e32 v126, v116, v90
; DI unsigned pk2(float a, float b) { f32x2 v = {a, b}; bf16x2_t r = __builtin_convertvector(v, bf16x2_t); return __builtin_bit_cast(unsigned, r); }
; DI float sigmoidf_(float x) { return 1.f / (1.f + __expf(-x)); }
; DI void phase_rwkvprep(const Args& a, int l, LAS unsigned char* lds, int tid, int gw, int NGW, int lane) {
;     ...
;             for (int j = 0; j < 4; ++j) {
;                 const float rc = (j & 1) ? bfhi(j < 2 ? zr_.x : zr_.y) : bflo(j < 2 ? zr_.x : zr_.y), rp = (j & 1) ? bfhi(j < 2 ? pr_.x : pr_.y) : bflo(j < 2 ? pr_.x : pr_.y);
;                 const float kc = (j & 1) ? bfhi(j < 2 ? zk_.x : zk_.y) : bflo(j < 2 ? zk_.x : zk_.y), kp = (j & 1) ? bfhi(j < 2 ? pk_.x : pk_.y) : bflo(j < 2 ? pk_.x : pk_.y);
;                 const float vc = (j & 1) ? bfhi(j < 2 ? zv_.x : zv_.y) : bflo(j < 2 ? zv_.x : zv_.y), vp = (j & 1) ? bfhi(j < 2 ? pv_.x : pv_.y) : bflo(j < 2 ? pv_.x : pv_.y);
;                 const float vfj = (j & 1) ? bfhi(j < 2 ? vfw.x : vfw.y) : bflo(j < 2 ? vfw.x : vfw.y);
;                 const float r = rc + (rp - rc) * mr[j]; float k = kc + (kp - kc) * mk[j]; float v = vc + (vp - vc) * mv[j];
;                 const float xw = -(w0v[j] + aw[j]);
;                 const float sp = fmaxf(xw, 0.f) + __logf(1.f + __expf(-fabsf(xw)));
;                 const float wlog = -sp - 0.5f; const float dec = __expf(-__expf(wlog));
;                 const float aval = sigmoidf_(a0v[j] + aa[j]);
;                 if (l > 0) v = v + (vfj - v) * sigmoidf_(v0v[j] + avr[j]);
;                 const float kk = k * kkw[j]; ss += kk * kk;
;                 k = k * (1.f + (aval - 1.f) * kaw[j]);
;                 rks += r * k * rkw[j];
;                 kkv[ct][j] = kk; av[ct][j] = aval;
;                 ro[j] = r; wo[j] = dec; ko[j] = k; vo[j] = v; go[j] = ag[j]; }
;             const size_t o = (size_t)row * C + c0;
;             *(u32x2*)(Rr + o) = (u32x2){pk2(ro[0], ro[1]), pk2(ro[2], ro[3])}; *(f32x4*)(Ww + o) = wo; *(u32x2*)(Kk + o) = (u32x2){pk2(ko[0], ko[1]), pk2(ko[2], ko[3])};
;             const u32x2 vpk = {pk2(vo[0], vo[1]), pk2(vo[2], vo[3])}; *(u32x2*)(Vv + o) = vpk; *(u32x2*)(Gg + o) = (u32x2){pk2(go[0], go[1]), pk2(go[2], go[3])};
;             if (l == 0) *(u32x2*)(VF + o) = vpk; }
.LBB0_934:
	v_add_f32_e32 v100, v100, v104
	s_mov_b32 s2, 0xbfb8aa3b
	v_max_f32_e64 v104, -v100, 0
	v_mul_f32_e64 v100, |v100|, s2
	v_exp_f32_e32 v100, v100
	v_lshlrev_b32_e32 v90, 16, v172
	v_lshlrev_b32_e32 v117, 16, v178
	v_lshlrev_b32_e32 v116, 16, v162
	v_lshlrev_b32_e32 v118, 16, v180
	v_sub_f32_e32 v117, v117, v90
	v_add_f32_e32 v100, 1.0, v100
	v_fmac_f32_e32 v90, v117, v112
	v_sub_f32_e32 v112, v118, v116
	v_cmp_gt_f32_e32 vcc, s14, v100
	v_fmac_f32_e32 v116, v112, v108
	v_add_f32_e32 v92, v92, v96
	v_cndmask_b32_e64 v108, 0, 32, vcc
	v_ldexp_f32 v100, v100, v108
	v_log_f32_e32 v100, v100
	v_mul_f32_e32 v92, 0xbfb8aa3b, v92
	s_mov_b32 s3, 0x3f317217
	v_exp_f32_e32 v92, v92
	v_mul_f32_e32 v108, 0x3f317217, v100
	v_fma_f32 v108, v100, s3, -v108
	v_fmac_f32_e32 v108, 0x3377d1cf, v100
	v_fmac_f32_e32 v108, 0x3f317217, v100
	v_cmp_lt_f32_e64 s[46:47], |v100|, s4
	v_add_f32_e32 v92, 1.0, v92
	s_nop 0
	v_cndmask_b32_e64 v100, v100, v108, s[46:47]
	v_cndmask_b32_e32 v108, 0, v224, vcc
	v_sub_f32_e32 v100, v100, v108
	v_add_f32_e32 v100, v104, v100
	v_and_b32_e32 v118, 0xffff0000, v162
	v_lshlrev_b32_e32 v120, 16, v163
	v_and_b32_e32 v122, 0xffff0000, v163
	v_rcp_f32_e32 v108, v92
	s_nop 0
	v_add_f32_e32 v92, -1.0, v108
	v_fma_f32 v86, v86, v92, 1.0
	v_mul_f32_e32 v117, v116, v86
	v_and_b32_e32 v112, 0xffff0000, v172
	v_and_b32_e32 v86, 0xffff0000, v178
	v_and_b32_e32 v92, 0xffff0000, v180
	v_sub_f32_e32 v86, v86, v112
	v_fmac_f32_e32 v112, v86, v113
	v_sub_f32_e32 v86, v92, v118
	v_fmac_f32_e32 v118, v86, v109
	v_add_f32_e32 v86, v101, v105
	v_max_f32_e64 v92, -v86, 0
	v_mul_f32_e64 v86, |v86|, s2
	v_exp_f32_e32 v86, v86
	v_lshlrev_b32_e32 v113, 16, v173
	v_sub_f32_e32 v100, -0.5, v100
	v_mul_f32_e32 v100, 0x3fb8aa3b, v100
	v_add_f32_e32 v86, 1.0, v86
	v_cmp_gt_f32_e32 vcc, s14, v86
	v_exp_f32_e32 v100, v100
	v_cvt_pk_bf16_f32 v54, v54, v55
	v_cndmask_b32_e64 v96, 0, 32, vcc
	v_ldexp_f32 v86, v86, v96
	v_log_f32_e32 v86, v86
	v_mul_f32_e32 v100, 0xbfb8aa3b, v100
	v_exp_f32_e32 v100, v100
	v_cvt_pk_bf16_f32 v55, v56, v57
	v_mul_f32_e32 v96, 0x3f317217, v86
	v_fma_f32 v96, v86, s3, -v96
	v_fmac_f32_e32 v96, 0x3377d1cf, v86
	v_fmac_f32_e32 v96, 0x3f317217, v86
	v_cmp_lt_f32_e64 s[46:47], |v86|, s4
	s_nop 1
	v_cndmask_b32_e64 v86, v86, v96, s[46:47]
	v_cndmask_b32_e32 v96, 0, v224, vcc
	v_sub_f32_e32 v86, v86, v96
	v_add_f32_e32 v86, v92, v86
	v_sub_f32_e32 v86, -0.5, v86
	v_mul_f32_e32 v86, 0x3fb8aa3b, v86
	v_exp_f32_e32 v86, v86
	s_nop 0
	v_mul_f32_e32 v86, 0xbfb8aa3b, v86
	v_exp_f32_e32 v101, v86
	v_add_f32_e32 v86, v93, v97
	v_mul_f32_e32 v86, 0xbfb8aa3b, v86
	v_exp_f32_e32 v86, v86
	s_nop 0
	v_add_f32_e32 v86, 1.0, v86
	v_rcp_f32_e32 v109, v86
	s_nop 0
	v_add_f32_e32 v86, -1.0, v109
	v_fma_f32 v86, v87, v86, 1.0
	v_mul_f32_e32 v119, v118, v86
	v_lshlrev_b32_e32 v86, 16, v179
	v_lshlrev_b32_e32 v87, 16, v181
	v_sub_f32_e32 v86, v86, v113
	v_fmac_f32_e32 v113, v86, v114
	v_sub_f32_e32 v86, v87, v120
	v_fmac_f32_e32 v120, v86, v110
	v_add_f32_e32 v86, v102, v106
	v_max_f32_e64 v87, -v86, 0
	v_mul_f32_e64 v86, |v86|, s2
	v_exp_f32_e32 v86, v86
	v_and_b32_e32 v114, 0xffff0000, v173
	v_add_f32_e32 v86, 1.0, v86
	v_cmp_gt_f32_e32 vcc, s14, v86
	s_nop 1
	v_cndmask_b32_e64 v92, 0, 32, vcc
	v_ldexp_f32 v86, v86, v92
	v_log_f32_e32 v86, v86
	s_nop 0
	v_mul_f32_e32 v92, 0x3f317217, v86
	v_fma_f32 v92, v86, s3, -v92
	v_fmac_f32_e32 v92, 0x3377d1cf, v86
	v_fmac_f32_e32 v92, 0x3f317217, v86
	v_cmp_lt_f32_e64 s[46:47], |v86|, s4
	s_nop 1
	v_cndmask_b32_e64 v86, v86, v92, s[46:47]
	v_cndmask_b32_e32 v92, 0, v224, vcc
	v_sub_f32_e32 v86, v86, v92
	v_add_f32_e32 v86, v87, v86
	v_sub_f32_e32 v86, -0.5, v86
	v_mul_f32_e32 v86, 0x3fb8aa3b, v86
	v_exp_f32_e32 v86, v86
	s_nop 0
	v_mul_f32_e32 v86, 0xbfb8aa3b, v86
	v_exp_f32_e32 v102, v86
	v_add_f32_e32 v86, v94, v98
	v_mul_f32_e32 v86, 0xbfb8aa3b, v86
	v_exp_f32_e32 v86, v86
	s_nop 0
	v_add_f32_e32 v86, 1.0, v86
	v_rcp_f32_e32 v110, v86
	s_nop 0
	v_add_f32_e32 v86, -1.0, v110
	v_fma_f32 v86, v88, v86, 1.0
	v_mul_f32_e32 v121, v120, v86
	v_and_b32_e32 v86, 0xffff0000, v179
	v_and_b32_e32 v87, 0xffff0000, v181
	v_sub_f32_e32 v86, v86, v114
	v_fmac_f32_e32 v114, v86, v115
	v_sub_f32_e32 v86, v87, v122
	v_fmac_f32_e32 v122, v86, v111
	v_add_f32_e32 v86, v103, v107
	v_max_f32_e64 v87, -v86, 0
	v_mul_f32_e64 v86, |v86|, s2
	v_exp_f32_e32 v86, v86
	s_nop 0
	v_add_f32_e32 v86, 1.0, v86
	v_cmp_gt_f32_e32 vcc, s14, v86
	s_nop 1
	v_cndmask_b32_e64 v88, 0, 32, vcc
	v_ldexp_f32 v86, v86, v88
	v_log_f32_e32 v86, v86
	s_nop 0
	v_mul_f32_e32 v88, 0x3f317217, v86
	v_fma_f32 v88, v86, s3, -v88
	v_fmac_f32_e32 v88, 0x3377d1cf, v86
	v_fmac_f32_e32 v88, 0x3f317217, v86
	v_cmp_lt_f32_e64 s[46:47], |v86|, s4
	s_nop 1
	v_cndmask_b32_e64 v86, v86, v88, s[46:47]
	v_cndmask_b32_e32 v88, 0, v224, vcc
	v_sub_f32_e32 v86, v86, v88
	v_add_f32_e32 v86, v87, v86
	v_sub_f32_e32 v86, -0.5, v86
	v_mul_f32_e32 v86, 0x3fb8aa3b, v86
	v_exp_f32_e32 v86, v86
	s_nop 0
	v_mul_f32_e32 v86, 0xbfb8aa3b, v86
	v_exp_f32_e32 v103, v86
	v_add_f32_e32 v86, v95, v99
	v_mul_f32_e32 v86, 0xbfb8aa3b, v86
	v_exp_f32_e32 v86, v86
	s_nop 0
	v_add_f32_e32 v86, 1.0, v86
	v_rcp_f32_e32 v111, v86
	s_nop 0
	v_add_f32_e32 v86, -1.0, v111
	v_fma_f32 v86, v89, v86, 1.0
	v_mul_f32_e32 v115, v122, v86
	v_or3_b32 v86, v197, v152, 32
	v_mov_b32_e32 v87, v153
	v_lshlrev_b64 v[92:93], 1, v[86:87]
	v_cvt_pk_bf16_f32 v88, v90, v112
	v_cvt_pk_bf16_f32 v89, v113, v114
	v_lshl_add_u64 v[94:95], s[58:59], 0, v[92:93]
	global_store_dwordx2 v[94:95], v[88:89], off
	v_lshl_add_u64 v[88:89], v[86:87], 2, s[64:65]
	global_store_dwordx4 v[88:89], v[100:103], off
	v_cvt_pk_bf16_f32 v88, v117, v119
	v_cvt_pk_bf16_f32 v89, v121, v115
	v_lshl_add_u64 v[94:95], s[52:53], 0, v[92:93]
	global_store_dwordx2 v[94:95], v[88:89], off
	v_cvt_pk_bf16_f32 v88, v144, v124
	v_cvt_pk_bf16_f32 v89, v125, v126
	v_lshl_add_u64 v[94:95], s[66:67], 0, v[92:93]
	v_lshl_add_u64 v[56:57], s[70:71], 0, v[92:93]
	s_and_b64 vcc, exec, s[48:49]
	global_store_dwordx2 v[94:95], v[88:89], off
	global_store_dwordx2 v[56:57], v[54:55], off
	s_cbranch_vccnz .LBB0_936
	v_lshl_add_u64 v[54:55], v[86:87], 1, s[54:55]
	global_store_dwordx2 v[54:55], v[88:89], off

; #define LAS __attribute__((address_space(3)))
; DI float sigmoidf_(float x) { return 1.f / (1.f + __expf(-x)); }
; DI void phase_rwkvprep(const Args& a, int l, LAS unsigned char* lds, int tid, int gw, int NGW, int lane) {
;     ...
;             const f32x4 mr = *(const LAS f32x4*)(par + c0), mk = *(const LAS f32x4*)(par + C + c0), mv = *(const LAS f32x4*)(par + 2 * C + c0);
;             const f32x4 w0v = *(const LAS f32x4*)(par + 3 * C + c0), a0v = *(const LAS f32x4*)(par + 4 * C + c0), kkw = *(const LAS f32x4*)(par + 5 * C + c0), kaw = *(const LAS f32x4*)(par + 6 * C + c0), rkw = *(const LAS f32x4*)(par + 7 * C + c0);
;             const f32x4 v0v = *(const LAS f32x4*)(par + 8 * C + c0);
;             f32x4 ro, wo, ko, vo, go;
; #pragma unroll
;             for (int j = 0; j < 4; ++j) {
;                 const float rc = (j & 1) ? bfhi(j < 2 ? zr_.x : zr_.y) : bflo(j < 2 ? zr_.x : zr_.y), rp = (j & 1) ? bfhi(j < 2 ? pr_.x : pr_.y) : bflo(j < 2 ? pr_.x : pr_.y);
;                 const float kc = (j & 1) ? bfhi(j < 2 ? zk_.x : zk_.y) : bflo(j < 2 ? zk_.x : zk_.y), kp = (j & 1) ? bfhi(j < 2 ? pk_.x : pk_.y) : bflo(j < 2 ? pk_.x : pk_.y);
;                 const float vc = (j & 1) ? bfhi(j < 2 ? zv_.x : zv_.y) : bflo(j < 2 ? zv_.x : zv_.y), vp = (j & 1) ? bfhi(j < 2 ? pv_.x : pv_.y) : bflo(j < 2 ? pv_.x : pv_.y);
;                 const float vfj = (j & 1) ? bfhi(j < 2 ? vfw.x : vfw.y) : bflo(j < 2 ? vfw.x : vfw.y);
;                 const float r = rc + (rp - rc) * mr[j]; float k = kc + (kp - kc) * mk[j]; float v = vc + (vp - vc) * mv[j];
;                 const float xw = -(w0v[j] + aw[j]);
;                 const float sp = fmaxf(xw, 0.f) + __logf(1.f + __expf(-fabsf(xw)));
;                 const float wlog = -sp - 0.5f; const float dec = __expf(-__expf(wlog));
;                 const float aval = sigmoidf_(a0v[j] + aa[j]);
;                 if (l > 0) v = v + (vfj - v) * sigmoidf_(v0v[j] + avr[j]);
;                 const float kk = k * kkw[j]; ss += kk * kk;
;                 k = k * (1.f + (aval - 1.f) * kaw[j]);
;                 rks += r * k * rkw[j];
;                 kkv[ct][j] = kk; av[ct][j] = aval;
;                 ro[j] = r; wo[j] = dec; ko[j] = k; vo[j] = v; go[j] = ag[j]; }
.LBB0_938:
	s_waitcnt vmcnt(5)
	v_lshlrev_b32_e32 v124, 16, v192
	v_lshlrev_b32_e32 v123, 16, v188
	v_sub_f32_e32 v124, v124, v123
	ds_read_b128 v[86:89], v209 offset:4288
	ds_read_b128 v[100:103], v209 offset:8384
	ds_read_b128 v[82:85], v209 offset:12480
	ds_read_b128 v[74:77], v209 offset:16576
	ds_read_b128 v[58:61], v209 offset:20672
	ds_read_b128 v[62:65], v209 offset:24768
	ds_read_b128 v[54:57], v209 offset:28864
	ds_read_b128 v[92:95], v209 offset:192
	ds_read_b128 v[104:107], v209 offset:32960
	s_and_b64 vcc, exec, s[38:39]
	s_waitcnt lgkmcnt(7)
	v_fmac_f32_e32 v123, v124, v100
	s_cbranch_vccnz .LBB0_940
	s_waitcnt lgkmcnt(0)
	v_add_f32_e32 v96, v96, v104
	v_mul_f32_e32 v96, 0xbfb8aa3b, v96
	v_exp_f32_e32 v96, v96
	v_lshlrev_b32_e32 v100, 16, v182
	v_sub_f32_e32 v100, v100, v123
	v_add_f32_e32 v96, 1.0, v96
	v_rcp_f32_e32 v96, v96
	s_nop 0
	v_fmac_f32_e32 v123, v100, v96
.LBB0_940:
	v_and_b32_e32 v100, 0xffff0000, v188
	v_and_b32_e32 v96, 0xffff0000, v192
	v_sub_f32_e32 v96, v96, v100
	s_and_b64 vcc, exec, s[38:39]
	v_fmac_f32_e32 v100, v96, v101
	s_cbranch_vccnz .LBB0_942
	s_waitcnt lgkmcnt(0)
	v_add_f32_e32 v96, v97, v105
	v_mul_f32_e32 v96, 0xbfb8aa3b, v96
	v_exp_f32_e32 v96, v96
	v_and_b32_e32 v97, 0xffff0000, v182
	v_sub_f32_e32 v97, v97, v100
	v_add_f32_e32 v96, 1.0, v96
	v_rcp_f32_e32 v96, v96
	s_nop 0
	v_fmac_f32_e32 v100, v97, v96
.LBB0_942:
	v_lshlrev_b32_e32 v101, 16, v189
	v_lshlrev_b32_e32 v96, 16, v193
	v_sub_f32_e32 v96, v96, v101
	s_and_b64 vcc, exec, s[38:39]
	v_fmac_f32_e32 v101, v96, v102
	s_cbranch_vccnz .LBB0_944
	s_waitcnt lgkmcnt(0)
	v_add_f32_e32 v96, v98, v106
	v_mul_f32_e32 v96, 0xbfb8aa3b, v96
	v_exp_f32_e32 v96, v96
	v_lshlrev_b32_e32 v97, 16, v183
	v_sub_f32_e32 v97, v97, v101
	v_add_f32_e32 v96, 1.0, v96
	v_rcp_f32_e32 v96, v96
	s_nop 0
	v_fmac_f32_e32 v101, v97, v96
.LBB0_944:
	v_and_b32_e32 v98, 0xffff0000, v189
	v_and_b32_e32 v96, 0xffff0000, v193
	v_sub_f32_e32 v96, v96, v98
	s_and_b64 vcc, exec, s[38:39]
	v_fmac_f32_e32 v98, v96, v103
	s_cbranch_vccnz .LBB0_946
	s_waitcnt lgkmcnt(0)
	v_add_f32_e32 v96, v99, v107
	v_mul_f32_e32 v96, 0xbfb8aa3b, v96
	v_exp_f32_e32 v96, v96
	v_and_b32_e32 v97, 0xffff0000, v183
	v_sub_f32_e32 v97, v97, v98
	v_add_f32_e32 v96, 1.0, v96
	v_rcp_f32_e32 v96, v96
	s_nop 0
	v_fmac_f32_e32 v98, v97, v96
.LBB0_946:
	s_waitcnt lgkmcnt(6)
	v_add_f32_e32 v78, v78, v82
	v_max_f32_e64 v82, -v78, 0
	v_mul_f32_e64 v78, |v78|, s2
	v_exp_f32_e32 v78, v78
	v_lshlrev_b32_e32 v96, 16, v160
	v_lshlrev_b32_e32 v99, 16, v174
	v_lshlrev_b32_e32 v97, 16, v142
	v_lshlrev_b32_e32 v102, 16, v176
	v_sub_f32_e32 v99, v99, v96
	v_add_f32_e32 v78, 1.0, v78
	s_waitcnt lgkmcnt(1)
	v_fmac_f32_e32 v96, v99, v92
	v_sub_f32_e32 v92, v102, v97
	v_cmp_gt_f32_e32 vcc, s14, v78
	v_fmac_f32_e32 v97, v92, v86
	v_add_f32_e32 v70, v70, v74
	v_cndmask_b32_e64 v86, 0, 32, vcc
	v_ldexp_f32 v78, v78, v86
	v_log_f32_e32 v78, v78
	v_mul_f32_e32 v70, 0xbfb8aa3b, v70
	v_exp_f32_e32 v70, v70
	v_or3_b32 v152, v197, v152, 48
	v_mul_f32_e32 v86, 0x3f317217, v78
	v_fma_f32 v86, v78, s3, -v86
	v_fmac_f32_e32 v86, 0x3377d1cf, v78
	v_fmac_f32_e32 v86, 0x3f317217, v78
	v_cmp_lt_f32_e64 s[46:47], |v78|, s4
	v_add_f32_e32 v70, 1.0, v70
	s_nop 0
	v_cndmask_b32_e64 v78, v78, v86, s[46:47]
	v_cndmask_b32_e32 v86, 0, v224, vcc
	v_sub_f32_e32 v78, v78, v86
	v_add_f32_e32 v78, v82, v78
	v_sub_f32_e32 v78, -0.5, v78
	v_mul_f32_e32 v78, 0x3fb8aa3b, v78
	v_exp_f32_e32 v78, v78
	v_rcp_f32_e32 v70, v70
	s_nop 0
	v_add_f32_e32 v74, -1.0, v70
	v_fma_f32 v62, v62, v74, 1.0
	v_mul_f32_e32 v82, v97, v62
	v_and_b32_e32 v74, 0xffff0000, v160
	v_and_b32_e32 v62, 0xffff0000, v174
	v_and_b32_e32 v86, 0xffff0000, v142
	v_and_b32_e32 v92, 0xffff0000, v176
	v_sub_f32_e32 v62, v62, v74
	v_fmac_f32_e32 v74, v62, v93
	v_sub_f32_e32 v62, v92, v86
	v_fmac_f32_e32 v86, v62, v87
	v_add_f32_e32 v62, v79, v83
	v_max_f32_e64 v79, -v62, 0
	v_mul_f32_e64 v62, |v62|, s2
	v_exp_f32_e32 v62, v62
	v_mul_f32_e32 v78, 0xbfb8aa3b, v78
	v_exp_f32_e32 v78, v78
	v_cvt_pk_bf16_f32 v66, v66, v67
	v_add_f32_e32 v62, 1.0, v62
	v_cmp_gt_f32_e32 vcc, s14, v62
	v_cvt_pk_bf16_f32 v67, v68, v69
	s_nop 0
	v_cndmask_b32_e64 v83, 0, 32, vcc
	v_ldexp_f32 v62, v62, v83
	v_log_f32_e32 v62, v62
	s_nop 0
	v_mul_f32_e32 v83, 0x3f317217, v62
	v_fma_f32 v83, v62, s3, -v83
	v_fmac_f32_e32 v83, 0x3377d1cf, v62
	v_fmac_f32_e32 v83, 0x3f317217, v62
	v_cmp_lt_f32_e64 s[46:47], |v62|, s4
	s_nop 1
	v_cndmask_b32_e64 v62, v62, v83, s[46:47]
	v_cndmask_b32_e32 v83, 0, v224, vcc
	v_sub_f32_e32 v62, v62, v83
	v_add_f32_e32 v62, v79, v62
	v_sub_f32_e32 v62, -0.5, v62
	v_mul_f32_e32 v62, 0x3fb8aa3b, v62
	v_exp_f32_e32 v62, v62
	s_nop 0
	v_mul_f32_e32 v62, 0xbfb8aa3b, v62
	v_exp_f32_e32 v79, v62
	v_add_f32_e32 v62, v71, v75
	v_mul_f32_e32 v62, 0xbfb8aa3b, v62
	v_exp_f32_e32 v62, v62
	s_nop 0
	v_add_f32_e32 v62, 1.0, v62
	v_rcp_f32_e32 v71, v62
	s_nop 0
	v_add_f32_e32 v62, -1.0, v71
	v_fma_f32 v62, v63, v62, 1.0
	v_mul_f32_e32 v83, v86, v62
	v_lshlrev_b32_e32 v75, 16, v161
	v_lshlrev_b32_e32 v62, 16, v175
	v_lshlrev_b32_e32 v87, 16, v143
	v_lshlrev_b32_e32 v63, 16, v177
	v_sub_f32_e32 v62, v62, v75
	v_fmac_f32_e32 v75, v62, v94
	v_sub_f32_e32 v62, v63, v87
	v_fmac_f32_e32 v87, v62, v88
	v_add_f32_e32 v62, v80, v84
	v_max_f32_e64 v63, -v62, 0
	v_mul_f32_e64 v62, |v62|, s2
	v_exp_f32_e32 v62, v62
	s_nop 0
	v_add_f32_e32 v62, 1.0, v62
	v_cmp_gt_f32_e32 vcc, s14, v62
	s_nop 1
	v_cndmask_b32_e64 v80, 0, 32, vcc
	v_ldexp_f32 v62, v62, v80
	v_log_f32_e32 v62, v62
	s_nop 0
	v_mul_f32_e32 v80, 0x3f317217, v62
	v_fma_f32 v80, v62, s3, -v80
	v_fmac_f32_e32 v80, 0x3377d1cf, v62
	v_fmac_f32_e32 v80, 0x3f317217, v62
; DI unsigned pk2(float a, float b) { f32x2 v = {a, b}; bf16x2_t r = __builtin_convertvector(v, bf16x2_t); return __builtin_bit_cast(unsigned, r); }
; DI float sigmoidf_(float x) { return 1.f / (1.f + __expf(-x)); }
; DI void phase_rwkvprep(const Args& a, int l, LAS unsigned char* lds, int tid, int gw, int NGW, int lane) {
;     ...
;                 const float r = rc + (rp - rc) * mr[j]; float k = kc + (kp - kc) * mk[j]; float v = vc + (vp - vc) * mv[j];
;                 const float xw = -(w0v[j] + aw[j]);
;                 const float sp = fmaxf(xw, 0.f) + __logf(1.f + __expf(-fabsf(xw)));
;                 const float wlog = -sp - 0.5f; const float dec = __expf(-__expf(wlog));
;                 const float aval = sigmoidf_(a0v[j] + aa[j]);
;                 if (l > 0) v = v + (vfj - v) * sigmoidf_(v0v[j] + avr[j]);
;                 const float kk = k * kkw[j]; ss += kk * kk;
;                 k = k * (1.f + (aval - 1.f) * kaw[j]);
;                 rks += r * k * rkw[j];
;                 kkv[ct][j] = kk; av[ct][j] = aval;
;                 ro[j] = r; wo[j] = dec; ko[j] = k; vo[j] = v; go[j] = ag[j]; }
;             const size_t o = (size_t)row * C + c0;
;             *(u32x2*)(Rr + o) = (u32x2){pk2(ro[0], ro[1]), pk2(ro[2], ro[3])}; *(f32x4*)(Ww + o) = wo; *(u32x2*)(Kk + o) = (u32x2){pk2(ko[0], ko[1]), pk2(ko[2], ko[3])};
;             const u32x2 vpk = {pk2(vo[0], vo[1]), pk2(vo[2], vo[3])}; *(u32x2*)(Vv + o) = vpk; *(u32x2*)(Gg + o) = (u32x2){pk2(go[0], go[1]), pk2(go[2], go[3])};
;             if (l == 0) *(u32x2*)(VF + o) = vpk; }
	v_cmp_lt_f32_e64 s[46:47], |v62|, s4
	s_nop 1
	v_cndmask_b32_e64 v62, v62, v80, s[46:47]
	v_cndmask_b32_e32 v80, 0, v224, vcc
	v_sub_f32_e32 v62, v62, v80
	v_add_f32_e32 v62, v63, v62
	v_sub_f32_e32 v62, -0.5, v62
	v_mul_f32_e32 v62, 0x3fb8aa3b, v62
	v_exp_f32_e32 v62, v62
	s_nop 0
	v_mul_f32_e32 v62, 0xbfb8aa3b, v62
	v_exp_f32_e32 v80, v62
	v_add_f32_e32 v62, v72, v76
	v_mul_f32_e32 v62, 0xbfb8aa3b, v62
	v_exp_f32_e32 v62, v62
	s_nop 0
	v_add_f32_e32 v62, 1.0, v62
	v_rcp_f32_e32 v62, v62
	s_nop 0
	v_add_f32_e32 v63, -1.0, v62
	v_fma_f32 v63, v64, v63, 1.0
	v_mul_f32_e32 v76, v87, v63
	v_and_b32_e32 v72, 0xffff0000, v161
	v_and_b32_e32 v63, 0xffff0000, v175
	v_and_b32_e32 v84, 0xffff0000, v143
	v_and_b32_e32 v64, 0xffff0000, v177
	v_sub_f32_e32 v63, v63, v72
	v_fmac_f32_e32 v72, v63, v95
	v_sub_f32_e32 v63, v64, v84
	v_fmac_f32_e32 v84, v63, v89
	v_add_f32_e32 v63, v81, v85
	v_max_f32_e64 v64, -v63, 0
	v_mul_f32_e64 v63, |v63|, s2
	v_exp_f32_e32 v63, v63
	s_nop 0
	v_add_f32_e32 v63, 1.0, v63
	v_cmp_gt_f32_e32 vcc, s14, v63
	s_nop 1
	v_cndmask_b32_e64 v81, 0, 32, vcc
	v_ldexp_f32 v63, v63, v81
	v_log_f32_e32 v63, v63
	s_nop 0
	v_mul_f32_e32 v81, 0x3f317217, v63
	v_fma_f32 v81, v63, s3, -v81
	v_fmac_f32_e32 v81, 0x3377d1cf, v63
	v_fmac_f32_e32 v81, 0x3f317217, v63
	v_cmp_lt_f32_e64 s[46:47], |v63|, s4
	s_nop 1
	v_cndmask_b32_e64 v63, v63, v81, s[46:47]
	v_cndmask_b32_e32 v81, 0, v224, vcc
	v_sub_f32_e32 v63, v63, v81
	v_add_f32_e32 v63, v64, v63
	v_sub_f32_e32 v63, -0.5, v63
	v_mul_f32_e32 v63, 0x3fb8aa3b, v63
	v_exp_f32_e32 v63, v63
	s_nop 0
	v_mul_f32_e32 v63, 0xbfb8aa3b, v63
	v_exp_f32_e32 v81, v63
	v_add_f32_e32 v63, v73, v77
	v_mul_f32_e32 v63, 0xbfb8aa3b, v63
	v_exp_f32_e32 v63, v63
	s_nop 0
	v_add_f32_e32 v63, 1.0, v63
	v_rcp_f32_e32 v63, v63
	s_nop 0
	v_add_f32_e32 v64, -1.0, v63
	v_fma_f32 v64, v65, v64, 1.0
	v_lshlrev_b64 v[88:89], 1, v[152:153]
	v_mul_f32_e32 v73, v84, v64
	v_cvt_pk_bf16_f32 v64, v96, v74
	v_cvt_pk_bf16_f32 v65, v75, v72
	v_lshl_add_u64 v[92:93], s[58:59], 0, v[88:89]
	global_store_dwordx2 v[92:93], v[64:65], off
	v_lshl_add_u64 v[64:65], v[152:153], 2, s[64:65]
	global_store_dwordx4 v[64:65], v[78:81], off
	v_cvt_pk_bf16_f32 v64, v82, v83
	v_cvt_pk_bf16_f32 v65, v76, v73
	v_lshl_add_u64 v[78:79], s[52:53], 0, v[88:89]
	global_store_dwordx2 v[78:79], v[64:65], off
	v_cvt_pk_bf16_f32 v64, v123, v100
	v_cvt_pk_bf16_f32 v65, v101, v98
	v_lshl_add_u64 v[78:79], s[66:67], 0, v[88:89]
	v_lshl_add_u64 v[68:69], s[70:71], 0, v[88:89]
	s_and_b64 vcc, exec, s[48:49]
	global_store_dwordx2 v[78:79], v[64:65], off
	global_store_dwordx2 v[68:69], v[66:67], off
	s_cbranch_vccnz .LBB0_948
	v_lshl_add_u64 v[66:67], v[152:153], 1, s[54:55]
	global_store_dwordx2 v[66:67], v[64:65], off
; DI unsigned pk2(float a, float b) { f32x2 v = {a, b}; bf16x2_t r = __builtin_convertvector(v, bf16x2_t); return __builtin_bit_cast(unsigned, r); }
; DI void phase_rwkvprep(const Args& a, int l, LAS unsigned char* lds, int tid, int gw, int NGW, int lane) {
;     ...
;         ss += __shfl_xor(ss, 16); ss += __shfl_xor(ss, 32); rks += __shfl_xor(rks, 16); rks += __shfl_xor(rks, 32);
;         const float inv = 1.f / fmaxf(sqrtf(ss), 1e-12f);
; #pragma unroll
;         for (int ct = 0; ct < 4; ++ct) { const size_t o = (size_t)row * C + hd * 64 + ct * 16 + 4 * q;
;             float kn[4], bo[4];
; #pragma unroll
;             for (int j = 0; j < 4; ++j) { kn[j] = kkv[ct][j] * inv; bo[j] = kn[j] * av[ct][j]; }
;             *(u32x2*)(KKn + o) = (u32x2){pk2(kn[0], kn[1]), pk2(kn[2], kn[3])}; *(u32x2*)(Bb + o) = (u32x2){pk2(bo[0], bo[1]), pk2(bo[2], bo[3])}; }
;         if (q == 0) RK[(size_t)row * NH + hd] = rks;
.LBB0_948:
	v_mul_f32_e32 v64, v139, v200
	v_mul_f32_e32 v35, v201, v35
	v_mul_f32_e32 v34, v198, v34
	v_fma_f32 v30, v30, v64, 0
	v_mul_f32_e32 v64, v35, v35
	v_fmac_f32_e32 v64, v34, v34
	v_mul_f32_e32 v65, v199, v203
	v_mul_f32_e32 v36, v204, v36
	v_fmac_f32_e32 v30, v31, v65
	v_fmac_f32_e32 v64, v36, v36
	v_mul_f32_e32 v31, v202, v206
	v_mul_f32_e32 v37, v207, v37
	v_fmac_f32_e32 v30, v32, v31
	v_fmac_f32_e32 v64, v37, v37
	v_mul_f32_e32 v31, v205, v208
	v_mul_f32_e32 v32, v211, v42
	v_fmac_f32_e32 v30, v33, v31
	v_fmac_f32_e32 v64, v32, v32
	v_mul_f32_e32 v31, v210, v213
	v_mul_f32_e32 v33, v214, v43
	v_fmac_f32_e32 v30, v38, v31
	v_fmac_f32_e32 v64, v33, v33
	v_mul_f32_e32 v31, v212, v216
	v_mul_f32_e32 v38, v217, v44
	v_fmac_f32_e32 v30, v39, v31
	v_fmac_f32_e32 v64, v38, v38
	v_mul_f32_e32 v31, v215, v234
	v_mul_f32_e32 v39, v235, v45
	v_fmac_f32_e32 v30, v40, v31
	v_fmac_f32_e32 v64, v39, v39
	v_mul_f32_e32 v31, v233, v236
	v_mul_f32_e32 v40, v116, v50
	v_fmac_f32_e32 v30, v41, v31
	v_fmac_f32_e32 v64, v40, v40
	v_mul_f32_e32 v31, v90, v117
	v_mul_f32_e32 v41, v118, v51
	v_fmac_f32_e32 v30, v46, v31
	v_fmac_f32_e32 v64, v41, v41
	v_mul_f32_e32 v31, v112, v119
	v_mul_f32_e32 v42, v120, v52
	v_fmac_f32_e32 v30, v47, v31
	v_fmac_f32_e32 v64, v42, v42
	v_mul_f32_e32 v31, v113, v121
	v_mul_f32_e32 v43, v122, v53
	v_fmac_f32_e32 v30, v48, v31
	v_fmac_f32_e32 v64, v43, v43
	v_mul_f32_e32 v44, v97, v58
	v_and_b32_e32 v48, 64, v218
	v_fmac_f32_e32 v64, v44, v44
	v_mul_f32_e32 v45, v86, v59
	v_xor_b32_e32 v31, 16, v218
	v_add_u32_e32 v48, 64, v48
	v_fmac_f32_e32 v64, v45, v45
	v_mul_f32_e32 v46, v87, v60
	v_cmp_lt_i32_e32 vcc, v31, v48
	v_fmac_f32_e32 v64, v46, v46
	v_mul_f32_e32 v47, v84, v61
	v_cndmask_b32_e32 v31, v218, v31, vcc
	v_fmac_f32_e32 v64, v47, v47
	v_lshlrev_b32_e32 v31, 2, v31
	ds_bpermute_b32 v50, v31, v64
	v_mul_f32_e32 v51, v114, v115
	v_fmac_f32_e32 v30, v49, v51
	v_mul_f32_e32 v49, v96, v82
	v_fmac_f32_e32 v30, v54, v49
	s_waitcnt lgkmcnt(0)
	v_add_f32_e32 v49, v64, v50
	v_xor_b32_e32 v50, 32, v218
	v_cmp_lt_i32_e32 vcc, v50, v48
	s_mov_b32 s0, 0xf800000
	v_mul_f32_e32 v51, v74, v83
	v_cndmask_b32_e32 v48, v218, v50, vcc
	v_lshlrev_b32_e32 v48, 2, v48
	ds_bpermute_b32 v50, v48, v49
	v_fmac_f32_e32 v30, v55, v51
	v_mul_f32_e32 v51, v75, v76
	v_fmac_f32_e32 v30, v56, v51
	v_mul_f32_e32 v51, v72, v73
	s_waitcnt lgkmcnt(0)
	v_add_f32_e32 v49, v49, v50
	v_mul_f32_e32 v50, 0x4f800000, v49
	v_cmp_gt_f32_e32 vcc, s0, v49
	v_fmac_f32_e32 v30, v57, v51
	ds_bpermute_b32 v31, v31, v30
	v_cndmask_b32_e32 v49, v49, v50, vcc
	v_sqrt_f32_e32 v50, v49
	s_waitcnt lgkmcnt(0)
	v_add_f32_e32 v30, v30, v31
	v_add_u32_e32 v51, -1, v50
	v_fma_f32 v52, -v51, v50, v49
	v_cmp_ge_f32_e64 s[46:47], 0, v52
	v_add_u32_e32 v52, 1, v50
	ds_bpermute_b32 v31, v48, v30
	v_cndmask_b32_e64 v51, v50, v51, s[46:47]
	v_fma_f32 v50, -v52, v50, v49
	v_cmp_lt_f32_e64 s[46:47], 0, v50
	s_nop 1
	v_cndmask_b32_e64 v50, v51, v52, s[46:47]
	v_mul_f32_e32 v51, 0x37800000, v50
	v_cndmask_b32_e32 v50, v50, v51, vcc
	v_cmp_class_f32_e32 vcc, v49, v222
	s_nop 1
	v_cndmask_b32_e32 v49, v50, v49, vcc
	v_max_f32_e32 v49, 0x2b8cbccc, v49
	v_rcp_f32_e32 v48, v49
	s_nop 0
	v_pk_mul_f32 v[34:35], v[34:35], v[48:49] op_sel_hi:[1,0]
	v_pk_mul_f32 v[36:37], v[36:37], v[48:49] op_sel_hi:[1,0]
	v_pk_mul_f32 v[50:51], v[146:147], v[34:35]
	v_pk_mul_f32 v[52:53], v[148:149], v[36:37]
	v_cvt_pk_bf16_f32 v34, v34, v35
	v_cvt_pk_bf16_f32 v35, v36, v37
	v_lshl_add_u64 v[36:37], s[60:61], 0, v[150:151]
	global_store_dwordx2 v[36:37], v[34:35], off
	v_cvt_pk_bf16_f32 v34, v50, v51
	v_cvt_pk_bf16_f32 v35, v52, v53
	v_lshl_add_u64 v[36:37], s[68:69], 0, v[150:151]
	global_store_dwordx2 v[36:37], v[34:35], off
	v_pk_mul_f32 v[32:33], v[32:33], v[48:49] op_sel_hi:[1,0]
	v_pk_mul_f32 v[36:37], v[38:39], v[48:49] op_sel_hi:[1,0]
	v_pk_mul_f32 v[34:35], v[154:155], v[32:33]
	v_pk_mul_f32 v[38:39], v[156:157], v[36:37]
	v_cvt_pk_bf16_f32 v32, v32, v33
	v_cvt_pk_bf16_f32 v33, v36, v37
	v_or_b32_e32 v36, 32, v150
	v_mov_b32_e32 v37, v151
	v_lshl_add_u64 v[50:51], s[60:61], 0, v[36:37]
	global_store_dwordx2 v[50:51], v[32:33], off
	v_cvt_pk_bf16_f32 v32, v34, v35
	v_cvt_pk_bf16_f32 v33, v38, v39
	v_lshl_add_u64 v[34:35], s[68:69], 0, v[36:37]
	global_store_dwordx2 v[34:35], v[32:33], off
	v_pk_mul_f32 v[32:33], v[40:41], v[48:49] op_sel_hi:[1,0]
	v_pk_mul_f32 v[36:37], v[42:43], v[48:49] op_sel_hi:[1,0]
	v_pk_mul_f32 v[34:35], v[108:109], v[32:33]
	v_pk_mul_f32 v[38:39], v[110:111], v[36:37]
	v_cvt_pk_bf16_f32 v32, v32, v33
	v_cvt_pk_bf16_f32 v33, v36, v37
	v_or_b32_e32 v36, 64, v150
	v_mov_b32_e32 v37, v151
	v_lshl_add_u64 v[40:41], s[60:61], 0, v[36:37]
	global_store_dwordx2 v[40:41], v[32:33], off
	v_cvt_pk_bf16_f32 v32, v34, v35
	v_cvt_pk_bf16_f32 v33, v38, v39
	v_lshl_add_u64 v[34:35], s[68:69], 0, v[36:37]
	global_store_dwordx2 v[34:35], v[32:33], off
	v_pk_mul_f32 v[32:33], v[44:45], v[48:49] op_sel_hi:[1,0]
	v_pk_mul_f32 v[36:37], v[46:47], v[48:49] op_sel_hi:[1,0]
	v_or_b32_e32 v150, 0x60, v150
	v_pk_mul_f32 v[34:35], v[70:71], v[32:33]
	v_pk_mul_f32 v[38:39], v[62:63], v[36:37]
	v_cvt_pk_bf16_f32 v32, v32, v33
	v_cvt_pk_bf16_f32 v33, v36, v37
	v_lshl_add_u64 v[36:37], s[60:61], 0, v[150:151]
	global_store_dwordx2 v[36:37], v[32:33], off
	v_cvt_pk_bf16_f32 v32, v34, v35
	v_cvt_pk_bf16_f32 v33, v38, v39
	v_lshl_add_u64 v[34:35], s[68:69], 0, v[150:151]
	global_store_dwordx2 v[34:35], v[32:33], off
	s_and_saveexec_b64 s[2:3], s[44:45]
	s_cbranch_execz .LBB0_837
	v_lshlrev_b64 v[32:33], 6, v[140:141]
	v_lshl_add_u64 v[32:33], s[62:63], 0, v[32:33]
	s_lshl_b32 s94, s12, 2
	v_lshl_add_u64 v[32:33], v[32:33], 0, s[94:95]
	s_waitcnt lgkmcnt(0)
	v_add_f32_e32 v30, v30, v31
	global_store_dword v[32:33], v30, off
	s_branch .LBB0_837

; DI void phase_chunkA(const Args& a, LAS unsigned char* lds, int wave, int lane, int tid, int bid, int G) {
;     ...
;           for (int e = 0; e < 8; ++e) gp[e] = gv[e] / wv[e];
;           if (t == CK - 1) {
; #pragma unroll
;               for (int e = 0; e < 8; ++e) gC[c8 + e] = gv[e]; } }
;         {
;           float rt[8], at[8], kt[8], bt[8], vv[8];
; #pragma unroll
;           for (int e = 0; e < 8; ++e) { const unsigned rw = (e < 2) ? r8.x : (e < 4) ? r8.y : (e < 6) ? r8.z : r8.w, kw = (e < 2) ? k8.x : (e < 4) ? k8.y : (e < 6) ? k8.z : k8.w, vw = (e < 2) ? v8.x : (e < 4) ? v8.y : (e < 6) ? v8.z : v8.w,
;                   qw = (e < 2) ? kk8.x : (e < 4) ? kk8.y : (e < 6) ? kk8.z : kk8.w, bw = (e < 2) ? b8.x : (e < 4) ? b8.y : (e < 6) ? b8.z : b8.w;
;               const float rv = (e & 1) ? bfhi(rw) : bflo(rw), kv = (e & 1) ? bfhi(kw) : bflo(kw), vx = (e & 1) ? bfhi(vw) : bflo(vw), qv = (e & 1) ? bfhi(qw) : bflo(qw), bv = (e & 1) ? bfhi(bw) : bflo(bw);
;               const float ig = 1.f / gv[e];
;               rt[e] = rv * gv[e]; at[e] = -qv * gp[e]; kt[e] = kv * ig; bt[e] = bv * ig; vv[e] = vx; }
;           *(LAS u32x4*)(SL(6) + t * CP + c8) = (u32x4){pk2(rt[0], rt[1]), pk2(rt[2], rt[3]), pk2(rt[4], rt[5]), pk2(rt[6], rt[7])};
;           *(LAS u32x4*)(SL(0) + t * CP + c8) = (u32x4){pk2(at[0], at[1]), pk2(at[2], at[3]), pk2(at[4], at[5]), pk2(at[6], at[7])};
;           *(LAS u32x4*)(SL(4) + t * CP + c8) = (u32x4){pk2(kt[0], kt[1]), pk2(kt[2], kt[3]), pk2(kt[4], kt[5]), pk2(kt[6], kt[7])};
;           *(LAS u32x4*)(SL(2) + t * CP + c8) = (u32x4){pk2(bt[0], bt[1]), pk2(bt[2], bt[3]), pk2(bt[4], bt[5]), pk2(bt[6], bt[7])};
;           *(LAS u32x4*)(SL(10) + t * CP + c8) = (u32x4){pk2(vv[0], vv[1]), pk2(vv[2], vv[3]), pk2(vv[4], vv[5]), pk2(vv[6], vv[7])};
;           { unsigned iw[4];
; #pragma unroll
;             for (int e = 0; e < 4; ++e) iw[e] = ((c8 + 2 * e == t) ? 0x3f80u : 0u) | ((c8 + 2 * e + 1 == t) ? 0x3f800000u : 0u);
;             *(LAS u32x4*)(SL(11) + t * CP + c8) = (u32x4){iw[0], iw[1], iw[2], iw[3]}; } }
;         CK_BAR();
;     ...
;         { auto t1 = [&](int m, int n, f32x4 v) { ck_wr_tr(SL(1), m, n, v); }; auto t3 = [&](int m, int n, f32x4 v) { ck_wr_tr(SL(3), m, n, v); };
;           auto t5 = [&](int m, int n, f32x4 v) { ck_wr_tr(SL(5), m, n, v); }; auto t7 = [&](int m, int n, f32x4 v) { ck_wr_tr(SL(7), m, n, v); };
.LBB0_1017:
	s_or_b64 exec, exec, s[2:3]
	v_lshlrev_b32_e32 v84, 16, v42
	v_and_b32_e32 v85, 0xffff0000, v42
	v_lshlrev_b32_e32 v90, 16, v43
	v_rcp_f32_e32 v78, v59
	s_nop 0
	v_mul_f32_e32 v79, v67, v78
	v_and_b32_e32 v92, 0xffff0000, v43
	v_lshlrev_b32_e32 v93, 16, v45
	v_and_b32_e32 v144, 0xffff0000, v45
	v_rcp_f32_e32 v59, v58
	s_nop 0
	v_mul_f32_e32 v78, v66, v59
	v_rcp_f32_e32 v58, v61
	s_nop 0
	v_mul_f32_e32 v61, v69, v58
	v_rcp_f32_e32 v58, v60
	s_nop 0
	v_mul_f32_e32 v60, v68, v58
	v_rcp_f32_e32 v58, v55
	s_nop 0
	v_mul_f32_e32 v59, v63, v58
	v_rcp_f32_e32 v55, v54
	s_nop 0
	v_mul_f32_e32 v58, v62, v55
	v_rcp_f32_e32 v54, v57
	s_nop 0
	v_mul_f32_e32 v55, v65, v54
	v_rcp_f32_e32 v54, v56
	s_nop 0
	v_mul_f32_e32 v54, v64, v54
	v_rcp_f32_e32 v57, v67
	v_lshlrev_b32_e32 v80, 16, v34
	v_and_b32_e32 v81, 0xffff0000, v34
	v_rcp_f32_e32 v56, v66
	v_pk_mul_f32 v[80:81], v[66:67], v[80:81]
	v_lshlrev_b32_e32 v66, 16, v46
	v_and_b32_e32 v67, 0xffff0000, v46
	v_pk_mul_f32 v[78:79], v[78:79], v[66:67] neg_lo:[0,1] neg_hi:[0,1]
	v_lshlrev_b32_e32 v66, 16, v38
	v_and_b32_e32 v67, 0xffff0000, v38
	v_lshlrev_b32_e32 v82, 16, v50
	v_and_b32_e32 v83, 0xffff0000, v50
	v_pk_mul_f32 v[66:67], v[56:57], v[66:67]
	v_pk_mul_f32 v[56:57], v[56:57], v[82:83]
	v_rcp_f32_e32 v83, v69
	v_rcp_f32_e32 v82, v68
	v_lshlrev_b32_e32 v34, 16, v35
	v_and_b32_e32 v35, 0xffff0000, v35
	v_pk_mul_f32 v[42:43], v[68:69], v[34:35]
	v_lshlrev_b32_e32 v34, 16, v47
	v_and_b32_e32 v35, 0xffff0000, v47
	v_pk_mul_f32 v[46:47], v[60:61], v[34:35] neg_lo:[0,1] neg_hi:[0,1]
	v_lshlrev_b32_e32 v34, 16, v39
	v_and_b32_e32 v35, 0xffff0000, v39
	v_pk_mul_f32 v[38:39], v[82:83], v[34:35]
	v_lshlrev_b32_e32 v34, 16, v51
	v_and_b32_e32 v35, 0xffff0000, v51
	v_pk_mul_f32 v[50:51], v[82:83], v[34:35]
	v_lshlrev_b32_e32 v82, 16, v44
	v_and_b32_e32 v83, 0xffff0000, v44
	v_rcp_f32_e32 v35, v63
	v_lshlrev_b32_e32 v60, 16, v36
	v_and_b32_e32 v61, 0xffff0000, v36
	v_rcp_f32_e32 v34, v62
	v_pk_mul_f32 v[60:61], v[62:63], v[60:61]
	v_lshlrev_b32_e32 v62, 16, v48
	v_and_b32_e32 v63, 0xffff0000, v48
	v_pk_mul_f32 v[58:59], v[58:59], v[62:63] neg_lo:[0,1] neg_hi:[0,1]
	v_lshlrev_b32_e32 v62, 16, v40
	v_and_b32_e32 v63, 0xffff0000, v40
	v_lshlrev_b32_e32 v68, 16, v52
	v_and_b32_e32 v69, 0xffff0000, v52
	v_pk_mul_f32 v[62:63], v[34:35], v[62:63]
	v_pk_mul_f32 v[68:69], v[34:35], v[68:69]
	v_rcp_f32_e32 v35, v65
	v_lshlrev_b32_e32 v36, 16, v37
	v_and_b32_e32 v37, 0xffff0000, v37
	v_pk_mul_f32 v[44:45], v[64:65], v[36:37]
	v_lshlrev_b32_e32 v36, 16, v49
	v_and_b32_e32 v37, 0xffff0000, v49
	v_rcp_f32_e32 v34, v64
	v_pk_mul_f32 v[48:49], v[54:55], v[36:37] neg_lo:[0,1] neg_hi:[0,1]
	v_lshlrev_b32_e32 v36, 16, v41
	v_and_b32_e32 v37, 0xffff0000, v41
	v_pk_mul_f32 v[40:41], v[34:35], v[36:37]
	v_lshlrev_b32_e32 v36, 16, v53
	v_and_b32_e32 v37, 0xffff0000, v53
	v_pk_mul_f32 v[52:53], v[34:35], v[36:37]
	v_cvt_pk_bf16_f32 v34, v80, v81
	v_cvt_pk_bf16_f32 v35, v42, v43
	v_cvt_pk_bf16_f32 v36, v60, v61
	v_cvt_pk_bf16_f32 v37, v44, v45
	ds_write_b128 v89, v[34:37] offset:55296
	v_cvt_pk_bf16_f32 v34, v78, v79
	v_cvt_pk_bf16_f32 v35, v46, v47
	v_cvt_pk_bf16_f32 v36, v58, v59
	v_cvt_pk_bf16_f32 v37, v48, v49
	ds_write_b128 v89, v[34:37]
	v_cvt_pk_bf16_f32 v34, v66, v67
	v_cvt_pk_bf16_f32 v35, v38, v39
	v_cvt_pk_bf16_f32 v36, v62, v63
	v_cvt_pk_bf16_f32 v37, v40, v41
	ds_write_b128 v89, v[34:37] offset:36864
	v_cvt_pk_bf16_f32 v34, v56, v57
	v_cvt_pk_bf16_f32 v35, v50, v51
	v_cvt_pk_bf16_f32 v36, v68, v69
	v_cvt_pk_bf16_f32 v37, v52, v53
	ds_write_b128 v89, v[34:37] offset:18432
	v_cvt_pk_bf16_f32 v34, v84, v85
	v_cvt_pk_bf16_f32 v35, v90, v92
	v_cvt_pk_bf16_f32 v36, v82, v83
	v_cvt_pk_bf16_f32 v37, v93, v144
	ds_write_b128 v94, v[34:37]
	ds_write_b128 v95, v[2:5]
	s_waitcnt lgkmcnt(0)
	s_barrier
	ds_read_b128 v[34:37], v97
	ds_read_b128 v[38:41], v142
	ds_read_b128 v[42:45], v142 offset:2304
	ds_read_b128 v[46:49], v97 offset:64
	ds_read_b128 v[50:53], v142 offset:64
	ds_read_b128 v[54:57], v142 offset:2368
	ds_read_b128 v[58:61], v97 offset:18432
	ds_read_b128 v[62:65], v97 offset:18496
	s_waitcnt lgkmcnt(6)
	v_mfma_f32_16x16x32_bf16 v[66:69], v[34:37], v[38:41], 0
	s_waitcnt lgkmcnt(5)
	v_mfma_f32_16x16x32_bf16 v[34:37], v[34:37], v[42:45], 0
	s_waitcnt lgkmcnt(2)
	v_mfma_f32_16x16x32_bf16 v[34:37], v[46:49], v[54:57], v[34:37]
	s_waitcnt lgkmcnt(1)
	v_mfma_f32_16x16x32_bf16 v[38:41], v[58:61], v[38:41], 0
	v_mfma_f32_16x16x32_bf16 v[42:45], v[58:61], v[42:45], 0
	s_nop 4
	v_cvt_pk_bf16_f32 v34, v34, v35
	v_cvt_pk_bf16_f32 v35, v36, v37
	ds_write_b64 v99, v[34:35] offset:11520
	s_waitcnt lgkmcnt(1)
	v_mfma_f32_16x16x32_bf16 v[34:37], v[62:65], v[50:53], v[38:41]
	v_mfma_f32_16x16x32_bf16 v[66:69], v[46:49], v[50:53], v[66:69]
	s_nop 6
	v_cvt_pk_bf16_f32 v34, v34, v35
	v_cvt_pk_bf16_f32 v35, v36, v37
	ds_write_b64 v99, v[34:35] offset:27648
	v_mfma_f32_16x16x32_bf16 v[34:37], v[62:65], v[54:57], v[42:45]
	v_cvt_pk_bf16_f32 v46, v66, v67
	v_cvt_pk_bf16_f32 v47, v68, v69
	ds_write_b64 v99, v[46:47] offset:9216
	s_nop 4
	v_cvt_pk_bf16_f32 v34, v34, v35
	v_cvt_pk_bf16_f32 v35, v36, v37
	ds_write_b64 v99, v[34:35] offset:29952
	ds_read_b128 v[34:37], v97 offset:36864
	ds_read_b128 v[38:41], v97 offset:36928
	ds_read_b128 v[42:45], v142
	ds_read_b128 v[46:49], v142 offset:64
	ds_read_b128 v[50:53], v142 offset:2304
	ds_read_b128 v[54:57], v142 offset:2368
	ds_read_b128 v[58:61], v101
	ds_read_b128 v[62:65], v101 offset:64
	s_waitcnt lgkmcnt(5)
	v_mfma_f32_16x16x32_bf16 v[66:69], v[34:37], v[42:45], 0
	s_waitcnt lgkmcnt(3)
	v_mfma_f32_16x16x32_bf16 v[34:37], v[34:37], v[50:53], 0
	s_waitcnt lgkmcnt(2)
	v_mfma_f32_16x16x32_bf16 v[34:37], v[38:41], v[54:57], v[34:37]
	v_mfma_f32_16x16x32_bf16 v[66:69], v[38:41], v[46:49], v[66:69]
	s_waitcnt lgkmcnt(1)
	v_mfma_f32_16x16x32_bf16 v[38:41], v[58:61], v[42:45], 0
	s_nop 4
	v_cvt_pk_bf16_f32 v34, v34, v35
	v_cvt_pk_bf16_f32 v35, v36, v37
	v_cvt_pk_bf16_f32 v42, v66, v67
	v_cvt_pk_bf16_f32 v43, v68, v69
	ds_write_b64 v99, v[34:35] offset:48384
	s_waitcnt lgkmcnt(1)
	v_mfma_f32_16x16x32_bf16 v[34:37], v[62:65], v[46:49], v[38:41]
	ds_write_b64 v99, v[42:43] offset:46080
	v_mfma_f32_16x16x32_bf16 v[42:45], v[58:61], v[50:53], 0
	s_nop 5
	v_cvt_pk_bf16_f32 v34, v34, v35
	v_cvt_pk_bf16_f32 v35, v36, v37
	ds_write_b64 v99, v[34:35] offset:64512
	v_mfma_f32_16x16x32_bf16 v[34:37], v[62:65], v[54:57], v[42:45]
	s_nop 7
	v_cvt_pk_bf16_f32 v34, v34, v35
	v_cvt_pk_bf16_f32 v35, v36, v37
	ds_write_b64 v102, v[34:35]
	s_waitcnt lgkmcnt(0)
	s_barrier
; DI void ck_wr_tr(LAS bf16* XT, int m, int n, f32x4 v) { *(LAS u32x2*)(XT + n * CP + m) = (u32x2){pk2(v[0], v[1]), pk2(v[2], v[3])}; }
; #define CK_RUN2(A1, B1, E1, A2, B2, E2) do { CkF f1_, f2_; ck_ld(f1_, A1, B1, wave, lane); ck_ld(f2_, A2, B2, wave, lane); __builtin_amdgcn_sched_barrier(0); \
;             f32x4 c1_[2] = CK_Z2, c2_[2] = CK_Z2; ck_mma(c1_, f1_); ck_mma(c2_, f2_); ck_epi(c1_, wave, lane, E1); ck_epi(c2_, wave, lane, E2); } while (0)
; DI void phase_chunkA(const Args& a, LAS unsigned char* lds, int wave, int lane, int tid, int bid, int G) {
;     ...
;         { auto ePT = [&](int m, int n, f32x4 v) {
; #pragma unroll
;               for (int g = 0; g < 4; ++g) v[g] = (n < m + g) ? v[g] : 0.f;
;               ck_wr_tr(SL(13), m, n, v); };
;           auto ePA = [&](int m, int n, f32x4 v) { f32x4 tt;
; #pragma unroll
;               for (int g = 0; g < 4; ++g) { v[g] = (m + g < n) ? v[g] : 0.f; tt[g] = (m + g == n) ? 1.f : v[g]; }
;               ck_wr_tr(SL(12), m, n, v); ck_wr_tr(SL(8), m, n, tt); };
;           auto eMak = [&](int m, int n, f32x4 v) {
; #pragma unroll
;               for (int g = 0; g < 4; ++g) v[g] = (m + g < n) ? v[g] : 0.f;
;               ck_wr_tr(SL(9), m, n, v); };
;           CK_RUN3(SL(0), SL(2), ePT, SL(2), SL(0), ePA, SL(4), SL(0), eMak); }
;         { auto eNrb = [&](int m, int n, f32x4 v) {
; #pragma unroll
;               for (int g = 0; g < 4; ++g) v[g] = (m + g <= n) ? v[g] : 0.f;
;               ck_wr_tr(SL(10), m, n, v); };
;           auto eNrk = [&](int m, int n, f32x4 v) {
; #pragma unroll
;               for (int g = 0; g < 4; ++g) v[g] = (m + g <= n) ? v[g] : 0.f;
;               ck_wr_tr(SL(11), m, n, v); };
;           CK_RUN2(SL(2), SL(6), eNrb, SL(4), SL(6), eNrk); }
	v_add_u32_e32 v34, v96, v98
	ds_read_b128 v[36:39], v97
	ds_read_b128 v[40:43], v97 offset:64
	ds_read_b128 v[44:47], v34 offset:18432
	ds_read_b128 v[48:51], v34 offset:18496
	ds_read_b128 v[52:55], v34 offset:20736
	ds_read_b128 v[56:59], v34 offset:20800
	ds_read_b128 v[60:63], v97 offset:18432
	ds_read_b128 v[64:67], v97 offset:18496
	ds_read_b128 v[78:81], v34
	ds_read_b128 v[82:85], v34 offset:64
	ds_read_b128 v[144:147], v34 offset:2304
	ds_read_b128 v[148:151], v34 offset:2368
	ds_read_b128 v[152:155], v97 offset:36864
	ds_read_b128 v[156:159], v97 offset:36928
	s_waitcnt lgkmcnt(11)
	v_mfma_f32_16x16x32_bf16 v[44:47], v[36:39], v[44:47], 0
	s_waitcnt lgkmcnt(9)
	v_mfma_f32_16x16x32_bf16 v[36:39], v[36:39], v[52:55], 0
	v_mfma_f32_16x16x32_bf16 v[44:47], v[40:43], v[48:51], v[44:47]
	s_waitcnt lgkmcnt(8)
	v_mfma_f32_16x16x32_bf16 v[36:39], v[40:43], v[56:59], v[36:39]
	s_nop 5
	v_cndmask_b32_e64 v35, 0, v44, s[48:49]
	v_cndmask_b32_e64 v44, v45, 0, s[50:51]
	v_cvt_pk_bf16_f32 v44, v35, v44
	v_cndmask_b32_e64 v35, 0, v36, s[56:57]
	v_cndmask_b32_e64 v40, v37, 0, s[58:59]
	v_cndmask_b32_e64 v41, 0, v38, s[60:61]
	v_cndmask_b32_e64 v42, 0, v39, s[62:63]
	s_waitcnt lgkmcnt(5)
	v_mfma_f32_16x16x32_bf16 v[36:39], v[60:63], v[78:81], 0
	v_cndmask_b32_e64 v45, 0, v46, s[52:53]
	v_cndmask_b32_e64 v46, 0, v47, s[54:55]
	v_cvt_pk_bf16_f32 v45, v45, v46
	s_waitcnt lgkmcnt(4)
	v_mfma_f32_16x16x32_bf16 v[36:39], v[64:67], v[82:85], v[36:39]
	v_cvt_pk_bf16_f32 v40, v35, v40
	v_cvt_pk_bf16_f32 v41, v41, v42
	ds_write_b64 v103, v[44:45]
	ds_write_b64 v104, v[40:41]
	s_waitcnt lgkmcnt(5)
	v_mfma_f32_16x16x32_bf16 v[40:43], v[60:63], v[144:147], 0
	s_nop 1
	v_cndmask_b32_e64 v35, 0, v36, s[50:51]
	v_cndmask_b32_e64 v36, 0, v37, s[64:65]
	v_cndmask_b32_e64 v45, 0, v38, s[66:67]
	v_cndmask_b32_e64 v49, 0, v39, s[68:69]
	v_cndmask_b32_e64 v46, v35, 1.0, s[76:77]
	v_cndmask_b32_e64 v47, v36, 1.0, s[78:79]
	v_cndmask_b32_e64 v48, v45, 1.0, s[80:81]
	v_cndmask_b32_e64 v50, v49, 1.0, s[82:83]
	v_cvt_pk_bf16_f32 v44, v35, v36
	v_cvt_pk_bf16_f32 v45, v45, v49
	s_waitcnt lgkmcnt(4)
	v_mfma_f32_16x16x32_bf16 v[36:39], v[64:67], v[148:151], v[40:43]
	ds_write_b64 v105, v[44:45]
	v_cvt_pk_bf16_f32 v44, v46, v47
	v_cvt_pk_bf16_f32 v45, v48, v50
	s_waitcnt lgkmcnt(4)
	v_mfma_f32_16x16x32_bf16 v[40:43], v[152:155], v[78:81], 0
	ds_write_b64 v107, v[44:45]
	s_nop 1
	v_cndmask_b32_e64 v35, 0, v36, s[58:59]
	v_cndmask_b32_e64 v49, 0, v37, s[70:71]
	v_mfma_f32_16x16x32_bf16 v[44:47], v[152:155], v[144:147], 0
	v_cndmask_b32_e64 v51, 0, v38, s[72:73]
	v_cndmask_b32_e64 v53, 0, v39, s[74:75]
	v_cndmask_b32_e64 v48, v35, 1.0, s[84:85]
	s_waitcnt lgkmcnt(4)
	v_mfma_f32_16x16x32_bf16 v[40:43], v[156:159], v[82:85], v[40:43]
	v_cndmask_b32_e64 v50, v49, 1.0, s[86:87]
	v_cndmask_b32_e64 v52, v51, 1.0, s[88:89]
	v_mfma_f32_16x16x32_bf16 v[36:39], v[156:159], v[148:151], v[44:47]
	s_nop 2
	v_cvt_pk_bf16_f32 v44, v35, v49
	s_nop 0
	v_cndmask_b32_e64 v35, 0, v40, s[50:51]
	v_cndmask_b32_e64 v40, 0, v41, s[64:65]
	v_cndmask_b32_e64 v46, v53, 1.0, s[90:91]
	v_cvt_pk_bf16_f32 v45, v51, v53
	v_cndmask_b32_e64 v41, 0, v42, s[66:67]
	v_cndmask_b32_e64 v42, 0, v43, s[68:69]
	v_cvt_pk_bf16_f32 v40, v35, v40
	v_cndmask_b32_e64 v35, 0, v36, s[58:59]
	v_cndmask_b32_e64 v36, 0, v37, s[70:71]
	v_cndmask_b32_e64 v37, 0, v38, s[72:73]
	v_cndmask_b32_e64 v38, 0, v39, s[74:75]
	ds_write_b64 v108, v[44:45]
	v_cvt_pk_bf16_f32 v44, v48, v50
	v_cvt_pk_bf16_f32 v45, v52, v46
	v_cvt_pk_bf16_f32 v41, v41, v42
	v_cvt_pk_bf16_f32 v36, v35, v36
	v_cvt_pk_bf16_f32 v37, v37, v38
	ds_write_b64 v109, v[44:45]
	ds_write_b64 v110, v[40:41]
	ds_write_b64 v111, v[36:37]
	ds_read_b128 v[36:39], v97 offset:18432
	ds_read_b128 v[40:43], v97 offset:18496
	ds_read_b128 v[44:47], v34 offset:55296
	ds_read_b128 v[48:51], v34 offset:55360
	ds_read_b128 v[52:55], v34 offset:57600
	ds_read_b128 v[56:59], v34 offset:57664
	ds_read_b128 v[60:63], v97 offset:36864
	ds_read_b128 v[64:67], v97 offset:36928
	s_waitcnt lgkmcnt(5)
	v_mfma_f32_16x16x32_bf16 v[78:81], v[36:39], v[44:47], 0
	s_waitcnt lgkmcnt(3)
	v_mfma_f32_16x16x32_bf16 v[36:39], v[36:39], v[52:55], 0
	v_mfma_f32_16x16x32_bf16 v[78:81], v[40:43], v[48:51], v[78:81]
	s_waitcnt lgkmcnt(2)
	v_mfma_f32_16x16x32_bf16 v[36:39], v[40:43], v[56:59], v[36:39]
	s_nop 5
	v_cndmask_b32_e64 v35, v78, 0, s[48:49]
	v_cndmask_b32_e64 v68, 0, v79, s[50:51]
	v_cvt_pk_bf16_f32 v68, v35, v68
	v_cndmask_b32_e64 v35, v36, 0, s[56:57]
	v_cndmask_b32_e64 v40, 0, v37, s[58:59]
	v_cndmask_b32_e64 v41, v38, 0, s[60:61]
	v_cndmask_b32_e64 v42, v39, 0, s[62:63]
	s_waitcnt lgkmcnt(1)
	v_mfma_f32_16x16x32_bf16 v[36:39], v[60:63], v[44:47], 0
	v_cndmask_b32_e64 v69, v80, 0, s[52:53]
	v_cndmask_b32_e64 v78, v81, 0, s[54:55]
	v_cvt_pk_bf16_f32 v69, v69, v78
	s_waitcnt lgkmcnt(0)
	v_mfma_f32_16x16x32_bf16 v[36:39], v[64:67], v[48:51], v[36:39]
	v_cvt_pk_bf16_f32 v40, v35, v40
	v_cvt_pk_bf16_f32 v41, v41, v42
	ds_write_b64 v112, v[68:69]
	ds_write_b64 v113, v[40:41]
	s_nop 3
	v_cndmask_b32_e64 v35, v36, 0, s[48:49]
	v_cndmask_b32_e64 v40, 0, v37, s[50:51]
	v_cndmask_b32_e64 v41, v38, 0, s[52:53]
	v_cndmask_b32_e64 v42, v39, 0, s[54:55]
	v_mfma_f32_16x16x32_bf16 v[36:39], v[60:63], v[52:55], 0
	v_cvt_pk_bf16_f32 v40, v35, v40
	v_cvt_pk_bf16_f32 v41, v41, v42
	ds_write_b64 v114, v[40:41]
	v_mfma_f32_16x16x32_bf16 v[36:39], v[64:67], v[56:59], v[36:39]
	s_nop 7
	v_cndmask_b32_e64 v35, v36, 0, s[56:57]
	v_cndmask_b32_e64 v36, 0, v37, s[58:59]
	v_cndmask_b32_e64 v37, v38, 0, s[60:61]
	v_cndmask_b32_e64 v38, v39, 0, s[62:63]
	v_cvt_pk_bf16_f32 v36, v35, v36
	v_cvt_pk_bf16_f32 v37, v37, v38
	ds_write_b64 v115, v[36:37]
	s_waitcnt lgkmcnt(0)
	s_barrier
; DI void ck_wr_tr(LAS bf16* XT, int m, int n, f32x4 v) { *(LAS u32x2*)(XT + n * CP + m) = (u32x2){pk2(v[0], v[1]), pk2(v[2], v[3])}; }
; #define CK_BAR() do { asm volatile("s_waitcnt lgkmcnt(0)" ::: "memory"); __builtin_amdgcn_s_barrier(); asm volatile("" ::: "memory"); } while (0)
; #define CK_RUN2(A1, B1, E1, A2, B2, E2) do { CkF f1_, f2_; ck_ld(f1_, A1, B1, wave, lane); ck_ld(f2_, A2, B2, wave, lane); __builtin_amdgcn_sched_barrier(0); \
;             f32x4 c1_[2] = CK_Z2, c2_[2] = CK_Z2; ck_mma(c1_, f1_); ck_mma(c2_, f2_); ck_epi(c1_, wave, lane, E1); ck_epi(c2_, wave, lane, E2); } while (0)
; DI void phase_chunkA(const Args& a, LAS unsigned char* lds, int wave, int lane, int tid, int bid, int G) {
;     ...
;         { auto eS1 = [&](int m, int n, f32x4 v) { ck_wr_tr(SL(2), m, n, v); }; auto eS2 = [&](int m, int n, f32x4 v) { ck_wr_tr(SL(0), m, n, v); };
;           CK_RUN2(SL(12), SL(13), eS1, SL(13), SL(12), eS2); }
;         CK_BAR();
;         CK_NEU(8, 4, 0, 2, 12, 13);
	v_add_u32_e32 v37, v118, v98
	ds_read_b128 v[38:41], v117
	ds_read_b128 v[42:45], v117 offset:64
	ds_read_b128 v[46:49], v37
	ds_read_b128 v[50:53], v37 offset:64
	ds_read_b128 v[54:57], v37 offset:2304
	ds_read_b128 v[58:61], v37 offset:2368
	v_add_u32_e32 v35, v116, v98
	ds_read_b128 v[62:65], v119
	ds_read_b128 v[66:69], v119 offset:64
	ds_read_b128 v[78:81], v35
	ds_read_b128 v[82:85], v35 offset:64
	ds_read_b128 v[144:147], v35 offset:2304
	ds_read_b128 v[148:151], v35 offset:2368
	s_waitcnt lgkmcnt(9)
	v_mfma_f32_16x16x32_bf16 v[46:49], v[38:41], v[46:49], 0
	s_waitcnt lgkmcnt(7)
	v_mfma_f32_16x16x32_bf16 v[38:41], v[38:41], v[54:57], 0
	s_waitcnt lgkmcnt(6)
	v_mfma_f32_16x16x32_bf16 v[38:41], v[42:45], v[58:61], v[38:41]
	v_mfma_f32_16x16x32_bf16 v[46:49], v[42:45], v[50:53], v[46:49]
	s_waitcnt lgkmcnt(3)
	v_mfma_f32_16x16x32_bf16 v[42:45], v[62:65], v[78:81], 0
	s_nop 4
	v_cvt_pk_bf16_f32 v38, v38, v39
	v_cvt_pk_bf16_f32 v39, v40, v41
	v_cvt_pk_bf16_f32 v46, v46, v47
	v_cvt_pk_bf16_f32 v47, v48, v49
	ds_write_b64 v99, v[38:39] offset:20736
	s_waitcnt lgkmcnt(3)
	v_mfma_f32_16x16x32_bf16 v[38:41], v[66:69], v[82:85], v[42:45]
	ds_write_b64 v99, v[46:47] offset:18432
	s_waitcnt lgkmcnt(3)
	v_mfma_f32_16x16x32_bf16 v[46:49], v[62:65], v[144:147], 0
	s_nop 4
	v_cvt_pk_bf16_f32 v38, v38, v39
	v_cvt_pk_bf16_f32 v39, v40, v41
	ds_write_b64 v99, v[38:39]
	s_waitcnt lgkmcnt(3)
	v_mfma_f32_16x16x32_bf16 v[38:41], v[66:69], v[148:151], v[46:49]
	s_nop 7
	v_cvt_pk_bf16_f32 v38, v38, v39
	v_cvt_pk_bf16_f32 v39, v40, v41
	ds_write_b64 v99, v[38:39] offset:2304
	s_waitcnt lgkmcnt(0)
	s_barrier
	v_add_u32_e32 v38, v120, v98
	ds_read_b128 v[40:43], v97 offset:18432
	ds_read_b128 v[44:47], v97 offset:18496
	ds_read_b128 v[48:51], v38
	ds_read_b128 v[52:55], v38 offset:64
	ds_read_b128 v[56:59], v38 offset:2304
	ds_read_b128 v[60:63], v38 offset:2368
	ds_read_b128 v[64:67], v97
	ds_read_b128 v[78:81], v97 offset:64
	ds_read_b128 v[82:85], v34 offset:18432
	ds_read_b128 v[144:147], v34 offset:18496
	ds_read_b128 v[148:151], v34 offset:20736
	ds_read_b128 v[152:155], v34 offset:20800
	ds_read_b128 v[156:159], v34
	ds_read_b128 v[160:163], v34 offset:64
	ds_read_b128 v[172:175], v34 offset:2304
	ds_read_b128 v[176:179], v34 offset:2368
	s_waitcnt lgkmcnt(13)
	v_mfma_f32_16x16x32_bf16 v[48:51], v[40:43], v[48:51], 0
	v_add_u32_e32 v36, v106, v98
	s_waitcnt lgkmcnt(11)
	v_mfma_f32_16x16x32_bf16 v[56:59], v[40:43], v[56:59], 0
	v_mfma_f32_16x16x32_bf16 v[48:51], v[44:47], v[52:55], v[48:51]
	s_waitcnt lgkmcnt(10)
	v_mfma_f32_16x16x32_bf16 v[52:55], v[44:47], v[60:63], v[56:59]
	s_waitcnt lgkmcnt(7)
	v_mfma_f32_16x16x32_bf16 v[56:59], v[64:67], v[82:85], 0
	s_waitcnt lgkmcnt(5)
	v_mfma_f32_16x16x32_bf16 v[60:63], v[64:67], v[148:151], 0
	s_waitcnt lgkmcnt(3)
	v_mfma_f32_16x16x32_bf16 v[64:67], v[40:43], v[156:159], 0
	s_waitcnt lgkmcnt(1)
	v_mfma_f32_16x16x32_bf16 v[40:43], v[40:43], v[172:175], 0
	v_mfma_f32_16x16x32_bf16 v[64:67], v[44:47], v[160:163], v[64:67]
	s_waitcnt lgkmcnt(0)
	v_mfma_f32_16x16x32_bf16 v[40:43], v[44:47], v[176:179], v[40:43]
	ds_read_b64 v[44:45], v107
	s_waitcnt lgkmcnt(0)
	v_lshlrev_b32_e32 v46, 16, v44
	v_and_b32_e32 v47, 0xffff0000, v44
	v_lshlrev_b32_e32 v44, 16, v45
	v_and_b32_e32 v45, 0xffff0000, v45
	v_pk_add_f32 v[46:47], v[48:49], v[46:47]
	v_pk_add_f32 v[44:45], v[50:51], v[44:45]
	v_cvt_pk_bf16_f32 v46, v46, v47
	v_cvt_pk_bf16_f32 v47, v44, v45
	ds_read_b64 v[44:45], v36 offset:2304
	v_mfma_f32_16x16x32_bf16 v[56:59], v[78:81], v[144:147], v[56:59]
	ds_write_b64 v121, v[46:47] offset:36864
	v_cvt_pk_bf16_f32 v40, v40, v41
	v_cvt_pk_bf16_f32 v41, v42, v43
	v_mfma_f32_16x16x32_bf16 v[60:63], v[78:81], v[152:155], v[60:63]
	s_waitcnt lgkmcnt(1)
	v_lshlrev_b32_e32 v46, 16, v44
	v_and_b32_e32 v47, 0xffff0000, v44
	v_lshlrev_b32_e32 v44, 16, v45
	v_and_b32_e32 v45, 0xffff0000, v45
	v_pk_add_f32 v[46:47], v[52:53], v[46:47]
	v_pk_add_f32 v[44:45], v[54:55], v[44:45]
	v_cvt_pk_bf16_f32 v46, v46, v47
	v_cvt_pk_bf16_f32 v47, v44, v45
	v_cvt_pk_bf16_f32 v44, v56, v57
	v_cvt_pk_bf16_f32 v45, v58, v59
	ds_write_b64 v121, v[46:47] offset:39168
	ds_write_b64 v122, v[44:45]
	v_cvt_pk_bf16_f32 v44, v60, v61
	v_cvt_pk_bf16_f32 v45, v62, v63
	ds_write_b64 v123, v[44:45]
	v_cvt_pk_bf16_f32 v44, v64, v65
	v_cvt_pk_bf16_f32 v45, v66, v67
	ds_write_b64 v124, v[44:45]
	ds_write_b64 v125, v[40:41]
	s_waitcnt lgkmcnt(0)
	s_barrier
; DI void ck_wr_tr(LAS bf16* XT, int m, int n, f32x4 v) { *(LAS u32x2*)(XT + n * CP + m) = (u32x2){pk2(v[0], v[1]), pk2(v[2], v[3])}; }
; #define CK_BAR() do { asm volatile("s_waitcnt lgkmcnt(0)" ::: "memory"); __builtin_amdgcn_s_barrier(); asm volatile("" ::: "memory"); } while (0)
; #define CK_RUN2(A1, B1, E1, A2, B2, E2) do { CkF f1_, f2_; ck_ld(f1_, A1, B1, wave, lane); ck_ld(f2_, A2, B2, wave, lane); __builtin_amdgcn_sched_barrier(0); \
;             f32x4 c1_[2] = CK_Z2, c2_[2] = CK_Z2; ck_mma(c1_, f1_); ck_mma(c2_, f2_); ck_epi(c1_, wave, lane, E1); ck_epi(c2_, wave, lane, E2); } while (0)
; DI void phase_chunkA(const Args& a, LAS unsigned char* lds, int wave, int lane, int tid, int bid, int G) {
;     ...
;         { auto eS1 = [&](int m, int n, f32x4 v) { ck_wr_tr(SL(2), m, n, v); }; auto eS2 = [&](int m, int n, f32x4 v) { ck_wr_tr(SL(0), m, n, v); };
;           CK_RUN2(SL(12), SL(13), eS1, SL(13), SL(12), eS2); }
;         CK_BAR();
;         CK_NEU(8, 4, 0, 2, 12, 13);
;         CK_NEU(4, 8, 12, 13, 0, 2);
;         CK_NEU(8, 4, 0, 2, 12, 13);
	ds_read_b128 v[40:43], v119
	ds_read_b128 v[44:47], v34 offset:36864
	ds_read_b128 v[48:51], v34 offset:39168
	ds_read_b128 v[52:55], v119 offset:64
	ds_read_b128 v[56:59], v34 offset:36928
	ds_read_b128 v[60:63], v34 offset:39232
	ds_read_b128 v[64:67], v117
	ds_read_b128 v[78:81], v37
	ds_read_b128 v[82:85], v37 offset:2304
	ds_read_b128 v[144:147], v117 offset:64
	ds_read_b128 v[148:151], v37 offset:64
	ds_read_b128 v[152:155], v37 offset:2368
	ds_read_b128 v[156:159], v35
	ds_read_b128 v[160:163], v35 offset:2304
	ds_read_b128 v[172:175], v35 offset:64
	ds_read_b128 v[176:179], v35 offset:2368
	s_waitcnt lgkmcnt(14)
	v_mfma_f32_16x16x32_bf16 v[44:47], v[40:43], v[44:47], 0
	s_waitcnt lgkmcnt(13)
	v_mfma_f32_16x16x32_bf16 v[48:51], v[40:43], v[48:51], 0
	s_waitcnt lgkmcnt(11)
	v_mfma_f32_16x16x32_bf16 v[44:47], v[52:55], v[56:59], v[44:47]
	s_waitcnt lgkmcnt(10)
	v_mfma_f32_16x16x32_bf16 v[48:51], v[52:55], v[60:63], v[48:51]
	s_waitcnt lgkmcnt(8)
	v_mfma_f32_16x16x32_bf16 v[56:59], v[64:67], v[78:81], 0
	s_waitcnt lgkmcnt(7)
	v_mfma_f32_16x16x32_bf16 v[60:63], v[64:67], v[82:85], 0
	s_waitcnt lgkmcnt(3)
	v_mfma_f32_16x16x32_bf16 v[64:67], v[40:43], v[156:159], 0
	s_waitcnt lgkmcnt(2)
	v_mfma_f32_16x16x32_bf16 v[40:43], v[40:43], v[160:163], 0
	s_waitcnt lgkmcnt(1)
	v_mfma_f32_16x16x32_bf16 v[64:67], v[52:55], v[172:175], v[64:67]
	s_waitcnt lgkmcnt(0)
	v_mfma_f32_16x16x32_bf16 v[40:43], v[52:55], v[176:179], v[40:43]
	ds_read_b64 v[52:53], v121 offset:36864
	s_waitcnt lgkmcnt(0)
	v_lshlrev_b32_e32 v54, 16, v52
	v_and_b32_e32 v55, 0xffff0000, v52
	v_lshlrev_b32_e32 v52, 16, v53
	v_and_b32_e32 v53, 0xffff0000, v53
	v_pk_add_f32 v[44:45], v[44:45], v[54:55]
	v_pk_add_f32 v[46:47], v[46:47], v[52:53]
	v_cvt_pk_bf16_f32 v44, v44, v45
	v_cvt_pk_bf16_f32 v45, v46, v47
	ds_write_b64 v107, v[44:45]
	ds_read_b64 v[44:45], v121 offset:39168
	v_mfma_f32_16x16x32_bf16 v[56:59], v[144:147], v[148:151], v[56:59]
	v_cvt_pk_bf16_f32 v40, v40, v41
	v_cvt_pk_bf16_f32 v41, v42, v43
	s_waitcnt lgkmcnt(0)
	v_lshlrev_b32_e32 v46, 16, v44
	v_mfma_f32_16x16x32_bf16 v[60:63], v[144:147], v[152:155], v[60:63]
	v_and_b32_e32 v47, 0xffff0000, v44
	v_lshlrev_b32_e32 v44, 16, v45
	v_and_b32_e32 v45, 0xffff0000, v45
	v_pk_add_f32 v[46:47], v[48:49], v[46:47]
	v_pk_add_f32 v[44:45], v[50:51], v[44:45]
	v_cvt_pk_bf16_f32 v46, v46, v47
	v_cvt_pk_bf16_f32 v47, v44, v45
	v_cvt_pk_bf16_f32 v44, v56, v57
	v_cvt_pk_bf16_f32 v45, v58, v59
	ds_write_b64 v36, v[46:47] offset:2304
	ds_write_b64 v99, v[44:45] offset:18432
	v_cvt_pk_bf16_f32 v44, v60, v61
	v_cvt_pk_bf16_f32 v45, v62, v63
	ds_write_b64 v99, v[44:45] offset:20736
	v_cvt_pk_bf16_f32 v44, v64, v65
	v_cvt_pk_bf16_f32 v45, v66, v67
	ds_write_b64 v99, v[44:45]
	ds_write_b64 v99, v[40:41] offset:2304
	s_waitcnt lgkmcnt(0)
	s_barrier
	ds_read_b128 v[40:43], v97 offset:18432
	ds_read_b128 v[44:47], v38
	ds_read_b128 v[48:51], v38 offset:2304
	ds_read_b128 v[52:55], v97 offset:18496
	ds_read_b128 v[56:59], v38 offset:64
	ds_read_b128 v[60:63], v38 offset:2368
	ds_read_b128 v[64:67], v97
	ds_read_b128 v[78:81], v34 offset:18432
	ds_read_b128 v[82:85], v34 offset:20736
	ds_read_b128 v[144:147], v97 offset:64
	ds_read_b128 v[148:151], v34 offset:18496
	ds_read_b128 v[152:155], v34 offset:20800
	ds_read_b128 v[156:159], v34
	ds_read_b128 v[160:163], v34 offset:2304
	ds_read_b128 v[172:175], v34 offset:64
	ds_read_b128 v[176:179], v34 offset:2368
	s_waitcnt lgkmcnt(14)
	v_mfma_f32_16x16x32_bf16 v[44:47], v[40:43], v[44:47], 0
	s_waitcnt lgkmcnt(13)
	v_mfma_f32_16x16x32_bf16 v[48:51], v[40:43], v[48:51], 0
	s_waitcnt lgkmcnt(11)
	v_mfma_f32_16x16x32_bf16 v[44:47], v[52:55], v[56:59], v[44:47]
	s_waitcnt lgkmcnt(10)
	v_mfma_f32_16x16x32_bf16 v[48:51], v[52:55], v[60:63], v[48:51]
	s_waitcnt lgkmcnt(8)
	v_mfma_f32_16x16x32_bf16 v[56:59], v[64:67], v[78:81], 0
	s_waitcnt lgkmcnt(7)
	v_mfma_f32_16x16x32_bf16 v[60:63], v[64:67], v[82:85], 0
	s_waitcnt lgkmcnt(3)
	v_mfma_f32_16x16x32_bf16 v[64:67], v[40:43], v[156:159], 0
	s_waitcnt lgkmcnt(2)
	v_mfma_f32_16x16x32_bf16 v[38:41], v[40:43], v[160:163], 0
	ds_read_b64 v[42:43], v107
	s_waitcnt lgkmcnt(2)
	v_mfma_f32_16x16x32_bf16 v[64:67], v[52:55], v[172:175], v[64:67]
	s_waitcnt lgkmcnt(1)
	v_mfma_f32_16x16x32_bf16 v[38:41], v[52:55], v[176:179], v[38:41]
	s_waitcnt lgkmcnt(0)
	v_lshlrev_b32_e32 v52, 16, v42
	v_and_b32_e32 v53, 0xffff0000, v42
	v_lshlrev_b32_e32 v42, 16, v43
	v_and_b32_e32 v43, 0xffff0000, v43
	v_pk_add_f32 v[44:45], v[44:45], v[52:53]
	v_pk_add_f32 v[42:43], v[46:47], v[42:43]
	v_cvt_pk_bf16_f32 v44, v44, v45
	v_cvt_pk_bf16_f32 v45, v42, v43
	ds_read_b64 v[42:43], v36 offset:2304
	v_mfma_f32_16x16x32_bf16 v[56:59], v[144:147], v[148:151], v[56:59]
	ds_write_b64 v121, v[44:45] offset:36864
	v_cvt_pk_bf16_f32 v38, v38, v39
	v_cvt_pk_bf16_f32 v39, v40, v41
	v_mfma_f32_16x16x32_bf16 v[60:63], v[144:147], v[152:155], v[60:63]
	s_waitcnt lgkmcnt(1)
	v_lshlrev_b32_e32 v44, 16, v42
	v_and_b32_e32 v45, 0xffff0000, v42
	v_lshlrev_b32_e32 v42, 16, v43
	v_and_b32_e32 v43, 0xffff0000, v43
	v_pk_add_f32 v[44:45], v[48:49], v[44:45]
	v_pk_add_f32 v[42:43], v[50:51], v[42:43]
	v_cvt_pk_bf16_f32 v44, v44, v45
	v_cvt_pk_bf16_f32 v45, v42, v43
	v_cvt_pk_bf16_f32 v42, v56, v57
	v_cvt_pk_bf16_f32 v43, v58, v59
	ds_write_b64 v121, v[44:45] offset:39168
	ds_write_b64 v122, v[42:43]
	v_cvt_pk_bf16_f32 v42, v60, v61
	v_cvt_pk_bf16_f32 v43, v62, v63
	ds_write_b64 v123, v[42:43]
	v_cvt_pk_bf16_f32 v42, v64, v65
	v_cvt_pk_bf16_f32 v43, v66, v67
	ds_write_b64 v124, v[42:43]
	ds_write_b64 v125, v[38:39]
	s_waitcnt lgkmcnt(0)
	s_barrier
; #define LAS __attribute__((address_space(3)))
; DI void ck_wr_tr(LAS bf16* XT, int m, int n, f32x4 v) { *(LAS u32x2*)(XT + n * CP + m) = (u32x2){pk2(v[0], v[1]), pk2(v[2], v[3])}; }
; #define CK_BAR() do { asm volatile("s_waitcnt lgkmcnt(0)" ::: "memory"); __builtin_amdgcn_s_barrier(); asm volatile("" ::: "memory"); } while (0)
; #define CK_RUN2(A1, B1, E1, A2, B2, E2) do { CkF f1_, f2_; ck_ld(f1_, A1, B1, wave, lane); ck_ld(f2_, A2, B2, wave, lane); __builtin_amdgcn_sched_barrier(0); \
;             f32x4 c1_[2] = CK_Z2, c2_[2] = CK_Z2; ck_mma(c1_, f1_); ck_mma(c2_, f2_); ck_epi(c1_, wave, lane, E1); ck_epi(c2_, wave, lane, E2); } while (0)
; DI void phase_chunkA(const Args& a, LAS unsigned char* lds, int wave, int lane, int tid, int bid, int G) {
;     ...
;         CK_NEU(8, 4, 0, 2, 12, 13);
;         CK_NEU(4, 8, 12, 13, 0, 2);
;         CK_NEU(8, 4, 0, 2, 12, 13);
;         CK_NEU(4, 8, 12, 13, 0, 2);
;         ck_mm(SL(2), SL(8), nullptr, nullptr, wave, lane, [&](int m, int n, f32x4 v) { const u32x2 o = *(const LAS u32x2*)(SL(8) + n * CP + m);
;             v[0] += bflo(o.x); v[1] += bfhi(o.x); v[2] += bflo(o.y); v[3] += bfhi(o.y); ck_wr_tr(SL(4), m, n, v); });
;         CK_BAR();
;     ...
;         { auto e12 = [&](int m, int n, f32x4 v) { ck_wr_tr(SL(12), m, n, v); }; auto e0 = [&](int m, int n, f32x4 v) { ck_wr_tr(SL(0), m, n, v); };
;           CK_RUN2(SL(9), SL(7), e12, SL(4), SL(1), e0); }
;         CK_BAR();
	ds_read_b128 v[38:41], v119
	ds_read_b128 v[42:45], v34 offset:36864
	ds_read_b128 v[46:49], v34 offset:39168
	ds_read_b128 v[50:53], v119 offset:64
	ds_read_b128 v[54:57], v34 offset:36928
	ds_read_b128 v[58:61], v34 offset:39232
	ds_read_b128 v[62:65], v117
	ds_read_b128 v[66:69], v37
	ds_read_b128 v[78:81], v37 offset:2304
	ds_read_b128 v[82:85], v117 offset:64
	ds_read_b128 v[144:147], v37 offset:64
	ds_read_b128 v[148:151], v37 offset:2368
	ds_read_b128 v[152:155], v35
	ds_read_b128 v[156:159], v35 offset:2304
	ds_read_b128 v[160:163], v35 offset:64
	ds_read_b128 v[172:175], v35 offset:2368
	s_waitcnt lgkmcnt(14)
	v_mfma_f32_16x16x32_bf16 v[42:45], v[38:41], v[42:45], 0
	s_waitcnt lgkmcnt(13)
	v_mfma_f32_16x16x32_bf16 v[46:49], v[38:41], v[46:49], 0
	s_waitcnt lgkmcnt(11)
	v_mfma_f32_16x16x32_bf16 v[42:45], v[50:53], v[54:57], v[42:45]
	s_waitcnt lgkmcnt(10)
	v_mfma_f32_16x16x32_bf16 v[46:49], v[50:53], v[58:61], v[46:49]
	s_waitcnt lgkmcnt(8)
	v_mfma_f32_16x16x32_bf16 v[54:57], v[62:65], v[66:69], 0
	s_waitcnt lgkmcnt(7)
	v_mfma_f32_16x16x32_bf16 v[58:61], v[62:65], v[78:81], 0
	s_waitcnt lgkmcnt(3)
	v_mfma_f32_16x16x32_bf16 v[62:65], v[38:41], v[152:155], 0
	s_waitcnt lgkmcnt(2)
	v_mfma_f32_16x16x32_bf16 v[38:41], v[38:41], v[156:159], 0
	s_waitcnt lgkmcnt(1)
	v_mfma_f32_16x16x32_bf16 v[62:65], v[50:53], v[160:163], v[62:65]
	s_waitcnt lgkmcnt(0)
	v_mfma_f32_16x16x32_bf16 v[38:41], v[50:53], v[172:175], v[38:41]
	ds_read_b64 v[50:51], v121 offset:36864
	s_waitcnt lgkmcnt(0)
	v_lshlrev_b32_e32 v52, 16, v50
	v_and_b32_e32 v53, 0xffff0000, v50
	v_lshlrev_b32_e32 v50, 16, v51
	v_and_b32_e32 v51, 0xffff0000, v51
	v_pk_add_f32 v[42:43], v[42:43], v[52:53]
	v_pk_add_f32 v[44:45], v[44:45], v[50:51]
	v_cvt_pk_bf16_f32 v42, v42, v43
	v_cvt_pk_bf16_f32 v43, v44, v45
	ds_write_b64 v107, v[42:43]
	ds_read_b64 v[42:43], v121 offset:39168
	v_mfma_f32_16x16x32_bf16 v[54:57], v[82:85], v[144:147], v[54:57]
	s_waitcnt lgkmcnt(0)
	v_lshlrev_b32_e32 v44, 16, v42
	v_mfma_f32_16x16x32_bf16 v[58:61], v[82:85], v[148:151], v[58:61]
	v_and_b32_e32 v45, 0xffff0000, v42
	v_lshlrev_b32_e32 v42, 16, v43
	v_and_b32_e32 v43, 0xffff0000, v43
	v_pk_add_f32 v[44:45], v[46:47], v[44:45]
	v_pk_add_f32 v[42:43], v[48:49], v[42:43]
	v_cvt_pk_bf16_f32 v44, v44, v45
	v_cvt_pk_bf16_f32 v45, v42, v43
	ds_write_b64 v36, v[44:45] offset:2304
	v_cvt_pk_bf16_f32 v36, v54, v55
	v_cvt_pk_bf16_f32 v37, v56, v57
	ds_write_b64 v99, v[36:37] offset:18432
	v_cvt_pk_bf16_f32 v36, v58, v59
	v_cvt_pk_bf16_f32 v37, v60, v61
	ds_write_b64 v99, v[36:37] offset:20736
	v_cvt_pk_bf16_f32 v36, v62, v63
	v_cvt_pk_bf16_f32 v37, v64, v65
	ds_write_b64 v99, v[36:37]
	v_cvt_pk_bf16_f32 v36, v38, v39
	v_cvt_pk_bf16_f32 v37, v40, v41
	ds_write_b64 v99, v[36:37] offset:2304
	s_waitcnt lgkmcnt(0)
	s_barrier
	ds_read_b128 v[36:39], v97 offset:18432
	v_add_u32_e32 v56, v120, v126
	ds_read_b128 v[40:43], v56
	ds_read_b128 v[44:47], v56 offset:2304
	ds_read_b128 v[48:51], v97 offset:18496
	ds_read_b128 v[52:55], v56 offset:64
	ds_read_b128 v[56:59], v56 offset:2368
	s_waitcnt lgkmcnt(4)
	v_mfma_f32_16x16x32_bf16 v[40:43], v[36:39], v[40:43], 0
	s_waitcnt lgkmcnt(3)
	v_mfma_f32_16x16x32_bf16 v[36:39], v[36:39], v[44:47], 0
	ds_read_b64 v[44:45], v127
	s_waitcnt lgkmcnt(0)
	v_lshlrev_b32_e32 v46, 16, v44
	v_mfma_f32_16x16x32_bf16 v[40:43], v[48:51], v[52:55], v[40:43]
	v_and_b32_e32 v47, 0xffff0000, v44
	v_lshlrev_b32_e32 v44, 16, v45
	v_and_b32_e32 v45, 0xffff0000, v45
	v_mfma_f32_16x16x32_bf16 v[36:39], v[48:51], v[56:59], v[36:39]
	s_nop 3
	v_add_f32_e64 v40, v40, v46
	v_add_f32_e64 v41, v41, v47
	v_pk_add_f32 v[42:43], v[42:43], v[44:45]
	v_cvt_pk_bf16_f32 v40, v40, v41
	v_cvt_pk_bf16_f32 v41, v42, v43
	ds_write_b64 v128, v[40:41] offset:36864
	v_add_u32_e32 v40, v106, v126
	ds_read_b64 v[40:41], v40 offset:2304
	s_waitcnt lgkmcnt(0)
	v_lshlrev_b32_e32 v42, 16, v40
	v_and_b32_e32 v43, 0xffff0000, v40
	v_lshlrev_b32_e32 v40, 16, v41
	v_and_b32_e32 v41, 0xffff0000, v41
	v_pk_add_f32 v[36:37], v[36:37], v[42:43]
	v_pk_add_f32 v[38:39], v[38:39], v[40:41]
	v_cvt_pk_bf16_f32 v36, v36, v37
	v_cvt_pk_bf16_f32 v37, v38, v39
	ds_write_b64 v128, v[36:37] offset:39168
	s_waitcnt lgkmcnt(0)
	s_barrier
	ds_read_b128 v[36:39], v129
	ds_read_b128 v[40:43], v34 offset:64512
	ds_read_b128 v[44:47], v143 offset:64512
	ds_read_b128 v[48:51], v129 offset:64
	ds_read_b128 v[52:55], v34 offset:64576
	ds_read_b128 v[56:59], v143 offset:64576
	ds_read_b128 v[60:63], v97 offset:36864
	ds_read_b128 v[64:67], v34 offset:9216
	ds_read_b128 v[78:81], v34 offset:11520
	ds_read_b128 v[82:85], v97 offset:36928
	ds_read_b128 v[144:147], v34 offset:9280
	ds_read_b128 v[148:151], v34 offset:11584
	s_waitcnt lgkmcnt(10)
	v_mfma_f32_16x16x32_bf16 v[40:43], v[36:39], v[40:43], 0
	s_ashr_i32 s29, s28, 31
	s_lshl_b64 s[26:27], s[28:29], 13
	s_add_u32 s2, s5, s26
	s_waitcnt lgkmcnt(9)
	v_mfma_f32_16x16x32_bf16 v[36:39], v[36:39], v[44:47], 0
	s_addc_u32 s3, s7, s27
	s_add_u32 vcc_lo, s0, s26
	s_addc_u32 vcc_hi, s33, s27
	s_waitcnt lgkmcnt(6)
	v_mfma_f32_16x16x32_bf16 v[36:39], v[48:51], v[56:59], v[36:39]
	v_mfma_f32_16x16x32_bf16 v[40:43], v[48:51], v[52:55], v[40:43]
	s_waitcnt lgkmcnt(4)
	v_mfma_f32_16x16x32_bf16 v[44:47], v[60:63], v[64:67], 0
	s_nop 4
	v_cvt_pk_bf16_f32 v36, v36, v37
	v_cvt_pk_bf16_f32 v37, v38, v39
	v_cvt_pk_bf16_f32 v40, v40, v41
	v_cvt_pk_bf16_f32 v41, v42, v43
	ds_write_b64 v125, v[36:37]
	s_waitcnt lgkmcnt(2)
	v_mfma_f32_16x16x32_bf16 v[36:39], v[82:85], v[144:147], v[44:47]
	ds_write_b64 v124, v[40:41]
	v_mfma_f32_16x16x32_bf16 v[40:43], v[60:63], v[78:81], 0
	s_nop 5
	v_cvt_pk_bf16_f32 v36, v36, v37
	v_cvt_pk_bf16_f32 v37, v38, v39
	ds_write_b64 v99, v[36:37]
	s_waitcnt lgkmcnt(3)
	v_mfma_f32_16x16x32_bf16 v[36:39], v[82:85], v[148:151], v[40:43]
	s_nop 7
	v_cvt_pk_bf16_f32 v36, v36, v37
	v_cvt_pk_bf16_f32 v37, v38, v39
	ds_write_b64 v99, v[36:37] offset:2304
	s_waitcnt lgkmcnt(0)
	s_barrier
; #define LAS __attribute__((address_space(3)))
; DI unsigned pk2(float a, float b) { f32x2 v = {a, b}; bf16x2_t r = __builtin_convertvector(v, bf16x2_t); return __builtin_bit_cast(unsigned, r); }
; DI void ck_wr_tr(LAS bf16* XT, int m, int n, f32x4 v) { *(LAS u32x2*)(XT + n * CP + m) = (u32x2){pk2(v[0], v[1]), pk2(v[2], v[3])}; }
; DI void phase_chunkA(const Args& a, LAS unsigned char* lds, int wave, int lane, int tid, int bid, int G) {
;     ...
;         { bf16* Pg = (bf16*)(ws + CH_P) + (size_t)cid * 4096; bf16* Rg = (bf16*)(ws + CH_RH) + (size_t)cid * 4096;
;           auto e13 = [&](int m, int n, f32x4 v) { ck_wr_tr(SL(13), m, n, v); };
;           auto eP = [&](int m, int n, f32x4 v) { const float gc = gC[n];
; #pragma unroll
;               for (int g = 0; g < 4; ++g) v[g] = gc * (((m + g == n) ? 1.f : 0.f) + v[g]);
;               *(u32x2*)(Pg + n * 64 + m) = (u32x2){pk2(v[0], v[1]), pk2(v[2], v[3])}; };
;           auto eR = [&](int m, int n, f32x4 v) { const u32x2 o = *(const LAS u32x2*)(SL(6) + n * CP + m);
;               v[0] += bflo(o.x); v[1] += bfhi(o.x); v[2] += bflo(o.y); v[3] += bfhi(o.y);
;               *(u32x2*)(Rg + n * 64 + m) = (u32x2){pk2(v[0], v[1]), pk2(v[2], v[3])}; };
;           CK_RUN3(SL(4), SL(12), e13, SL(0), SL(3), eP, SL(0), SL(10), eR); }
	ds_read_b128 v[36:39], v97 offset:36864
	ds_read_b128 v[40:43], v97 offset:36928
	ds_read_b128 v[44:47], v35
	ds_read_b128 v[48:51], v35 offset:64
	ds_read_b128 v[52:55], v35 offset:2304
	ds_read_b128 v[56:59], v35 offset:2368
	ds_read_b128 v[60:63], v97
	ds_read_b128 v[64:67], v97 offset:64
	ds_read_b128 v[78:81], v34 offset:27648
	ds_read_b128 v[82:85], v34 offset:27712
	ds_read_b128 v[144:147], v34 offset:29952
	ds_read_b128 v[148:151], v34 offset:30016
	v_add_u32_e32 v35, v100, v98
	ds_read_b128 v[152:155], v35
	ds_read_b128 v[156:159], v35 offset:64
	ds_read_b128 v[160:163], v35 offset:2304
	ds_read_b128 v[172:175], v35 offset:2368
	s_waitcnt lgkmcnt(13)
	v_mfma_f32_16x16x32_bf16 v[44:47], v[36:39], v[44:47], 0
	v_lshlrev_b32_e32 v90, 1, v72
	s_waitcnt lgkmcnt(11)
	v_mfma_f32_16x16x32_bf16 v[36:39], v[36:39], v[52:55], 0
	v_lshlrev_b64 v[52:53], 1, v[70:71]
	v_mfma_f32_16x16x32_bf16 v[44:47], v[40:43], v[48:51], v[44:47]
	s_waitcnt lgkmcnt(10)
	v_mfma_f32_16x16x32_bf16 v[36:39], v[40:43], v[56:59], v[36:39]
	s_waitcnt lgkmcnt(7)
	v_mfma_f32_16x16x32_bf16 v[40:43], v[60:63], v[78:81], 0
	s_nop 3
	v_cvt_pk_bf16_f32 v44, v44, v45
	v_cvt_pk_bf16_f32 v45, v46, v47
	v_cvt_pk_bf16_f32 v36, v36, v37
	v_cvt_pk_bf16_f32 v37, v38, v39
	ds_write_b64 v122, v[44:45]
	ds_write_b64 v123, v[36:37]
	ds_read_b32 v44, v130
	s_waitcnt lgkmcnt(9)
	v_mfma_f32_16x16x32_bf16 v[36:39], v[64:67], v[82:85], v[40:43]
	ds_read_b32 v54, v135
	ds_read_b64 v[48:49], v140 offset:55296
	ds_read_b64 v[50:51], v121 offset:55296
	v_lshl_add_u64 v[42:43], s[2:3], 0, v[90:91]
	v_lshl_add_u64 v[42:43], v[42:43], 0, v[52:53]
	s_nop 2
	v_add_f32_e32 v36, v131, v36
	v_add_f32_e32 v37, v132, v37
	v_add_f32_e32 v38, v133, v38
	v_add_f32_e32 v39, v134, v39
	s_waitcnt lgkmcnt(3)
	v_mul_f32_e32 v36, v36, v44
	v_mul_f32_e32 v37, v37, v44
	v_mul_f32_e32 v38, v38, v44
	v_mul_f32_e32 v39, v39, v44
	v_cvt_pk_bf16_f32 v40, v36, v37
	v_cvt_pk_bf16_f32 v41, v38, v39
	v_mfma_f32_16x16x32_bf16 v[36:39], v[60:63], v[144:147], 0
	global_store_dwordx2 v[42:43], v[40:41], off
	v_mfma_f32_16x16x32_bf16 v[36:39], v[64:67], v[148:151], v[36:39]
	v_mfma_f32_16x16x32_bf16 v[40:43], v[60:63], v[152:155], 0
	v_mfma_f32_16x16x32_bf16 v[44:47], v[60:63], v[160:163], 0
	s_nop 5
	v_add_f32_e32 v36, v136, v36
	s_waitcnt lgkmcnt(2)
	v_mul_f32_e32 v55, v36, v54
	v_add_f32_e32 v36, v137, v37
	v_mul_f32_e32 v56, v36, v54
	v_add_f32_e32 v36, v138, v38
	v_add_f32_e32 v58, v139, v39
	v_mul_f32_e32 v57, v36, v54
	v_mfma_f32_16x16x32_bf16 v[36:39], v[64:67], v[156:159], v[40:43]
	s_nop 2
	v_mul_f32_e32 v40, v58, v54
	v_cvt_pk_bf16_f32 v54, v55, v56
	v_cvt_pk_bf16_f32 v55, v57, v40
	v_mfma_f32_16x16x32_bf16 v[40:43], v[64:67], v[172:175], v[44:47]
	s_nop 2
	v_lshlrev_b32_e32 v44, 1, v74
	v_mov_b32_e32 v45, v91
	v_lshl_add_u64 v[46:47], s[2:3], 0, v[44:45]
	v_lshl_add_u64 v[46:47], v[46:47], 0, v[52:53]
	global_store_dwordx2 v[46:47], v[54:55], off
	s_waitcnt lgkmcnt(0)
	v_lshlrev_b32_e32 v46, 16, v50
	v_and_b32_e32 v47, 0xffff0000, v50
	v_pk_add_f32 v[36:37], v[36:37], v[46:47]
	v_lshlrev_b32_e32 v46, 16, v51
	v_and_b32_e32 v47, 0xffff0000, v51
	v_pk_add_f32 v[38:39], v[38:39], v[46:47]
	v_cvt_pk_bf16_f32 v36, v36, v37
	v_cvt_pk_bf16_f32 v37, v38, v39
	v_lshl_add_u64 v[38:39], vcc, 0, v[90:91]
	v_lshl_add_u64 v[38:39], v[38:39], 0, v[52:53]
	global_store_dwordx2 v[38:39], v[36:37], off
	v_lshlrev_b32_e32 v36, 16, v48
	v_and_b32_e32 v37, 0xffff0000, v48
	v_lshlrev_b32_e32 v38, 16, v49
	v_and_b32_e32 v39, 0xffff0000, v49
	v_pk_add_f32 v[36:37], v[40:41], v[36:37]
	v_pk_add_f32 v[38:39], v[42:43], v[38:39]
	v_cvt_pk_bf16_f32 v36, v36, v37
	v_cvt_pk_bf16_f32 v37, v38, v39
	v_lshl_add_u64 v[38:39], vcc, 0, v[44:45]
	v_lshl_add_u64 v[38:39], v[38:39], 0, v[52:53]
	global_store_dwordx2 v[38:39], v[36:37], off
	s_waitcnt lgkmcnt(0)
	s_barrier
; DI void phase_chunkA(const Args& a, LAS unsigned char* lds, int wave, int lane, int tid, int bid, int G) {
;     ...
;         { float* Qg = (float*)(ws + CH_Q) + (size_t)cid * 4096; float* Yg = (float*)(ws + CH_YL) + (size_t)cid * 4096;
;           CkF f1, f2, f3, f4; ck_ld(f1, SL(13), SL(3), wave, lane); ck_ld(f2, SL(7), SL(5), wave, lane); ck_ld(f3, SL(13), SL(10), wave, lane); ck_ld(f4, SL(7), SL(11), wave, lane); __builtin_amdgcn_sched_barrier(0);
;           f32x4 cq[2] = CK_Z2, cy[2] = CK_Z2; ck_mma(cq, f1); ck_mma(cq, f2); ck_mma(cy, f3); ck_mma(cy, f4);
;           ck_epi(cq, wave, lane, [&](int m, int n, f32x4 v) { *(f32x4*)(Qg + n * 64 + m) = v * gC[n]; });
;           ck_epi(cy, wave, lane, [&](int m, int n, f32x4 v) { *(f32x4*)(Yg + n * 64 + m) = v; }); }
	ds_read_b128 v[36:39], v119
	ds_read_b128 v[40:43], v119 offset:64
	ds_read_b128 v[44:47], v34 offset:27648
	ds_read_b128 v[48:51], v34 offset:27712
	ds_read_b128 v[52:55], v34 offset:29952
	ds_read_b128 v[56:59], v34 offset:30016
	ds_read_b128 v[60:63], v97 offset:64512
	ds_read_b128 v[64:67], v97 offset:64576
	ds_read_b128 v[78:81], v34 offset:46080
	ds_read_b128 v[82:85], v34 offset:46144
	ds_read_b128 v[144:147], v34 offset:48384
	ds_read_b128 v[148:151], v34 offset:48448
	ds_read_b128 v[152:155], v35
	ds_read_b128 v[156:159], v35 offset:64
	ds_read_b128 v[160:163], v35 offset:2304
	ds_read_b128 v[172:175], v35 offset:2368
	ds_read_b128 v[176:179], v142
	ds_read_b128 v[180:183], v142 offset:64
	ds_read_b128 v[184:187], v142 offset:2304
	ds_read_b128 v[188:191], v142 offset:2368
	s_lshl_b64 s[2:3], s[28:29], 14
	s_add_u32 s26, s1, s2
	s_addc_u32 s27, s24, s3
	s_waitcnt lgkmcnt(14)
	v_mfma_f32_16x16x32_bf16 v[44:47], v[36:39], v[44:47], 0
	v_lshlrev_b32_e32 v90, 2, v72
	s_mov_b32 s28, s25
	v_mfma_f32_16x16x32_bf16 v[44:47], v[40:43], v[48:51], v[44:47]
	v_mfma_f32_16x16x32_bf16 v[52:55], v[36:39], v[52:55], 0
	s_waitcnt lgkmcnt(11)
	v_mfma_f32_16x16x32_bf16 v[44:47], v[60:63], v[78:81], v[44:47]
	v_mfma_f32_16x16x32_bf16 v[48:51], v[40:43], v[56:59], v[52:55]
	ds_read_b32 v34, v130
	ds_read_b32 v56, v135
	v_lshlrev_b64 v[58:59], 2, v[70:71]
	s_waitcnt lgkmcnt(12)
	v_mfma_f32_16x16x32_bf16 v[44:47], v[64:67], v[82:85], v[44:47]
	s_waitcnt lgkmcnt(9)
	v_mfma_f32_16x16x32_bf16 v[52:55], v[36:39], v[152:155], 0
	s_waitcnt lgkmcnt(8)
	v_mfma_f32_16x16x32_bf16 v[52:55], v[40:43], v[156:159], v[52:55]
	s_waitcnt lgkmcnt(1)
	s_nop 2
	v_pk_mul_f32 v[46:47], v[46:47], v[34:35] op_sel_hi:[1,0]
	v_pk_mul_f32 v[44:45], v[44:45], v[34:35] op_sel_hi:[1,0]
	v_mfma_f32_16x16x32_bf16 v[34:37], v[36:39], v[160:163], 0
	v_lshl_add_u64 v[38:39], s[26:27], 0, v[90:91]
	v_lshl_add_u64 v[38:39], v[38:39], 0, v[58:59]
	v_lshlrev_b32_e32 v90, 2, v74
	v_mfma_f32_16x16x32_bf16 v[48:51], v[60:63], v[144:147], v[48:51]
	global_store_dwordx4 v[38:39], v[44:47], off
	v_lshl_add_u64 v[38:39], s[26:27], 0, v[90:91]
	v_mfma_f32_16x16x32_bf16 v[34:37], v[40:43], v[172:175], v[34:37]
	v_lshl_add_u64 v[42:43], v[38:39], 0, v[58:59]
	v_mfma_f32_16x16x32_bf16 v[38:41], v[60:63], v[176:179], v[52:55]
	v_mfma_f32_16x16x32_bf16 v[48:51], v[64:67], v[148:151], v[48:51]
	s_waitcnt vmcnt(5)
	s_nop 0
	v_mov_b32_e32 v52, v32
	v_mov_b32_e32 v53, v33
	v_mfma_f32_16x16x32_bf16 v[34:37], v[60:63], v[184:187], v[34:37]
	v_mfma_f32_16x16x32_bf16 v[38:41], v[64:67], v[180:183], v[38:41]
	s_waitcnt lgkmcnt(0)
	s_nop 0
	v_pk_mul_f32 v[46:47], v[50:51], v[56:57] op_sel_hi:[1,0]
	v_pk_mul_f32 v[44:45], v[48:49], v[56:57] op_sel_hi:[1,0]
	global_store_dwordx4 v[42:43], v[44:47], off
	v_lshl_add_u64 v[42:43], v[76:77], 0, s[2:3]
	v_mfma_f32_16x16x32_bf16 v[34:37], v[64:67], v[188:191], v[34:37]
	v_lshl_add_u64 v[42:43], v[42:43], 0, v[58:59]
	global_store_dwordx4 v[42:43], v[38:41], off
	v_mov_b64_e32 v[60:61], v[12:13]
	v_mov_b64_e32 v[56:57], v[8:9]
	v_add_co_u32_e32 v38, vcc, 0x1000, v42
	v_mov_b64_e32 v[48:49], v[28:29]
	s_nop 0
	v_addc_co_u32_e32 v39, vcc, 0, v43, vcc
	global_store_dwordx4 v[38:39], v[34:37], off
	v_mov_b64_e32 v[40:41], v[20:21]
	v_mov_b64_e32 v[44:45], v[24:25]
	v_mov_b64_e32 v[36:37], v[16:17]
	s_andn2_b64 vcc, exec, s[96:97]
	v_mov_b64_e32 v[58:59], v[10:11]
	v_mov_b64_e32 v[54:55], v[6:7]
	v_mov_b64_e32 v[34:35], v[14:15]
	v_mov_b64_e32 v[38:39], v[18:19]
	v_mov_b64_e32 v[42:43], v[22:23]
	v_mov_b64_e32 v[46:47], v[26:27]
	v_mov_b32_e32 v50, v30
	v_mov_b32_e32 v51, v31
	s_cbranch_vccz .LBB0_1041

; DI unsigned pk2(float a, float b) { f32x2 v = {a, b}; bf16x2_t r = __builtin_convertvector(v, bf16x2_t); return __builtin_bit_cast(unsigned, r); }
; DI float sigmoidf_(float x) { return 1.f / (1.f + __expf(-x)); }
;     DI void operator()(const f32x4 (&acc)[2][2][4][2], const Unit& u, int wr, int wc, int fr, int fq) const {
;         const int row0 = u.pm * BM + wr * 64 + fr, col0 = u.pn * BM + wc * 32 + 8 * fq;
; #pragma unroll
;         for (int ai = 0; ai < 2; ++ai)
; #pragma unroll
;             for (int m = 0; m < 4; ++m) { const size_t row = (size_t)(row0 + ai * HALF + m * 16);
;                 u32x4 gzs[2], ts[2];
; #pragma unroll
;                 for (int bj = 0; bj < 2; ++bj) { const int col = col0 + bj * HALF; gzs[bj] = *(const u32x4*)(Zg + row * NZ + goff + col); if (add) ts[bj] = *(const u32x4*)(add + row * D + col); else ts[bj] = (u32x4){0u, 0u, 0u, 0u}; }
; #pragma unroll
;                 for (int bj = 0; bj < 2; ++bj) {
;                     const int col = col0 + bj * HALF;
;                     const u32x4 gz = gzs[bj];
;                     float a[8] = {0.f, 0.f, 0.f, 0.f, 0.f, 0.f, 0.f, 0.f};
;                     if (add) { const u32x4 t = ts[bj]; a[0] = bflo(t.x); a[1] = bfhi(t.x); a[2] = bflo(t.y); a[3] = bfhi(t.y); a[4] = bflo(t.z); a[5] = bfhi(t.z); a[6] = bflo(t.w); a[7] = bfhi(t.w); }
;                     const f32x4 v0 = acc[ai][bj][m][0], v1 = acc[ai][bj][m][1];
;                     float o[8];
;                     o[0] = a[0] + sigmoidf_(bflo(gz.x)) * v0[0]; o[1] = a[1] + sigmoidf_(bfhi(gz.x)) * v0[1];
;                     o[2] = a[2] + sigmoidf_(bflo(gz.y)) * v0[2]; o[3] = a[3] + sigmoidf_(bfhi(gz.y)) * v0[3];
;                     o[4] = a[4] + sigmoidf_(bflo(gz.z)) * v1[0]; o[5] = a[5] + sigmoidf_(bfhi(gz.z)) * v1[1];
;                     o[6] = a[6] + sigmoidf_(bflo(gz.w)) * v1[2]; o[7] = a[7] + sigmoidf_(bfhi(gz.w)) * v1[3];
;                     u32x4 w; w.x = pk2(o[0], o[1]); w.y = pk2(o[2], o[3]); w.z = pk2(o[4], o[5]); w.w = pk2(o[6], o[7]);
;                     *(u32x4*)(O + row * D + col) = w; } }
.LBB0_1405:
	v_lshl_or_b32 v128, s0, 8, v161
	v_lshl_add_u32 v152, s12, 8, v159
	v_mov_b64_e32 v[154:155], s[40:41]
	v_ashrrev_i32_e32 v129, 31, v128
	v_mad_i64_i32 v[130:131], s[0:1], v152, s15, v[154:155]
	v_lshlrev_b64 v[150:151], 1, v[128:129]
	v_lshl_add_u64 v[128:129], v[130:131], 0, v[150:151]
	global_load_dwordx4 v[136:139], v[128:129], off offset:3072
	s_nop 0
	global_load_dwordx4 v[128:131], v[128:129], off offset:3328
	v_ashrrev_i32_e32 v153, 31, v152
	v_lshlrev_b64 v[156:157], 12, v[152:153]
	s_mov_b64 s[2:3], -1
	s_waitcnt vmcnt(0)
	v_lshlrev_b32_e32 v153, 16, v136
	v_and_b32_e32 v136, 0xffff0000, v136
	v_mul_f32_e32 v153, 0xbfb8aa3b, v153
	v_mul_f32_e32 v136, 0xbfb8aa3b, v136
	v_exp_f32_e32 v164, v153
	v_exp_f32_e32 v165, v136
	s_nop 0
	v_pk_add_f32 v[164:165], v[164:165], 1.0 op_sel_hi:[1,0]
	s_nop 0
	v_rcp_f32_e32 v165, v165
	v_rcp_f32_e32 v164, v164
	v_lshlrev_b32_e32 v136, 16, v137
	v_and_b32_e32 v137, 0xffff0000, v137
	v_mul_f32_e32 v136, 0xbfb8aa3b, v136
	v_mul_f32_e32 v137, 0xbfb8aa3b, v137
	v_exp_f32_e32 v136, v136
	v_exp_f32_e32 v137, v137
	v_pk_fma_f32 v[132:133], v[132:133], v[164:165], 0 op_sel_hi:[1,1,0]
	v_pk_add_f32 v[136:137], v[136:137], 1.0 op_sel_hi:[1,0]
	s_nop 0
	v_cvt_pk_bf16_f32 v132, v132, v133
	v_rcp_f32_e32 v137, v137
	v_rcp_f32_e32 v136, v136
	s_nop 0
	v_pk_fma_f32 v[134:135], v[134:135], v[136:137], 0 op_sel_hi:[1,1,0]
	v_lshlrev_b32_e32 v136, 16, v138
	v_and_b32_e32 v137, 0xffff0000, v138
	v_mul_f32_e32 v136, 0xbfb8aa3b, v136
	v_mul_f32_e32 v137, 0xbfb8aa3b, v137
	v_exp_f32_e32 v136, v136
	v_exp_f32_e32 v137, v137
	v_cvt_pk_bf16_f32 v133, v134, v135
	v_pk_add_f32 v[136:137], v[136:137], 1.0 op_sel_hi:[1,0]
	s_nop 0
	v_rcp_f32_e32 v137, v137
	v_rcp_f32_e32 v136, v136
	s_nop 0
	v_pk_fma_f32 v[124:125], v[124:125], v[136:137], 0 op_sel_hi:[1,1,0]
	v_lshlrev_b32_e32 v136, 16, v139
	v_and_b32_e32 v137, 0xffff0000, v139
	v_mul_f32_e32 v136, 0xbfb8aa3b, v136
	v_mul_f32_e32 v137, 0xbfb8aa3b, v137
	v_exp_f32_e32 v136, v136
	v_exp_f32_e32 v137, v137
	v_cvt_pk_bf16_f32 v134, v124, v125
	v_lshl_add_u64 v[124:125], s[8:9], 0, v[156:157]
	v_lshl_add_u64 v[124:125], v[124:125], 0, v[150:151]
	v_pk_add_f32 v[136:137], v[136:137], 1.0 op_sel_hi:[1,0]
	s_nop 0
	v_rcp_f32_e32 v137, v137
	v_rcp_f32_e32 v136, v136
	s_nop 0
	v_pk_fma_f32 v[126:127], v[126:127], v[136:137], 0 op_sel_hi:[1,1,0]
	s_nop 0
	v_cvt_pk_bf16_f32 v135, v126, v127
	v_lshlrev_b32_e32 v126, 16, v128
	v_and_b32_e32 v127, 0xffff0000, v128
	v_mul_f32_e32 v126, 0xbfb8aa3b, v126
	v_mul_f32_e32 v127, 0xbfb8aa3b, v127
	v_exp_f32_e32 v126, v126
	v_exp_f32_e32 v127, v127
	global_store_dwordx4 v[124:125], v[132:135], off
	v_pk_add_f32 v[126:127], v[126:127], 1.0 op_sel_hi:[1,0]
	s_nop 0
	v_rcp_f32_e32 v127, v127
	v_rcp_f32_e32 v126, v126
	s_nop 0
	v_pk_fma_f32 v[120:121], v[120:121], v[126:127], 0 op_sel_hi:[1,1,0]
	v_lshlrev_b32_e32 v126, 16, v129
	v_and_b32_e32 v127, 0xffff0000, v129
	v_mul_f32_e32 v126, 0xbfb8aa3b, v126
	v_mul_f32_e32 v127, 0xbfb8aa3b, v127
	v_exp_f32_e32 v126, v126
	v_exp_f32_e32 v127, v127
	s_nop 0
	v_pk_add_f32 v[126:127], v[126:127], 1.0 op_sel_hi:[1,0]
	s_nop 0
	v_rcp_f32_e32 v127, v127
	v_rcp_f32_e32 v126, v126
	s_nop 0
	v_pk_fma_f32 v[122:123], v[122:123], v[126:127], 0 op_sel_hi:[1,1,0]
	v_lshlrev_b32_e32 v126, 16, v130
	v_and_b32_e32 v127, 0xffff0000, v130
	v_mul_f32_e32 v126, 0xbfb8aa3b, v126
	v_mul_f32_e32 v127, 0xbfb8aa3b, v127
	v_exp_f32_e32 v126, v126
	v_exp_f32_e32 v127, v127
	s_nop 0
	v_pk_add_f32 v[126:127], v[126:127], 1.0 op_sel_hi:[1,0]
	s_nop 0
	v_rcp_f32_e32 v127, v127
	v_rcp_f32_e32 v126, v126
	s_nop 0
	v_pk_fma_f32 v[126:127], v[116:117], v[126:127], 0 op_sel_hi:[1,1,0]
	v_lshlrev_b32_e32 v116, 16, v131
	v_and_b32_e32 v117, 0xffff0000, v131
	v_mul_f32_e32 v116, 0xbfb8aa3b, v116
	v_mul_f32_e32 v117, 0xbfb8aa3b, v117
	v_exp_f32_e32 v116, v116
	v_exp_f32_e32 v117, v117
	s_nop 0
	v_pk_add_f32 v[116:117], v[116:117], 1.0 op_sel_hi:[1,0]
	s_nop 0
	v_rcp_f32_e32 v117, v117
	v_rcp_f32_e32 v116, v116
	s_nop 0
	v_pk_fma_f32 v[128:129], v[118:119], v[116:117], 0 op_sel_hi:[1,1,0]
	v_cvt_pk_bf16_f32 v116, v120, v121
	v_cvt_pk_bf16_f32 v117, v122, v123
	v_cvt_pk_bf16_f32 v118, v126, v127
	v_cvt_pk_bf16_f32 v119, v128, v129
	global_store_dwordx4 v[124:125], v[116:119], off offset:256
	s_nop 1
	v_or_b32_e32 v116, 16, v152
	v_ashrrev_i32_e32 v117, 31, v116
	v_mad_i64_i32 v[118:119], s[0:1], v116, s15, v[154:155]
	v_lshlrev_b64 v[124:125], 12, v[116:117]
	v_lshl_add_u64 v[116:117], v[118:119], 0, v[150:151]
	global_load_dwordx4 v[120:123], v[116:117], off offset:3072
	s_nop 0
	global_load_dwordx4 v[116:119], v[116:117], off offset:3328
	s_waitcnt vmcnt(1)
	v_lshlrev_b32_e32 v126, 16, v120
	v_and_b32_e32 v120, 0xffff0000, v120
	v_mul_f32_e32 v126, 0xbfb8aa3b, v126
	v_mul_f32_e32 v120, 0xbfb8aa3b, v120
	v_exp_f32_e32 v126, v126
	v_exp_f32_e32 v127, v120
	s_nop 0
	v_pk_add_f32 v[126:127], v[126:127], 1.0 op_sel_hi:[1,0]
	s_nop 0
	v_rcp_f32_e32 v127, v127
	v_rcp_f32_e32 v126, v126
	v_lshlrev_b32_e32 v120, 16, v121
	v_and_b32_e32 v121, 0xffff0000, v121
	v_mul_f32_e32 v120, 0xbfb8aa3b, v120
	v_mul_f32_e32 v121, 0xbfb8aa3b, v121
	v_exp_f32_e32 v120, v120
	v_exp_f32_e32 v121, v121
	v_pk_fma_f32 v[112:113], v[112:113], v[126:127], 0 op_sel_hi:[1,1,0]
	v_pk_add_f32 v[120:121], v[120:121], 1.0 op_sel_hi:[1,0]
	s_nop 0
	v_rcp_f32_e32 v121, v121
	v_rcp_f32_e32 v120, v120
	s_nop 0
	v_pk_fma_f32 v[114:115], v[114:115], v[120:121], 0 op_sel_hi:[1,1,0]
	v_lshlrev_b32_e32 v120, 16, v122
	v_and_b32_e32 v121, 0xffff0000, v122
	v_mul_f32_e32 v120, 0xbfb8aa3b, v120
	v_mul_f32_e32 v121, 0xbfb8aa3b, v121
	v_exp_f32_e32 v120, v120
	v_exp_f32_e32 v121, v121
	s_nop 0
	v_pk_add_f32 v[120:121], v[120:121], 1.0 op_sel_hi:[1,0]
	s_nop 0
	v_rcp_f32_e32 v121, v121
	v_rcp_f32_e32 v120, v120
	s_nop 0
	v_pk_fma_f32 v[108:109], v[108:109], v[120:121], 0 op_sel_hi:[1,1,0]
	v_lshlrev_b32_e32 v120, 16, v123
	v_and_b32_e32 v121, 0xffff0000, v123
	v_mul_f32_e32 v120, 0xbfb8aa3b, v120
	v_mul_f32_e32 v121, 0xbfb8aa3b, v121
	v_exp_f32_e32 v120, v120
	v_exp_f32_e32 v121, v121
	s_nop 0
	v_pk_add_f32 v[120:121], v[120:121], 1.0 op_sel_hi:[1,0]
	s_nop 0
	v_rcp_f32_e32 v121, v121
	v_rcp_f32_e32 v120, v120
	s_nop 0
	v_pk_fma_f32 v[120:121], v[110:111], v[120:121], 0 op_sel_hi:[1,1,0]
	v_cvt_pk_bf16_f32 v110, v112, v113
	v_cvt_pk_bf16_f32 v112, v108, v109
	v_lshl_add_u64 v[108:109], s[8:9], 0, v[124:125]
	v_cvt_pk_bf16_f32 v111, v114, v115
	v_cvt_pk_bf16_f32 v113, v120, v121
	v_lshl_add_u64 v[108:109], v[108:109], 0, v[150:151]
	global_store_dwordx4 v[108:109], v[110:113], off
	s_waitcnt vmcnt(1)
; DI unsigned pk2(float a, float b) { f32x2 v = {a, b}; bf16x2_t r = __builtin_convertvector(v, bf16x2_t); return __builtin_bit_cast(unsigned, r); }
; DI float sigmoidf_(float x) { return 1.f / (1.f + __expf(-x)); }
;     DI void operator()(const f32x4 (&acc)[2][2][4][2], const Unit& u, int wr, int wc, int fr, int fq) const {
;         const int row0 = u.pm * BM + wr * 64 + fr, col0 = u.pn * BM + wc * 32 + 8 * fq;
; #pragma unroll
;         for (int ai = 0; ai < 2; ++ai)
; #pragma unroll
;             for (int m = 0; m < 4; ++m) { const size_t row = (size_t)(row0 + ai * HALF + m * 16);
;                 u32x4 gzs[2], ts[2];
; #pragma unroll
;                 for (int bj = 0; bj < 2; ++bj) { const int col = col0 + bj * HALF; gzs[bj] = *(const u32x4*)(Zg + row * NZ + goff + col); if (add) ts[bj] = *(const u32x4*)(add + row * D + col); else ts[bj] = (u32x4){0u, 0u, 0u, 0u}; }
; #pragma unroll
;                 for (int bj = 0; bj < 2; ++bj) {
;                     const int col = col0 + bj * HALF;
;                     const u32x4 gz = gzs[bj];
;                     float a[8] = {0.f, 0.f, 0.f, 0.f, 0.f, 0.f, 0.f, 0.f};
;                     if (add) { const u32x4 t = ts[bj]; a[0] = bflo(t.x); a[1] = bfhi(t.x); a[2] = bflo(t.y); a[3] = bfhi(t.y); a[4] = bflo(t.z); a[5] = bfhi(t.z); a[6] = bflo(t.w); a[7] = bfhi(t.w); }
;                     const f32x4 v0 = acc[ai][bj][m][0], v1 = acc[ai][bj][m][1];
;                     float o[8];
;                     o[0] = a[0] + sigmoidf_(bflo(gz.x)) * v0[0]; o[1] = a[1] + sigmoidf_(bfhi(gz.x)) * v0[1];
;                     o[2] = a[2] + sigmoidf_(bflo(gz.y)) * v0[2]; o[3] = a[3] + sigmoidf_(bfhi(gz.y)) * v0[3];
;                     o[4] = a[4] + sigmoidf_(bflo(gz.z)) * v1[0]; o[5] = a[5] + sigmoidf_(bfhi(gz.z)) * v1[1];
;                     o[6] = a[6] + sigmoidf_(bflo(gz.w)) * v1[2]; o[7] = a[7] + sigmoidf_(bfhi(gz.w)) * v1[3];
;                     u32x4 w; w.x = pk2(o[0], o[1]); w.y = pk2(o[2], o[3]); w.z = pk2(o[4], o[5]); w.w = pk2(o[6], o[7]);
;                     *(u32x4*)(O + row * D + col) = w; } }
	s_nop 0
	v_lshlrev_b32_e32 v110, 16, v116
	v_and_b32_e32 v111, 0xffff0000, v116
	v_mul_f32_e32 v110, 0xbfb8aa3b, v110
	v_mul_f32_e32 v111, 0xbfb8aa3b, v111
	v_exp_f32_e32 v110, v110
	v_exp_f32_e32 v111, v111
	s_nop 0
	v_pk_add_f32 v[110:111], v[110:111], 1.0 op_sel_hi:[1,0]
	s_nop 0
	v_rcp_f32_e32 v111, v111
	v_rcp_f32_e32 v110, v110
	s_nop 0
	v_pk_fma_f32 v[104:105], v[104:105], v[110:111], 0 op_sel_hi:[1,1,0]
	v_lshlrev_b32_e32 v110, 16, v117
	v_and_b32_e32 v111, 0xffff0000, v117
	v_mul_f32_e32 v110, 0xbfb8aa3b, v110
	v_mul_f32_e32 v111, 0xbfb8aa3b, v111
	v_exp_f32_e32 v110, v110
	v_exp_f32_e32 v111, v111
	s_nop 0
	v_pk_add_f32 v[110:111], v[110:111], 1.0 op_sel_hi:[1,0]
	s_nop 0
	v_rcp_f32_e32 v111, v111
	v_rcp_f32_e32 v110, v110
	s_nop 0
	v_pk_fma_f32 v[106:107], v[106:107], v[110:111], 0 op_sel_hi:[1,1,0]
	v_lshlrev_b32_e32 v110, 16, v118
	v_and_b32_e32 v111, 0xffff0000, v118
	v_mul_f32_e32 v110, 0xbfb8aa3b, v110
	v_mul_f32_e32 v111, 0xbfb8aa3b, v111
	v_exp_f32_e32 v110, v110
	v_exp_f32_e32 v111, v111
	s_nop 0
	v_pk_add_f32 v[110:111], v[110:111], 1.0 op_sel_hi:[1,0]
	s_nop 0
	v_rcp_f32_e32 v111, v111
	v_rcp_f32_e32 v110, v110
	s_nop 0
	v_pk_fma_f32 v[110:111], v[100:101], v[110:111], 0 op_sel_hi:[1,1,0]
	v_lshlrev_b32_e32 v100, 16, v119
	v_and_b32_e32 v101, 0xffff0000, v119
	v_mul_f32_e32 v100, 0xbfb8aa3b, v100
	v_mul_f32_e32 v101, 0xbfb8aa3b, v101
	v_exp_f32_e32 v100, v100
	v_exp_f32_e32 v101, v101
	s_nop 0
	v_pk_add_f32 v[100:101], v[100:101], 1.0 op_sel_hi:[1,0]
	s_nop 0
	v_rcp_f32_e32 v101, v101
	v_rcp_f32_e32 v100, v100
	s_nop 0
	v_pk_fma_f32 v[112:113], v[102:103], v[100:101], 0 op_sel_hi:[1,1,0]
	v_cvt_pk_bf16_f32 v100, v104, v105
	v_cvt_pk_bf16_f32 v101, v106, v107
	v_cvt_pk_bf16_f32 v102, v110, v111
	v_cvt_pk_bf16_f32 v103, v112, v113
	global_store_dwordx4 v[108:109], v[100:103], off offset:256
	s_nop 1
	v_or_b32_e32 v100, 32, v152
	v_ashrrev_i32_e32 v101, 31, v100
	v_mad_i64_i32 v[102:103], s[0:1], v100, s15, v[154:155]
	v_lshlrev_b64 v[108:109], 12, v[100:101]
	v_lshl_add_u64 v[100:101], v[102:103], 0, v[150:151]
	global_load_dwordx4 v[104:107], v[100:101], off offset:3072
	s_nop 0
	global_load_dwordx4 v[100:103], v[100:101], off offset:3328
	s_waitcnt vmcnt(1)
	v_lshlrev_b32_e32 v110, 16, v104
	v_and_b32_e32 v104, 0xffff0000, v104
	v_mul_f32_e32 v110, 0xbfb8aa3b, v110
	v_mul_f32_e32 v104, 0xbfb8aa3b, v104
	v_exp_f32_e32 v110, v110
	v_exp_f32_e32 v111, v104
	s_nop 0
	v_pk_add_f32 v[110:111], v[110:111], 1.0 op_sel_hi:[1,0]
	s_nop 0
	v_rcp_f32_e32 v111, v111
	v_rcp_f32_e32 v110, v110
	v_lshlrev_b32_e32 v104, 16, v105
	v_and_b32_e32 v105, 0xffff0000, v105
	v_mul_f32_e32 v104, 0xbfb8aa3b, v104
	v_mul_f32_e32 v105, 0xbfb8aa3b, v105
	v_exp_f32_e32 v104, v104
	v_exp_f32_e32 v105, v105
	v_pk_fma_f32 v[96:97], v[96:97], v[110:111], 0 op_sel_hi:[1,1,0]
	v_pk_add_f32 v[104:105], v[104:105], 1.0 op_sel_hi:[1,0]
	s_nop 0
	v_rcp_f32_e32 v105, v105
	v_rcp_f32_e32 v104, v104
	s_nop 0
	v_pk_fma_f32 v[98:99], v[98:99], v[104:105], 0 op_sel_hi:[1,1,0]
	v_lshlrev_b32_e32 v104, 16, v106
	v_and_b32_e32 v105, 0xffff0000, v106
	v_mul_f32_e32 v104, 0xbfb8aa3b, v104
	v_mul_f32_e32 v105, 0xbfb8aa3b, v105
	v_exp_f32_e32 v104, v104
	v_exp_f32_e32 v105, v105
	s_nop 0
	v_pk_add_f32 v[104:105], v[104:105], 1.0 op_sel_hi:[1,0]
	s_nop 0
	v_rcp_f32_e32 v105, v105
	v_rcp_f32_e32 v104, v104
	s_nop 0
	v_pk_fma_f32 v[92:93], v[92:93], v[104:105], 0 op_sel_hi:[1,1,0]
	v_lshlrev_b32_e32 v104, 16, v107
	v_and_b32_e32 v105, 0xffff0000, v107
	v_mul_f32_e32 v104, 0xbfb8aa3b, v104
	v_mul_f32_e32 v105, 0xbfb8aa3b, v105
	v_exp_f32_e32 v104, v104
	v_exp_f32_e32 v105, v105
	s_nop 0
	v_pk_add_f32 v[104:105], v[104:105], 1.0 op_sel_hi:[1,0]
	s_nop 0
	v_rcp_f32_e32 v105, v105
	v_rcp_f32_e32 v104, v104
	s_nop 0
	v_pk_fma_f32 v[104:105], v[94:95], v[104:105], 0 op_sel_hi:[1,1,0]
	v_cvt_pk_bf16_f32 v94, v96, v97
	v_cvt_pk_bf16_f32 v96, v92, v93
	v_lshl_add_u64 v[92:93], s[8:9], 0, v[108:109]
	v_cvt_pk_bf16_f32 v95, v98, v99
	v_cvt_pk_bf16_f32 v97, v104, v105
	v_lshl_add_u64 v[92:93], v[92:93], 0, v[150:151]
	global_store_dwordx4 v[92:93], v[94:97], off
	s_waitcnt vmcnt(1)
	s_nop 0
	v_lshlrev_b32_e32 v94, 16, v100
	v_and_b32_e32 v95, 0xffff0000, v100
	v_mul_f32_e32 v94, 0xbfb8aa3b, v94
	v_mul_f32_e32 v95, 0xbfb8aa3b, v95
	v_exp_f32_e32 v94, v94
	v_exp_f32_e32 v95, v95
	s_nop 0
	v_pk_add_f32 v[94:95], v[94:95], 1.0 op_sel_hi:[1,0]
	s_nop 0
	v_rcp_f32_e32 v95, v95
	v_rcp_f32_e32 v94, v94
	s_nop 0
	v_pk_fma_f32 v[86:87], v[86:87], v[94:95], 0 op_sel_hi:[1,1,0]
	v_lshlrev_b32_e32 v94, 16, v101
	v_and_b32_e32 v95, 0xffff0000, v101
	v_mul_f32_e32 v94, 0xbfb8aa3b, v94
	v_mul_f32_e32 v95, 0xbfb8aa3b, v95
	v_exp_f32_e32 v94, v94
	v_exp_f32_e32 v95, v95
	s_nop 0
	v_pk_add_f32 v[94:95], v[94:95], 1.0 op_sel_hi:[1,0]
	s_nop 0
	v_rcp_f32_e32 v95, v95
	v_rcp_f32_e32 v94, v94
	s_nop 0
	v_pk_fma_f32 v[88:89], v[88:89], v[94:95], 0 op_sel_hi:[1,1,0]
	v_lshlrev_b32_e32 v94, 16, v102
	v_and_b32_e32 v95, 0xffff0000, v102
	v_mul_f32_e32 v94, 0xbfb8aa3b, v94
	v_mul_f32_e32 v95, 0xbfb8aa3b, v95
	v_exp_f32_e32 v94, v94
	v_exp_f32_e32 v95, v95
	s_nop 0
	v_pk_add_f32 v[94:95], v[94:95], 1.0 op_sel_hi:[1,0]
	s_nop 0
	v_rcp_f32_e32 v95, v95
	v_rcp_f32_e32 v94, v94
	s_nop 0
	v_pk_fma_f32 v[94:95], v[82:83], v[94:95], 0 op_sel_hi:[1,1,0]
	v_lshlrev_b32_e32 v82, 16, v103
	v_and_b32_e32 v83, 0xffff0000, v103
	v_mul_f32_e32 v82, 0xbfb8aa3b, v82
	v_mul_f32_e32 v83, 0xbfb8aa3b, v83
	v_exp_f32_e32 v82, v82
	v_exp_f32_e32 v83, v83
	s_nop 0
	v_pk_add_f32 v[82:83], v[82:83], 1.0 op_sel_hi:[1,0]
	s_nop 0
	v_rcp_f32_e32 v83, v83
	v_rcp_f32_e32 v82, v82
	s_nop 0
	v_pk_fma_f32 v[96:97], v[84:85], v[82:83], 0 op_sel_hi:[1,1,0]
	v_cvt_pk_bf16_f32 v82, v86, v87
	v_cvt_pk_bf16_f32 v83, v88, v89
	v_cvt_pk_bf16_f32 v84, v94, v95
	v_cvt_pk_bf16_f32 v85, v96, v97
	global_store_dwordx4 v[92:93], v[82:85], off offset:256
	s_nop 1
	v_or_b32_e32 v82, 48, v152
	v_ashrrev_i32_e32 v83, 31, v82
	v_mad_i64_i32 v[84:85], s[0:1], v82, s15, v[154:155]
	v_lshlrev_b64 v[92:93], 12, v[82:83]
	v_lshl_add_u64 v[82:83], v[84:85], 0, v[150:151]
	global_load_dwordx4 v[86:89], v[82:83], off offset:3072
	s_nop 0
	global_load_dwordx4 v[82:85], v[82:83], off offset:3328
	s_waitcnt vmcnt(1)
; DI unsigned pk2(float a, float b) { f32x2 v = {a, b}; bf16x2_t r = __builtin_convertvector(v, bf16x2_t); return __builtin_bit_cast(unsigned, r); }
; DI float sigmoidf_(float x) { return 1.f / (1.f + __expf(-x)); }
;     DI void operator()(const f32x4 (&acc)[2][2][4][2], const Unit& u, int wr, int wc, int fr, int fq) const {
;         const int row0 = u.pm * BM + wr * 64 + fr, col0 = u.pn * BM + wc * 32 + 8 * fq;
; #pragma unroll
;         for (int ai = 0; ai < 2; ++ai)
; #pragma unroll
;             for (int m = 0; m < 4; ++m) { const size_t row = (size_t)(row0 + ai * HALF + m * 16);
;                 u32x4 gzs[2], ts[2];
; #pragma unroll
;                 for (int bj = 0; bj < 2; ++bj) { const int col = col0 + bj * HALF; gzs[bj] = *(const u32x4*)(Zg + row * NZ + goff + col); if (add) ts[bj] = *(const u32x4*)(add + row * D + col); else ts[bj] = (u32x4){0u, 0u, 0u, 0u}; }
; #pragma unroll
;                 for (int bj = 0; bj < 2; ++bj) {
;                     const int col = col0 + bj * HALF;
;                     const u32x4 gz = gzs[bj];
;                     float a[8] = {0.f, 0.f, 0.f, 0.f, 0.f, 0.f, 0.f, 0.f};
;                     if (add) { const u32x4 t = ts[bj]; a[0] = bflo(t.x); a[1] = bfhi(t.x); a[2] = bflo(t.y); a[3] = bfhi(t.y); a[4] = bflo(t.z); a[5] = bfhi(t.z); a[6] = bflo(t.w); a[7] = bfhi(t.w); }
;                     const f32x4 v0 = acc[ai][bj][m][0], v1 = acc[ai][bj][m][1];
;                     float o[8];
;                     o[0] = a[0] + sigmoidf_(bflo(gz.x)) * v0[0]; o[1] = a[1] + sigmoidf_(bfhi(gz.x)) * v0[1];
;                     o[2] = a[2] + sigmoidf_(bflo(gz.y)) * v0[2]; o[3] = a[3] + sigmoidf_(bfhi(gz.y)) * v0[3];
;                     o[4] = a[4] + sigmoidf_(bflo(gz.z)) * v1[0]; o[5] = a[5] + sigmoidf_(bfhi(gz.z)) * v1[1];
;                     o[6] = a[6] + sigmoidf_(bflo(gz.w)) * v1[2]; o[7] = a[7] + sigmoidf_(bfhi(gz.w)) * v1[3];
;                     u32x4 w; w.x = pk2(o[0], o[1]); w.y = pk2(o[2], o[3]); w.z = pk2(o[4], o[5]); w.w = pk2(o[6], o[7]);
;                     *(u32x4*)(O + row * D + col) = w; } }
	v_lshlrev_b32_e32 v94, 16, v86
	v_and_b32_e32 v86, 0xffff0000, v86
	v_mul_f32_e32 v94, 0xbfb8aa3b, v94
	v_mul_f32_e32 v86, 0xbfb8aa3b, v86
	v_exp_f32_e32 v94, v94
	v_exp_f32_e32 v95, v86
	s_nop 0
	v_pk_add_f32 v[94:95], v[94:95], 1.0 op_sel_hi:[1,0]
	s_nop 0
	v_rcp_f32_e32 v95, v95
	v_rcp_f32_e32 v94, v94
	v_lshlrev_b32_e32 v86, 16, v87
	v_and_b32_e32 v87, 0xffff0000, v87
	v_mul_f32_e32 v86, 0xbfb8aa3b, v86
	v_mul_f32_e32 v87, 0xbfb8aa3b, v87
	v_exp_f32_e32 v86, v86
	v_exp_f32_e32 v87, v87
	v_pk_fma_f32 v[78:79], v[78:79], v[94:95], 0 op_sel_hi:[1,1,0]
	v_pk_add_f32 v[86:87], v[86:87], 1.0 op_sel_hi:[1,0]
	s_nop 0
	v_rcp_f32_e32 v87, v87
	v_rcp_f32_e32 v86, v86
	s_nop 0
	v_pk_fma_f32 v[80:81], v[80:81], v[86:87], 0 op_sel_hi:[1,1,0]
	v_lshlrev_b32_e32 v86, 16, v88
	v_and_b32_e32 v87, 0xffff0000, v88
	v_mul_f32_e32 v86, 0xbfb8aa3b, v86
	v_mul_f32_e32 v87, 0xbfb8aa3b, v87
	v_exp_f32_e32 v86, v86
	v_exp_f32_e32 v87, v87
	s_nop 0
	v_pk_add_f32 v[86:87], v[86:87], 1.0 op_sel_hi:[1,0]
	s_nop 0
	v_rcp_f32_e32 v87, v87
	v_rcp_f32_e32 v86, v86
	s_nop 0
	v_pk_fma_f32 v[74:75], v[74:75], v[86:87], 0 op_sel_hi:[1,1,0]
	v_lshlrev_b32_e32 v86, 16, v89
	v_and_b32_e32 v87, 0xffff0000, v89
	v_mul_f32_e32 v86, 0xbfb8aa3b, v86
	v_mul_f32_e32 v87, 0xbfb8aa3b, v87
	v_exp_f32_e32 v86, v86
	v_exp_f32_e32 v87, v87
	s_nop 0
	v_pk_add_f32 v[86:87], v[86:87], 1.0 op_sel_hi:[1,0]
	s_nop 0
	v_rcp_f32_e32 v87, v87
	v_rcp_f32_e32 v86, v86
	s_nop 0
	v_pk_fma_f32 v[86:87], v[76:77], v[86:87], 0 op_sel_hi:[1,1,0]
	v_cvt_pk_bf16_f32 v76, v78, v79
	v_cvt_pk_bf16_f32 v78, v74, v75
	v_lshl_add_u64 v[74:75], s[8:9], 0, v[92:93]
	v_cvt_pk_bf16_f32 v77, v80, v81
	v_cvt_pk_bf16_f32 v79, v86, v87
	v_lshl_add_u64 v[74:75], v[74:75], 0, v[150:151]
	global_store_dwordx4 v[74:75], v[76:79], off
	s_waitcnt vmcnt(1)
	s_nop 0
	v_lshlrev_b32_e32 v76, 16, v82
	v_and_b32_e32 v77, 0xffff0000, v82
	v_mul_f32_e32 v76, 0xbfb8aa3b, v76
	v_mul_f32_e32 v77, 0xbfb8aa3b, v77
	v_exp_f32_e32 v76, v76
	v_exp_f32_e32 v77, v77
	s_nop 0
	v_pk_add_f32 v[76:77], v[76:77], 1.0 op_sel_hi:[1,0]
	s_nop 0
	v_rcp_f32_e32 v77, v77
	v_rcp_f32_e32 v76, v76
	s_nop 0
	v_pk_fma_f32 v[70:71], v[70:71], v[76:77], 0 op_sel_hi:[1,1,0]
	v_lshlrev_b32_e32 v76, 16, v83
	v_and_b32_e32 v77, 0xffff0000, v83
	v_mul_f32_e32 v76, 0xbfb8aa3b, v76
	v_mul_f32_e32 v77, 0xbfb8aa3b, v77
	v_exp_f32_e32 v76, v76
	v_exp_f32_e32 v77, v77
	s_nop 0
	v_pk_add_f32 v[76:77], v[76:77], 1.0 op_sel_hi:[1,0]
	s_nop 0
	v_rcp_f32_e32 v77, v77
	v_rcp_f32_e32 v76, v76
	s_nop 0
	v_pk_fma_f32 v[72:73], v[72:73], v[76:77], 0 op_sel_hi:[1,1,0]
	v_lshlrev_b32_e32 v76, 16, v84
	v_and_b32_e32 v77, 0xffff0000, v84
	v_mul_f32_e32 v76, 0xbfb8aa3b, v76
	v_mul_f32_e32 v77, 0xbfb8aa3b, v77
	v_exp_f32_e32 v76, v76
	v_exp_f32_e32 v77, v77
	s_nop 0
	v_pk_add_f32 v[76:77], v[76:77], 1.0 op_sel_hi:[1,0]
	s_nop 0
	v_rcp_f32_e32 v77, v77
	v_rcp_f32_e32 v76, v76
	s_nop 0
	v_pk_fma_f32 v[76:77], v[66:67], v[76:77], 0 op_sel_hi:[1,1,0]
	v_lshlrev_b32_e32 v66, 16, v85
	v_and_b32_e32 v67, 0xffff0000, v85
	v_mul_f32_e32 v66, 0xbfb8aa3b, v66
	v_mul_f32_e32 v67, 0xbfb8aa3b, v67
	v_exp_f32_e32 v66, v66
	v_exp_f32_e32 v67, v67
	s_nop 0
	v_pk_add_f32 v[66:67], v[66:67], 1.0 op_sel_hi:[1,0]
	s_nop 0
	v_rcp_f32_e32 v67, v67
	v_rcp_f32_e32 v66, v66
	s_nop 0
	v_pk_fma_f32 v[78:79], v[68:69], v[66:67], 0 op_sel_hi:[1,1,0]
	v_cvt_pk_bf16_f32 v66, v70, v71
	v_cvt_pk_bf16_f32 v67, v72, v73
	v_cvt_pk_bf16_f32 v68, v76, v77
	v_cvt_pk_bf16_f32 v69, v78, v79
	global_store_dwordx4 v[74:75], v[66:69], off offset:256
	s_nop 1
	v_add_u32_e32 v66, 0x80, v152
	v_ashrrev_i32_e32 v67, 31, v66
	v_mad_i64_i32 v[68:69], s[0:1], v66, s15, v[154:155]
	v_lshlrev_b64 v[74:75], 12, v[66:67]
	v_lshl_add_u64 v[66:67], v[68:69], 0, v[150:151]
	global_load_dwordx4 v[70:73], v[66:67], off offset:3072
	s_nop 0
	global_load_dwordx4 v[66:69], v[66:67], off offset:3328
	s_waitcnt vmcnt(1)
	v_lshlrev_b32_e32 v76, 16, v70
	v_and_b32_e32 v70, 0xffff0000, v70
	v_mul_f32_e32 v76, 0xbfb8aa3b, v76
	v_mul_f32_e32 v70, 0xbfb8aa3b, v70
	v_exp_f32_e32 v76, v76
	v_exp_f32_e32 v77, v70
	s_nop 0
	v_pk_add_f32 v[76:77], v[76:77], 1.0 op_sel_hi:[1,0]
	s_nop 0
	v_rcp_f32_e32 v77, v77
	v_rcp_f32_e32 v76, v76
	v_lshlrev_b32_e32 v70, 16, v71
	v_and_b32_e32 v71, 0xffff0000, v71
	v_mul_f32_e32 v70, 0xbfb8aa3b, v70
	v_mul_f32_e32 v71, 0xbfb8aa3b, v71
	v_exp_f32_e32 v70, v70
	v_exp_f32_e32 v71, v71
	v_pk_fma_f32 v[62:63], v[62:63], v[76:77], 0 op_sel_hi:[1,1,0]
	v_pk_add_f32 v[70:71], v[70:71], 1.0 op_sel_hi:[1,0]
	s_nop 0
	v_rcp_f32_e32 v71, v71
	v_rcp_f32_e32 v70, v70
	s_nop 0
	v_pk_fma_f32 v[64:65], v[64:65], v[70:71], 0 op_sel_hi:[1,1,0]
	v_lshlrev_b32_e32 v70, 16, v72
	v_and_b32_e32 v71, 0xffff0000, v72
	v_mul_f32_e32 v70, 0xbfb8aa3b, v70
	v_mul_f32_e32 v71, 0xbfb8aa3b, v71
	v_exp_f32_e32 v70, v70
	v_exp_f32_e32 v71, v71
	s_nop 0
	v_pk_add_f32 v[70:71], v[70:71], 1.0 op_sel_hi:[1,0]
	s_nop 0
	v_rcp_f32_e32 v71, v71
	v_rcp_f32_e32 v70, v70
	s_nop 0
	v_pk_fma_f32 v[58:59], v[58:59], v[70:71], 0 op_sel_hi:[1,1,0]
	v_lshlrev_b32_e32 v70, 16, v73
	v_and_b32_e32 v71, 0xffff0000, v73
	v_mul_f32_e32 v70, 0xbfb8aa3b, v70
	v_mul_f32_e32 v71, 0xbfb8aa3b, v71
	v_exp_f32_e32 v70, v70
	v_exp_f32_e32 v71, v71
	s_nop 0
	v_pk_add_f32 v[70:71], v[70:71], 1.0 op_sel_hi:[1,0]
	s_nop 0
	v_rcp_f32_e32 v71, v71
	v_rcp_f32_e32 v70, v70
	s_nop 0
	v_pk_fma_f32 v[70:71], v[60:61], v[70:71], 0 op_sel_hi:[1,1,0]
	v_cvt_pk_bf16_f32 v60, v62, v63
	v_cvt_pk_bf16_f32 v62, v58, v59
	v_lshl_add_u64 v[58:59], s[8:9], 0, v[74:75]
	v_cvt_pk_bf16_f32 v61, v64, v65
	v_cvt_pk_bf16_f32 v63, v70, v71
	v_lshl_add_u64 v[58:59], v[58:59], 0, v[150:151]
	global_store_dwordx4 v[58:59], v[60:63], off
	s_waitcnt vmcnt(1)
; DI unsigned pk2(float a, float b) { f32x2 v = {a, b}; bf16x2_t r = __builtin_convertvector(v, bf16x2_t); return __builtin_bit_cast(unsigned, r); }
; DI float sigmoidf_(float x) { return 1.f / (1.f + __expf(-x)); }
;     DI void operator()(const f32x4 (&acc)[2][2][4][2], const Unit& u, int wr, int wc, int fr, int fq) const {
;         const int row0 = u.pm * BM + wr * 64 + fr, col0 = u.pn * BM + wc * 32 + 8 * fq;
; #pragma unroll
;         for (int ai = 0; ai < 2; ++ai)
; #pragma unroll
;             for (int m = 0; m < 4; ++m) { const size_t row = (size_t)(row0 + ai * HALF + m * 16);
;                 u32x4 gzs[2], ts[2];
; #pragma unroll
;                 for (int bj = 0; bj < 2; ++bj) { const int col = col0 + bj * HALF; gzs[bj] = *(const u32x4*)(Zg + row * NZ + goff + col); if (add) ts[bj] = *(const u32x4*)(add + row * D + col); else ts[bj] = (u32x4){0u, 0u, 0u, 0u}; }
; #pragma unroll
;                 for (int bj = 0; bj < 2; ++bj) {
;                     const int col = col0 + bj * HALF;
;                     const u32x4 gz = gzs[bj];
;                     float a[8] = {0.f, 0.f, 0.f, 0.f, 0.f, 0.f, 0.f, 0.f};
;                     if (add) { const u32x4 t = ts[bj]; a[0] = bflo(t.x); a[1] = bfhi(t.x); a[2] = bflo(t.y); a[3] = bfhi(t.y); a[4] = bflo(t.z); a[5] = bfhi(t.z); a[6] = bflo(t.w); a[7] = bfhi(t.w); }
;                     const f32x4 v0 = acc[ai][bj][m][0], v1 = acc[ai][bj][m][1];
;                     float o[8];
;                     o[0] = a[0] + sigmoidf_(bflo(gz.x)) * v0[0]; o[1] = a[1] + sigmoidf_(bfhi(gz.x)) * v0[1];
;                     o[2] = a[2] + sigmoidf_(bflo(gz.y)) * v0[2]; o[3] = a[3] + sigmoidf_(bfhi(gz.y)) * v0[3];
;                     o[4] = a[4] + sigmoidf_(bflo(gz.z)) * v1[0]; o[5] = a[5] + sigmoidf_(bfhi(gz.z)) * v1[1];
;                     o[6] = a[6] + sigmoidf_(bflo(gz.w)) * v1[2]; o[7] = a[7] + sigmoidf_(bfhi(gz.w)) * v1[3];
;                     u32x4 w; w.x = pk2(o[0], o[1]); w.y = pk2(o[2], o[3]); w.z = pk2(o[4], o[5]); w.w = pk2(o[6], o[7]);
;                     *(u32x4*)(O + row * D + col) = w; } }
	s_nop 0
	v_lshlrev_b32_e32 v60, 16, v66
	v_and_b32_e32 v61, 0xffff0000, v66
	v_mul_f32_e32 v60, 0xbfb8aa3b, v60
	v_mul_f32_e32 v61, 0xbfb8aa3b, v61
	v_exp_f32_e32 v60, v60
	v_exp_f32_e32 v61, v61
	s_nop 0
	v_pk_add_f32 v[60:61], v[60:61], 1.0 op_sel_hi:[1,0]
	s_nop 0
	v_rcp_f32_e32 v61, v61
	v_rcp_f32_e32 v60, v60
	s_nop 0
	v_pk_fma_f32 v[54:55], v[54:55], v[60:61], 0 op_sel_hi:[1,1,0]
	v_lshlrev_b32_e32 v60, 16, v67
	v_and_b32_e32 v61, 0xffff0000, v67
	v_mul_f32_e32 v60, 0xbfb8aa3b, v60
	v_mul_f32_e32 v61, 0xbfb8aa3b, v61
	v_exp_f32_e32 v60, v60
	v_exp_f32_e32 v61, v61
	s_nop 0
	v_pk_add_f32 v[60:61], v[60:61], 1.0 op_sel_hi:[1,0]
	s_nop 0
	v_rcp_f32_e32 v61, v61
	v_rcp_f32_e32 v60, v60
	s_nop 0
	v_pk_fma_f32 v[56:57], v[56:57], v[60:61], 0 op_sel_hi:[1,1,0]
	v_lshlrev_b32_e32 v60, 16, v68
	v_and_b32_e32 v61, 0xffff0000, v68
	v_mul_f32_e32 v60, 0xbfb8aa3b, v60
	v_mul_f32_e32 v61, 0xbfb8aa3b, v61
	v_exp_f32_e32 v60, v60
	v_exp_f32_e32 v61, v61
	s_nop 0
	v_pk_add_f32 v[60:61], v[60:61], 1.0 op_sel_hi:[1,0]
	s_nop 0
	v_rcp_f32_e32 v61, v61
	v_rcp_f32_e32 v60, v60
	s_nop 0
	v_pk_fma_f32 v[60:61], v[50:51], v[60:61], 0 op_sel_hi:[1,1,0]
	v_lshlrev_b32_e32 v50, 16, v69
	v_and_b32_e32 v51, 0xffff0000, v69
	v_mul_f32_e32 v50, 0xbfb8aa3b, v50
	v_mul_f32_e32 v51, 0xbfb8aa3b, v51
	v_exp_f32_e32 v50, v50
	v_exp_f32_e32 v51, v51
	s_nop 0
	v_pk_add_f32 v[50:51], v[50:51], 1.0 op_sel_hi:[1,0]
	s_nop 0
	v_rcp_f32_e32 v51, v51
	v_rcp_f32_e32 v50, v50
	s_nop 0
	v_pk_fma_f32 v[62:63], v[52:53], v[50:51], 0 op_sel_hi:[1,1,0]
	v_cvt_pk_bf16_f32 v50, v54, v55
	v_cvt_pk_bf16_f32 v51, v56, v57
	v_cvt_pk_bf16_f32 v52, v60, v61
	v_cvt_pk_bf16_f32 v53, v62, v63
	global_store_dwordx4 v[58:59], v[50:53], off offset:256
	s_nop 1
	v_add_u32_e32 v50, 0x90, v152
	v_ashrrev_i32_e32 v51, 31, v50
	v_mad_i64_i32 v[52:53], s[0:1], v50, s15, v[154:155]
	v_lshlrev_b64 v[58:59], 12, v[50:51]
	v_lshl_add_u64 v[50:51], v[52:53], 0, v[150:151]
	global_load_dwordx4 v[54:57], v[50:51], off offset:3072
	s_nop 0
	global_load_dwordx4 v[50:53], v[50:51], off offset:3328
	s_waitcnt vmcnt(1)
	v_lshlrev_b32_e32 v60, 16, v54
	v_and_b32_e32 v54, 0xffff0000, v54
	v_mul_f32_e32 v60, 0xbfb8aa3b, v60
	v_mul_f32_e32 v54, 0xbfb8aa3b, v54
	v_exp_f32_e32 v60, v60
	v_exp_f32_e32 v61, v54
	s_nop 0
	v_pk_add_f32 v[60:61], v[60:61], 1.0 op_sel_hi:[1,0]
	s_nop 0
	v_rcp_f32_e32 v61, v61
	v_rcp_f32_e32 v60, v60
	v_lshlrev_b32_e32 v54, 16, v55
	v_and_b32_e32 v55, 0xffff0000, v55
	v_mul_f32_e32 v54, 0xbfb8aa3b, v54
	v_mul_f32_e32 v55, 0xbfb8aa3b, v55
	v_exp_f32_e32 v54, v54
	v_exp_f32_e32 v55, v55
	v_pk_fma_f32 v[46:47], v[46:47], v[60:61], 0 op_sel_hi:[1,1,0]
	v_pk_add_f32 v[54:55], v[54:55], 1.0 op_sel_hi:[1,0]
	s_nop 0
	v_rcp_f32_e32 v55, v55
	v_rcp_f32_e32 v54, v54
	s_nop 0
	v_pk_fma_f32 v[48:49], v[48:49], v[54:55], 0 op_sel_hi:[1,1,0]
	v_lshlrev_b32_e32 v54, 16, v56
	v_and_b32_e32 v55, 0xffff0000, v56
	v_mul_f32_e32 v54, 0xbfb8aa3b, v54
	v_mul_f32_e32 v55, 0xbfb8aa3b, v55
	v_exp_f32_e32 v54, v54
	v_exp_f32_e32 v55, v55
	s_nop 0
	v_pk_add_f32 v[54:55], v[54:55], 1.0 op_sel_hi:[1,0]
	s_nop 0
	v_rcp_f32_e32 v55, v55
	v_rcp_f32_e32 v54, v54
	s_nop 0
	v_pk_fma_f32 v[42:43], v[42:43], v[54:55], 0 op_sel_hi:[1,1,0]
	v_lshlrev_b32_e32 v54, 16, v57
	v_and_b32_e32 v55, 0xffff0000, v57
	v_mul_f32_e32 v54, 0xbfb8aa3b, v54
	v_mul_f32_e32 v55, 0xbfb8aa3b, v55
	v_exp_f32_e32 v54, v54
	v_exp_f32_e32 v55, v55
	s_nop 0
	v_pk_add_f32 v[54:55], v[54:55], 1.0 op_sel_hi:[1,0]
	s_nop 0
	v_rcp_f32_e32 v55, v55
	v_rcp_f32_e32 v54, v54
	s_nop 0
	v_pk_fma_f32 v[54:55], v[44:45], v[54:55], 0 op_sel_hi:[1,1,0]
	v_cvt_pk_bf16_f32 v44, v46, v47
	v_cvt_pk_bf16_f32 v46, v42, v43
	v_lshl_add_u64 v[42:43], s[8:9], 0, v[58:59]
	v_cvt_pk_bf16_f32 v45, v48, v49
	v_cvt_pk_bf16_f32 v47, v54, v55
	v_lshl_add_u64 v[42:43], v[42:43], 0, v[150:151]
	global_store_dwordx4 v[42:43], v[44:47], off
	s_waitcnt vmcnt(1)
	s_nop 0
	v_lshlrev_b32_e32 v44, 16, v50
	v_and_b32_e32 v45, 0xffff0000, v50
	v_mul_f32_e32 v44, 0xbfb8aa3b, v44
	v_mul_f32_e32 v45, 0xbfb8aa3b, v45
	v_exp_f32_e32 v44, v44
	v_exp_f32_e32 v45, v45
	s_nop 0
	v_pk_add_f32 v[44:45], v[44:45], 1.0 op_sel_hi:[1,0]
	s_nop 0
	v_rcp_f32_e32 v45, v45
	v_rcp_f32_e32 v44, v44
	s_nop 0
	v_pk_fma_f32 v[38:39], v[38:39], v[44:45], 0 op_sel_hi:[1,1,0]
	v_lshlrev_b32_e32 v44, 16, v51
	v_and_b32_e32 v45, 0xffff0000, v51
	v_mul_f32_e32 v44, 0xbfb8aa3b, v44
	v_mul_f32_e32 v45, 0xbfb8aa3b, v45
	v_exp_f32_e32 v44, v44
	v_exp_f32_e32 v45, v45
	s_nop 0
	v_pk_add_f32 v[44:45], v[44:45], 1.0 op_sel_hi:[1,0]
	s_nop 0
	v_rcp_f32_e32 v45, v45
	v_rcp_f32_e32 v44, v44
	s_nop 0
	v_pk_fma_f32 v[40:41], v[40:41], v[44:45], 0 op_sel_hi:[1,1,0]
	v_lshlrev_b32_e32 v44, 16, v52
	v_and_b32_e32 v45, 0xffff0000, v52
	v_mul_f32_e32 v44, 0xbfb8aa3b, v44
	v_mul_f32_e32 v45, 0xbfb8aa3b, v45
	v_exp_f32_e32 v44, v44
	v_exp_f32_e32 v45, v45
	s_nop 0
	v_pk_add_f32 v[44:45], v[44:45], 1.0 op_sel_hi:[1,0]
	s_nop 0
	v_rcp_f32_e32 v45, v45
	v_rcp_f32_e32 v44, v44
	s_nop 0
	v_pk_fma_f32 v[44:45], v[34:35], v[44:45], 0 op_sel_hi:[1,1,0]
	v_lshlrev_b32_e32 v34, 16, v53
	v_and_b32_e32 v35, 0xffff0000, v53
	v_mul_f32_e32 v34, 0xbfb8aa3b, v34
	v_mul_f32_e32 v35, 0xbfb8aa3b, v35
	v_exp_f32_e32 v34, v34
	v_exp_f32_e32 v35, v35
	s_nop 0
	v_pk_add_f32 v[34:35], v[34:35], 1.0 op_sel_hi:[1,0]
	s_nop 0
	v_rcp_f32_e32 v35, v35
	v_rcp_f32_e32 v34, v34
	s_nop 0
	v_pk_fma_f32 v[46:47], v[36:37], v[34:35], 0 op_sel_hi:[1,1,0]
	v_cvt_pk_bf16_f32 v34, v38, v39
	v_cvt_pk_bf16_f32 v35, v40, v41
	v_cvt_pk_bf16_f32 v36, v44, v45
	v_cvt_pk_bf16_f32 v37, v46, v47
	global_store_dwordx4 v[42:43], v[34:37], off offset:256
	s_nop 1
	v_add_u32_e32 v34, 0xa0, v152
	v_ashrrev_i32_e32 v35, 31, v34
	v_mad_i64_i32 v[36:37], s[0:1], v34, s15, v[154:155]
	v_lshlrev_b64 v[42:43], 12, v[34:35]
	v_lshl_add_u64 v[34:35], v[36:37], 0, v[150:151]
	global_load_dwordx4 v[38:41], v[34:35], off offset:3072
	s_nop 0
	global_load_dwordx4 v[34:37], v[34:35], off offset:3328
	s_waitcnt vmcnt(1)
; DI unsigned pk2(float a, float b) { f32x2 v = {a, b}; bf16x2_t r = __builtin_convertvector(v, bf16x2_t); return __builtin_bit_cast(unsigned, r); }
; DI float sigmoidf_(float x) { return 1.f / (1.f + __expf(-x)); }
;     DI void operator()(const f32x4 (&acc)[2][2][4][2], const Unit& u, int wr, int wc, int fr, int fq) const {
;         const int row0 = u.pm * BM + wr * 64 + fr, col0 = u.pn * BM + wc * 32 + 8 * fq;
; #pragma unroll
;         for (int ai = 0; ai < 2; ++ai)
; #pragma unroll
;             for (int m = 0; m < 4; ++m) { const size_t row = (size_t)(row0 + ai * HALF + m * 16);
;                 u32x4 gzs[2], ts[2];
; #pragma unroll
;                 for (int bj = 0; bj < 2; ++bj) { const int col = col0 + bj * HALF; gzs[bj] = *(const u32x4*)(Zg + row * NZ + goff + col); if (add) ts[bj] = *(const u32x4*)(add + row * D + col); else ts[bj] = (u32x4){0u, 0u, 0u, 0u}; }
; #pragma unroll
;                 for (int bj = 0; bj < 2; ++bj) {
;                     const int col = col0 + bj * HALF;
;                     const u32x4 gz = gzs[bj];
;                     float a[8] = {0.f, 0.f, 0.f, 0.f, 0.f, 0.f, 0.f, 0.f};
;                     if (add) { const u32x4 t = ts[bj]; a[0] = bflo(t.x); a[1] = bfhi(t.x); a[2] = bflo(t.y); a[3] = bfhi(t.y); a[4] = bflo(t.z); a[5] = bfhi(t.z); a[6] = bflo(t.w); a[7] = bfhi(t.w); }
;                     const f32x4 v0 = acc[ai][bj][m][0], v1 = acc[ai][bj][m][1];
;                     float o[8];
;                     o[0] = a[0] + sigmoidf_(bflo(gz.x)) * v0[0]; o[1] = a[1] + sigmoidf_(bfhi(gz.x)) * v0[1];
;                     o[2] = a[2] + sigmoidf_(bflo(gz.y)) * v0[2]; o[3] = a[3] + sigmoidf_(bfhi(gz.y)) * v0[3];
;                     o[4] = a[4] + sigmoidf_(bflo(gz.z)) * v1[0]; o[5] = a[5] + sigmoidf_(bfhi(gz.z)) * v1[1];
;                     o[6] = a[6] + sigmoidf_(bflo(gz.w)) * v1[2]; o[7] = a[7] + sigmoidf_(bfhi(gz.w)) * v1[3];
;                     u32x4 w; w.x = pk2(o[0], o[1]); w.y = pk2(o[2], o[3]); w.z = pk2(o[4], o[5]); w.w = pk2(o[6], o[7]);
;                     *(u32x4*)(O + row * D + col) = w; } }
	v_lshlrev_b32_e32 v44, 16, v38
	v_and_b32_e32 v38, 0xffff0000, v38
	v_mul_f32_e32 v44, 0xbfb8aa3b, v44
	v_mul_f32_e32 v38, 0xbfb8aa3b, v38
	v_exp_f32_e32 v44, v44
	v_exp_f32_e32 v45, v38
	s_nop 0
	v_pk_add_f32 v[44:45], v[44:45], 1.0 op_sel_hi:[1,0]
	s_nop 0
	v_rcp_f32_e32 v45, v45
	v_rcp_f32_e32 v44, v44
	v_lshlrev_b32_e32 v38, 16, v39
	v_and_b32_e32 v39, 0xffff0000, v39
	v_mul_f32_e32 v38, 0xbfb8aa3b, v38
	v_mul_f32_e32 v39, 0xbfb8aa3b, v39
	v_exp_f32_e32 v38, v38
	v_exp_f32_e32 v39, v39
	v_pk_fma_f32 v[30:31], v[30:31], v[44:45], 0 op_sel_hi:[1,1,0]
	v_pk_add_f32 v[38:39], v[38:39], 1.0 op_sel_hi:[1,0]
	s_nop 0
	v_rcp_f32_e32 v39, v39
	v_rcp_f32_e32 v38, v38
	s_nop 0
	v_pk_fma_f32 v[32:33], v[32:33], v[38:39], 0 op_sel_hi:[1,1,0]
	v_lshlrev_b32_e32 v38, 16, v40
	v_and_b32_e32 v39, 0xffff0000, v40
	v_mul_f32_e32 v38, 0xbfb8aa3b, v38
	v_mul_f32_e32 v39, 0xbfb8aa3b, v39
	v_exp_f32_e32 v38, v38
	v_exp_f32_e32 v39, v39
	s_nop 0
	v_pk_add_f32 v[38:39], v[38:39], 1.0 op_sel_hi:[1,0]
	s_nop 0
	v_rcp_f32_e32 v39, v39
	v_rcp_f32_e32 v38, v38
	s_nop 0
	v_pk_fma_f32 v[26:27], v[26:27], v[38:39], 0 op_sel_hi:[1,1,0]
	v_lshlrev_b32_e32 v38, 16, v41
	v_and_b32_e32 v39, 0xffff0000, v41
	v_mul_f32_e32 v38, 0xbfb8aa3b, v38
	v_mul_f32_e32 v39, 0xbfb8aa3b, v39
	v_exp_f32_e32 v38, v38
	v_exp_f32_e32 v39, v39
	s_nop 0
	v_pk_add_f32 v[38:39], v[38:39], 1.0 op_sel_hi:[1,0]
	s_nop 0
	v_rcp_f32_e32 v39, v39
	v_rcp_f32_e32 v38, v38
	s_nop 0
	v_pk_fma_f32 v[38:39], v[28:29], v[38:39], 0 op_sel_hi:[1,1,0]
	v_cvt_pk_bf16_f32 v28, v30, v31
	v_cvt_pk_bf16_f32 v30, v26, v27
	v_lshl_add_u64 v[26:27], s[8:9], 0, v[42:43]
	v_cvt_pk_bf16_f32 v29, v32, v33
	v_cvt_pk_bf16_f32 v31, v38, v39
	v_lshl_add_u64 v[26:27], v[26:27], 0, v[150:151]
	global_store_dwordx4 v[26:27], v[28:31], off
	s_waitcnt vmcnt(1)
	s_nop 0
	v_lshlrev_b32_e32 v28, 16, v34
	v_and_b32_e32 v29, 0xffff0000, v34
	v_mul_f32_e32 v28, 0xbfb8aa3b, v28
	v_mul_f32_e32 v29, 0xbfb8aa3b, v29
	v_exp_f32_e32 v28, v28
	v_exp_f32_e32 v29, v29
	s_nop 0
	v_pk_add_f32 v[28:29], v[28:29], 1.0 op_sel_hi:[1,0]
	s_nop 0
	v_rcp_f32_e32 v29, v29
	v_rcp_f32_e32 v28, v28
	s_nop 0
	v_pk_fma_f32 v[22:23], v[22:23], v[28:29], 0 op_sel_hi:[1,1,0]
	v_lshlrev_b32_e32 v28, 16, v35
	v_and_b32_e32 v29, 0xffff0000, v35
	v_mul_f32_e32 v28, 0xbfb8aa3b, v28
	v_mul_f32_e32 v29, 0xbfb8aa3b, v29
	v_exp_f32_e32 v28, v28
	v_exp_f32_e32 v29, v29
	s_nop 0
	v_pk_add_f32 v[28:29], v[28:29], 1.0 op_sel_hi:[1,0]
	s_nop 0
	v_rcp_f32_e32 v29, v29
	v_rcp_f32_e32 v28, v28
	s_nop 0
	v_pk_fma_f32 v[24:25], v[24:25], v[28:29], 0 op_sel_hi:[1,1,0]
	v_lshlrev_b32_e32 v28, 16, v36
	v_and_b32_e32 v29, 0xffff0000, v36
	v_mul_f32_e32 v28, 0xbfb8aa3b, v28
	v_mul_f32_e32 v29, 0xbfb8aa3b, v29
	v_exp_f32_e32 v28, v28
	v_exp_f32_e32 v29, v29
	s_nop 0
	v_pk_add_f32 v[28:29], v[28:29], 1.0 op_sel_hi:[1,0]
	s_nop 0
	v_rcp_f32_e32 v29, v29
	v_rcp_f32_e32 v28, v28
	s_nop 0
	v_pk_fma_f32 v[28:29], v[18:19], v[28:29], 0 op_sel_hi:[1,1,0]
	v_lshlrev_b32_e32 v18, 16, v37
	v_and_b32_e32 v19, 0xffff0000, v37
	v_mul_f32_e32 v18, 0xbfb8aa3b, v18
	v_mul_f32_e32 v19, 0xbfb8aa3b, v19
	v_exp_f32_e32 v18, v18
	v_exp_f32_e32 v19, v19
	s_nop 0
	v_pk_add_f32 v[18:19], v[18:19], 1.0 op_sel_hi:[1,0]
	s_nop 0
	v_rcp_f32_e32 v19, v19
	v_rcp_f32_e32 v18, v18
	s_nop 0
	v_pk_fma_f32 v[30:31], v[20:21], v[18:19], 0 op_sel_hi:[1,1,0]
	v_cvt_pk_bf16_f32 v18, v22, v23
	v_cvt_pk_bf16_f32 v19, v24, v25
	v_cvt_pk_bf16_f32 v20, v28, v29
	v_cvt_pk_bf16_f32 v21, v30, v31
	global_store_dwordx4 v[26:27], v[18:21], off offset:256
	s_nop 1
	v_add_u32_e32 v18, 0xb0, v152
	v_ashrrev_i32_e32 v19, 31, v18
	v_mad_i64_i32 v[20:21], s[0:1], v18, s15, v[154:155]
	v_lshlrev_b64 v[26:27], 12, v[18:19]
	v_lshl_add_u64 v[18:19], v[20:21], 0, v[150:151]
	global_load_dwordx4 v[22:25], v[18:19], off offset:3072
	s_nop 0
	global_load_dwordx4 v[18:21], v[18:19], off offset:3328
	s_waitcnt vmcnt(1)
; template <class Epi, class Sched, bool ALIGN_EPI = true, bool SP2 = true>
; __device__ __forceinline__ void gemm_phase(LAS unsigned char* lds, const Dims g, const Sched& S, const Epi& E) {
;     ...
;         if constexpr (ALIGN_EPI) { if (wr == 0) PG8_BAR; }
;         E(acc, cur, wr, wc, fr, fq);
;         if (!has_next) break;
; #pragma unroll
;         for (int a = 0; a < 2; ++a)
; #pragma unroll
;             for (int b = 0; b < 2; ++b)
; #pragma unroll
;                 for (int m = 0; m < 4; ++m)
; #pragma unroll
;     DI void operator()(const f32x4 (&acc)[2][2][4][2], const Unit& u, int wr, int wc, int fr, int fq) const {
;         const int row0 = u.pm * BM + wr * 64 + fr, col0 = u.pn * BM + wc * 32 + 8 * fq;
; #pragma unroll
;         for (int ai = 0; ai < 2; ++ai)
; #pragma unroll
;             for (int m = 0; m < 4; ++m) { const size_t row = (size_t)(row0 + ai * HALF + m * 16);
;                 u32x4 gzs[2], ts[2];
; #pragma unroll
;                 for (int bj = 0; bj < 2; ++bj) { const int col = col0 + bj * HALF; gzs[bj] = *(const u32x4*)(Zg + row * NZ + goff + col); if (add) ts[bj] = *(const u32x4*)(add + row * D + col); else ts[bj] = (u32x4){0u, 0u, 0u, 0u}; }
; #pragma unroll
;                 for (int bj = 0; bj < 2; ++bj) {
;                     const int col = col0 + bj * HALF;
;                     const u32x4 gz = gzs[bj];
;                     float a[8] = {0.f, 0.f, 0.f, 0.f, 0.f, 0.f, 0.f, 0.f};
;                     if (add) { const u32x4 t = ts[bj]; a[0] = bflo(t.x); a[1] = bfhi(t.x); a[2] = bflo(t.y); a[3] = bfhi(t.y); a[4] = bflo(t.z); a[5] = bfhi(t.z); a[6] = bflo(t.w); a[7] = bfhi(t.w); }
;                     const f32x4 v0 = acc[ai][bj][m][0], v1 = acc[ai][bj][m][1];
;                     float o[8];
;                     o[0] = a[0] + sigmoidf_(bflo(gz.x)) * v0[0]; o[1] = a[1] + sigmoidf_(bfhi(gz.x)) * v0[1];
;                     o[2] = a[2] + sigmoidf_(bflo(gz.y)) * v0[2]; o[3] = a[3] + sigmoidf_(bfhi(gz.y)) * v0[3];
;                     o[4] = a[4] + sigmoidf_(bflo(gz.z)) * v1[0]; o[5] = a[5] + sigmoidf_(bfhi(gz.z)) * v1[1];
;                     o[6] = a[6] + sigmoidf_(bflo(gz.w)) * v1[2]; o[7] = a[7] + sigmoidf_(bfhi(gz.w)) * v1[3];
;                     u32x4 w; w.x = pk2(o[0], o[1]); w.y = pk2(o[2], o[3]); w.z = pk2(o[4], o[5]); w.w = pk2(o[6], o[7]);
;                     *(u32x4*)(O + row * D + col) = w; } }
;     }
	v_lshlrev_b32_e32 v28, 16, v22
	v_and_b32_e32 v22, 0xffff0000, v22
	v_mul_f32_e32 v28, 0xbfb8aa3b, v28
	v_mul_f32_e32 v22, 0xbfb8aa3b, v22
	v_exp_f32_e32 v28, v28
	v_exp_f32_e32 v29, v22
	s_nop 0
	v_pk_add_f32 v[28:29], v[28:29], 1.0 op_sel_hi:[1,0]
	s_nop 0
	v_rcp_f32_e32 v29, v29
	v_rcp_f32_e32 v28, v28
	v_lshlrev_b32_e32 v22, 16, v23
	v_and_b32_e32 v23, 0xffff0000, v23
	v_mul_f32_e32 v22, 0xbfb8aa3b, v22
	v_mul_f32_e32 v23, 0xbfb8aa3b, v23
	v_exp_f32_e32 v22, v22
	v_exp_f32_e32 v23, v23
	v_pk_fma_f32 v[14:15], v[14:15], v[28:29], 0 op_sel_hi:[1,1,0]
	v_pk_add_f32 v[22:23], v[22:23], 1.0 op_sel_hi:[1,0]
	s_nop 0
	v_rcp_f32_e32 v23, v23
	v_rcp_f32_e32 v22, v22
	s_nop 0
	v_pk_fma_f32 v[16:17], v[16:17], v[22:23], 0 op_sel_hi:[1,1,0]
	v_lshlrev_b32_e32 v22, 16, v24
	v_and_b32_e32 v23, 0xffff0000, v24
	v_mul_f32_e32 v22, 0xbfb8aa3b, v22
	v_mul_f32_e32 v23, 0xbfb8aa3b, v23
	v_exp_f32_e32 v22, v22
	v_exp_f32_e32 v23, v23
	s_nop 0
	v_pk_add_f32 v[22:23], v[22:23], 1.0 op_sel_hi:[1,0]
	s_nop 0
	v_rcp_f32_e32 v23, v23
	v_rcp_f32_e32 v22, v22
	s_nop 0
	v_pk_fma_f32 v[10:11], v[10:11], v[22:23], 0 op_sel_hi:[1,1,0]
	v_lshlrev_b32_e32 v22, 16, v25
	v_and_b32_e32 v23, 0xffff0000, v25
	v_mul_f32_e32 v22, 0xbfb8aa3b, v22
	v_mul_f32_e32 v23, 0xbfb8aa3b, v23
	v_exp_f32_e32 v22, v22
	v_exp_f32_e32 v23, v23
	s_nop 0
	v_pk_add_f32 v[22:23], v[22:23], 1.0 op_sel_hi:[1,0]
	s_nop 0
	v_rcp_f32_e32 v23, v23
	v_rcp_f32_e32 v22, v22
	s_nop 0
	v_pk_fma_f32 v[22:23], v[12:13], v[22:23], 0 op_sel_hi:[1,1,0]
	v_cvt_pk_bf16_f32 v12, v14, v15
	v_cvt_pk_bf16_f32 v14, v10, v11
	v_lshl_add_u64 v[10:11], s[8:9], 0, v[26:27]
	v_cvt_pk_bf16_f32 v13, v16, v17
	v_cvt_pk_bf16_f32 v15, v22, v23
	v_lshl_add_u64 v[10:11], v[10:11], 0, v[150:151]
	global_store_dwordx4 v[10:11], v[12:15], off
	s_waitcnt vmcnt(1)
	s_nop 0
	v_lshlrev_b32_e32 v12, 16, v18
	v_and_b32_e32 v13, 0xffff0000, v18
	v_mul_f32_e32 v12, 0xbfb8aa3b, v12
	v_mul_f32_e32 v13, 0xbfb8aa3b, v13
	v_exp_f32_e32 v12, v12
	v_exp_f32_e32 v13, v13
	s_nop 0
	v_pk_add_f32 v[12:13], v[12:13], 1.0 op_sel_hi:[1,0]
	s_nop 0
	v_rcp_f32_e32 v13, v13
	v_rcp_f32_e32 v12, v12
	s_nop 0
	v_pk_fma_f32 v[6:7], v[6:7], v[12:13], 0 op_sel_hi:[1,1,0]
	v_lshlrev_b32_e32 v12, 16, v19
	v_and_b32_e32 v13, 0xffff0000, v19
	v_mul_f32_e32 v12, 0xbfb8aa3b, v12
	v_mul_f32_e32 v13, 0xbfb8aa3b, v13
	v_exp_f32_e32 v12, v12
	v_exp_f32_e32 v13, v13
	s_nop 0
	v_pk_add_f32 v[12:13], v[12:13], 1.0 op_sel_hi:[1,0]
	s_nop 0
	v_rcp_f32_e32 v13, v13
	v_rcp_f32_e32 v12, v12
	s_nop 0
	v_pk_fma_f32 v[8:9], v[8:9], v[12:13], 0 op_sel_hi:[1,1,0]
	v_lshlrev_b32_e32 v12, 16, v20
	v_and_b32_e32 v13, 0xffff0000, v20
	v_mul_f32_e32 v12, 0xbfb8aa3b, v12
	v_mul_f32_e32 v13, 0xbfb8aa3b, v13
	v_exp_f32_e32 v12, v12
	v_exp_f32_e32 v13, v13
	s_nop 0
	v_pk_add_f32 v[12:13], v[12:13], 1.0 op_sel_hi:[1,0]
	s_nop 0
	v_rcp_f32_e32 v13, v13
	v_rcp_f32_e32 v12, v12
	s_nop 0
	v_pk_fma_f32 v[12:13], v[2:3], v[12:13], 0 op_sel_hi:[1,1,0]
	v_lshlrev_b32_e32 v2, 16, v21
	v_and_b32_e32 v3, 0xffff0000, v21
	v_mul_f32_e32 v2, 0xbfb8aa3b, v2
	v_mul_f32_e32 v3, 0xbfb8aa3b, v3
	v_exp_f32_e32 v2, v2
	v_exp_f32_e32 v3, v3
	s_nop 0
	v_pk_add_f32 v[2:3], v[2:3], 1.0 op_sel_hi:[1,0]
	s_nop 0
	v_rcp_f32_e32 v3, v3
	v_rcp_f32_e32 v2, v2
	s_nop 0
	v_pk_fma_f32 v[14:15], v[4:5], v[2:3], 0 op_sel_hi:[1,1,0]
	v_cvt_pk_bf16_f32 v2, v6, v7
	v_cvt_pk_bf16_f32 v3, v8, v9
	v_cvt_pk_bf16_f32 v4, v12, v13
	v_cvt_pk_bf16_f32 v5, v14, v15
	s_andn2_b64 vcc, exec, s[38:39]
	global_store_dwordx4 v[10:11], v[2:5], off offset:256
	s_cbranch_vccnz .LBB0_1394
	s_andn2_b64 vcc, exec, s[46:47]
	s_cbranch_vccnz .LBB0_1393
	s_barrier
	s_branch .LBB0_1393

; #define LAS __attribute__((address_space(3)))
; template <class Epi>
; DI void skinny64(const bf16* A, int lda, const bf16* Bt, int ldb, int N, int K, int r0, LAS unsigned char* lds, const Epi& epi, int wave, int lane, int bid, int G) {
;     const int n16 = lane & 15, q = lane >> 4; const int ksw = (K / 32) / 8;
;     LAS f32x4* red = (LAS f32x4*)lds;
;     for (int uu = bid; uu < (N / 16) * 2; uu += G) { const int nt = uu >> 1, mh = uu & 1;
;         f32x4 acc[2];
; #pragma unroll
;         for (int mt = 0; mt < 2; ++mt) acc[mt] = (f32x4){0.f, 0.f, 0.f, 0.f};
;         const bf16* wp = Bt + (size_t)(16 * nt + n16) * ldb + 8 * q + wave * ksw * 32; const bf16* ap = A + (size_t)(r0 + 32 * mh + n16) * lda + 8 * q + wave * ksw * 32;
; #pragma unroll 8
;         for (int ks = 0; ks < ksw; ++ks) { const bf16x8 wf = *(const bf16x8*)(wp + ks * 32);
; #pragma unroll
;             for (int mt = 0; mt < 2; ++mt) acc[mt] = __builtin_amdgcn_mfma_f32_16x16x32_bf16(wf, *(const bf16x8*)(ap + (size_t)(16 * mt) * lda + ks * 32), acc[mt], 0, 0, 0); }
;         __syncthreads();
; #pragma unroll
;         for (int mt = 0; mt < 2; ++mt) red[(wave * 2 + mt) * 64 + lane] = acc[mt];
;         __syncthreads();
;         if (wave < 2) { f32x4 s = red[wave * 64 + lane];
; #pragma unroll
;             for (int w = 1; w < 8; ++w) s = s + red[(w * 2 + wave) * 64 + lane];
;             epi(r0 + 32 * mh + 16 * wave + n16, 16 * nt + 4 * q, s); }
;     }
;     __syncthreads();
; }
.LBB0_1410:
	s_and_b32 s24, s4, -16
	v_or_b32_e32 v6, s24, v12
	v_ashrrev_i32_e32 v7, 31, v6
	s_and_b32 s25, s2, 32
	v_lshlrev_b64 v[6:7], 11, v[6:7]
	s_bitset1_b32 s25, 13
	v_lshl_add_u64 v[10:11], v[2:3], 0, v[6:7]
	v_or_b32_e32 v6, s25, v12
	v_lshlrev_b32_e32 v90, 11, v6
	v_lshl_add_u64 v[28:29], v[4:5], 0, v[90:91]
	s_mov_b32 s26, 0x8000
	v_add_co_u32_e32 v30, vcc, s26, v28
	global_load_dwordx4 v[6:9], v[10:11], off
	global_load_dwordx4 v[16:19], v[28:29], off
	v_addc_co_u32_e32 v31, vcc, 0, v29, vcc
	global_load_dwordx4 v[20:23], v[30:31], off
	global_load_dwordx4 v[108:111], v[10:11], off offset:64
	global_load_dwordx4 v[112:115], v[28:29], off offset:64
	global_load_dwordx4 v[116:119], v[30:31], off offset:64
	global_load_dwordx4 v[120:123], v[10:11], off offset:128
	global_load_dwordx4 v[124:127], v[28:29], off offset:128
	global_load_dwordx4 v[128:131], v[30:31], off offset:128
	global_load_dwordx4 v[132:135], v[10:11], off offset:192
	global_load_dwordx4 v[136:139], v[28:29], off offset:192
	global_load_dwordx4 v[140:143], v[30:31], off offset:192
	s_andn2_b64 vcc, exec, s[12:13]
	v_add_u32_e32 v10, s0, v13
	s_waitcnt vmcnt(10)
	v_mfma_f32_16x16x32_bf16 v[16:19], v[6:9], v[16:19], 0
	s_waitcnt vmcnt(9)
	v_mfma_f32_16x16x32_bf16 v[6:9], v[6:9], v[20:23], 0
	s_waitcnt vmcnt(7)
	v_mfma_f32_16x16x32_bf16 v[16:19], v[108:111], v[112:115], v[16:19]
	s_waitcnt vmcnt(6)
	v_mfma_f32_16x16x32_bf16 v[6:9], v[108:111], v[116:119], v[6:9]
	s_waitcnt vmcnt(4)
	v_mfma_f32_16x16x32_bf16 v[16:19], v[120:123], v[124:127], v[16:19]
	s_waitcnt vmcnt(3)
	v_mfma_f32_16x16x32_bf16 v[6:9], v[120:123], v[128:131], v[6:9]
	s_waitcnt vmcnt(1)
	v_mfma_f32_16x16x32_bf16 v[16:19], v[132:135], v[136:139], v[16:19]
	s_barrier
	s_waitcnt vmcnt(0)
	v_mfma_f32_16x16x32_bf16 v[6:9], v[132:135], v[140:143], v[6:9]
	s_nop 4
	ds_write_b128 v10, v[16:19]
	s_nop 2
	ds_write_b128 v10, v[6:9] offset:1024
	s_waitcnt lgkmcnt(0)
	s_barrier
	s_cbranch_vccnz .LBB0_1409
	v_add_u32_e32 v20, s1, v13
	ds_read_b128 v[6:9], v20
	ds_read_b128 v[16:19], v20 offset:2048
	s_waitcnt lgkmcnt(0)
	v_pk_add_f32 v[10:11], v[8:9], v[18:19]
	v_pk_add_f32 v[16:17], v[6:7], v[16:17]
	ds_read_b128 v[6:9], v20 offset:4096
	s_waitcnt lgkmcnt(0)
	v_pk_add_f32 v[10:11], v[10:11], v[8:9]
	v_pk_add_f32 v[16:17], v[16:17], v[6:7]
	ds_read_b128 v[6:9], v20 offset:6144
	s_waitcnt lgkmcnt(0)
	v_pk_add_f32 v[10:11], v[10:11], v[8:9]
	v_pk_add_f32 v[16:17], v[16:17], v[6:7]
	ds_read_b128 v[6:9], v20 offset:8192
	s_waitcnt lgkmcnt(0)
	v_pk_add_f32 v[10:11], v[10:11], v[8:9]
	v_pk_add_f32 v[16:17], v[16:17], v[6:7]
	ds_read_b128 v[6:9], v20 offset:10240
	s_waitcnt lgkmcnt(0)
	v_pk_add_f32 v[10:11], v[10:11], v[8:9]
	v_pk_add_f32 v[16:17], v[16:17], v[6:7]
	ds_read_b128 v[6:9], v20 offset:12288
	s_waitcnt lgkmcnt(0)
	v_pk_add_f32 v[10:11], v[10:11], v[8:9]
	v_pk_add_f32 v[16:17], v[16:17], v[6:7]
	ds_read_b128 v[6:9], v20 offset:14336
	s_waitcnt lgkmcnt(0)
	v_pk_add_f32 v[18:19], v[10:11], v[8:9]
	v_pk_add_f32 v[8:9], v[16:17], v[6:7]
	v_or_b32_e32 v6, s24, v15
	v_add_u32_e32 v10, s25, v14
	v_mov_b64_e32 v[16:17], s[40:41]
	v_ashrrev_i32_e32 v7, 31, v6
	v_mad_i64_i32 v[16:17], s[24:25], v10, s15, v[16:17]
	v_lshlrev_b64 v[6:7], 1, v[6:7]
	v_lshl_add_u64 v[16:17], v[16:17], 0, v[6:7]
	global_load_dwordx2 v[16:17], v[16:17], off offset:3072
	v_ashrrev_i32_e32 v11, 31, v10
	v_lshlrev_b64 v[10:11], 12, v[10:11]
	v_lshl_add_u64 v[10:11], s[8:9], 0, v[10:11]
	v_lshl_add_u64 v[6:7], v[10:11], 0, v[6:7]
	s_waitcnt vmcnt(0)
	v_lshlrev_b32_e32 v20, 16, v16
	v_and_b32_e32 v16, 0xffff0000, v16
	v_mul_f32_e32 v20, 0xbfb8aa3b, v20
	v_mul_f32_e32 v16, 0xbfb8aa3b, v16
	v_exp_f32_e32 v20, v20
	v_exp_f32_e32 v21, v16
	s_nop 0
	v_pk_add_f32 v[20:21], v[20:21], 1.0 op_sel_hi:[1,0]
	s_nop 0
	v_rcp_f32_e32 v21, v21
	v_rcp_f32_e32 v20, v20
	s_nop 0
	v_pk_fma_f32 v[8:9], v[8:9], v[20:21], 0 op_sel_hi:[1,1,0]
	s_nop 0
	v_cvt_pk_bf16_f32 v8, v8, v9
	v_lshlrev_b32_e32 v9, 16, v17
	v_mul_f32_e32 v9, 0xbfb8aa3b, v9
	v_exp_f32_e32 v16, v9
	v_and_b32_e32 v9, 0xffff0000, v17
	v_mul_f32_e32 v9, 0xbfb8aa3b, v9
	v_exp_f32_e32 v17, v9
	s_nop 0
	v_pk_add_f32 v[16:17], v[16:17], 1.0 op_sel_hi:[1,0]
	s_nop 0
	v_rcp_f32_e32 v17, v17
	v_rcp_f32_e32 v16, v16
	s_nop 0
	v_pk_fma_f32 v[16:17], v[18:19], v[16:17], 0 op_sel_hi:[1,1,0]
	s_nop 0
	v_cvt_pk_bf16_f32 v9, v16, v17
	global_store_dwordx2 v[6:7], v[8:9], off
	s_branch .LBB0_1409

; DI unsigned pk2(float a, float b) { f32x2 v = {a, b}; bf16x2_t r = __builtin_convertvector(v, bf16x2_t); return __builtin_bit_cast(unsigned, r); }
; DI float sigmoidf_(float x) { return 1.f / (1.f + __expf(-x)); }
;     DI void operator()(const f32x4 (&acc)[2][2][4][2], const Unit& u, int wr, int wc, int fr, int fq) const {
;         const int row0 = u.pm * BM + wr * 64 + fr, col0 = u.pn * BM + wc * 32 + 8 * fq;
; #pragma unroll
;         for (int ai = 0; ai < 2; ++ai)
; #pragma unroll
;             for (int m = 0; m < 4; ++m) { const size_t row = (size_t)(row0 + ai * HALF + m * 16);
;                 u32x4 gzs[2], ts[2];
; #pragma unroll
;                 for (int bj = 0; bj < 2; ++bj) { const int col = col0 + bj * HALF; gzs[bj] = *(const u32x4*)(Zg + row * NZ + goff + col); if (add) ts[bj] = *(const u32x4*)(add + row * D + col); else ts[bj] = (u32x4){0u, 0u, 0u, 0u}; }
; #pragma unroll
;                 for (int bj = 0; bj < 2; ++bj) {
;                     const int col = col0 + bj * HALF;
;                     const u32x4 gz = gzs[bj];
;                     float a[8] = {0.f, 0.f, 0.f, 0.f, 0.f, 0.f, 0.f, 0.f};
;                     if (add) { const u32x4 t = ts[bj]; a[0] = bflo(t.x); a[1] = bfhi(t.x); a[2] = bflo(t.y); a[3] = bfhi(t.y); a[4] = bflo(t.z); a[5] = bfhi(t.z); a[6] = bflo(t.w); a[7] = bfhi(t.w); }
;                     const f32x4 v0 = acc[ai][bj][m][0], v1 = acc[ai][bj][m][1];
;                     float o[8];
;                     o[0] = a[0] + sigmoidf_(bflo(gz.x)) * v0[0]; o[1] = a[1] + sigmoidf_(bfhi(gz.x)) * v0[1];
;                     o[2] = a[2] + sigmoidf_(bflo(gz.y)) * v0[2]; o[3] = a[3] + sigmoidf_(bfhi(gz.y)) * v0[3];
;                     o[4] = a[4] + sigmoidf_(bflo(gz.z)) * v1[0]; o[5] = a[5] + sigmoidf_(bfhi(gz.z)) * v1[1];
;                     o[6] = a[6] + sigmoidf_(bflo(gz.w)) * v1[2]; o[7] = a[7] + sigmoidf_(bfhi(gz.w)) * v1[3];
;                     u32x4 w; w.x = pk2(o[0], o[1]); w.y = pk2(o[2], o[3]); w.z = pk2(o[4], o[5]); w.w = pk2(o[6], o[7]);
;                     *(u32x4*)(O + row * D + col) = w; } }
.LBB0_1432:
	v_lshl_add_u32 v162, s12, 8, v177
	v_lshl_or_b32 v128, s0, 8, v179
	v_mov_b64_e32 v[172:173], s[40:41]
	v_mad_i64_i32 v[130:131], s[0:1], v162, s15, v[172:173]
	s_mov_b64 s[2:3], 0x1c00
	v_ashrrev_i32_e32 v129, 31, v128
	v_lshl_add_u64 v[130:131], v[130:131], 0, s[2:3]
	v_lshlrev_b64 v[158:159], 1, v[128:129]
	v_lshl_add_u64 v[134:135], v[130:131], 0, v[158:159]
	global_load_dwordx4 v[140:143], v[134:135], off
	v_ashrrev_i32_e32 v163, 31, v162
	v_lshlrev_b64 v[174:175], 12, v[162:163]
	v_lshl_add_u64 v[132:133], s[42:43], 0, v[174:175]
	v_lshl_add_u64 v[164:165], v[132:133], 0, v[158:159]
	global_load_dwordx4 v[144:147], v[164:165], off
	v_or_b32_e32 v128, 0x80, v128
	v_ashrrev_i32_e32 v129, 31, v128
	v_lshlrev_b64 v[160:161], 1, v[128:129]
	v_lshl_add_u64 v[128:129], v[130:131], 0, v[160:161]
	global_load_dwordx4 v[132:135], v[128:129], off
	s_nop 0
	global_load_dwordx4 v[128:131], v[164:165], off offset:256
	s_waitcnt vmcnt(0)
	v_lshlrev_b32_e32 v163, 16, v140
	v_and_b32_e32 v140, 0xffff0000, v140
	v_mul_f32_e32 v163, 0xbfb8aa3b, v163
	v_mul_f32_e32 v140, 0xbfb8aa3b, v140
	v_exp_f32_e32 v164, v163
	v_exp_f32_e32 v165, v140
	v_lshlrev_b32_e32 v166, 16, v144
	v_and_b32_e32 v167, 0xffff0000, v144
	v_pk_add_f32 v[164:165], v[164:165], 1.0 op_sel_hi:[1,0]
	s_nop 0
	v_rcp_f32_e32 v165, v165
	v_rcp_f32_e32 v164, v164
	v_lshlrev_b32_e32 v140, 16, v141
	v_and_b32_e32 v141, 0xffff0000, v141
	v_mul_f32_e32 v140, 0xbfb8aa3b, v140
	v_mul_f32_e32 v141, 0xbfb8aa3b, v141
	v_exp_f32_e32 v140, v140
	v_exp_f32_e32 v141, v141
	v_pk_fma_f32 v[136:137], v[136:137], v[164:165], v[166:167]
	v_lshlrev_b32_e32 v144, 16, v145
	v_and_b32_e32 v145, 0xffff0000, v145
	v_pk_add_f32 v[140:141], v[140:141], 1.0 op_sel_hi:[1,0]
	v_cvt_pk_bf16_f32 v136, v136, v137
	v_rcp_f32_e32 v141, v141
	v_rcp_f32_e32 v140, v140
	s_nop 0
	v_pk_fma_f32 v[138:139], v[138:139], v[140:141], v[144:145]
	v_lshlrev_b32_e32 v140, 16, v142
	v_mul_f32_e32 v140, 0xbfb8aa3b, v140
	v_exp_f32_e32 v144, v140
	v_and_b32_e32 v140, 0xffff0000, v142
	v_mul_f32_e32 v140, 0xbfb8aa3b, v140
	v_exp_f32_e32 v145, v140
	v_lshlrev_b32_e32 v140, 16, v146
	v_and_b32_e32 v141, 0xffff0000, v146
	v_cvt_pk_bf16_f32 v137, v138, v139
	v_pk_add_f32 v[144:145], v[144:145], 1.0 op_sel_hi:[1,0]
	s_nop 0
	v_rcp_f32_e32 v145, v145
	v_rcp_f32_e32 v144, v144
	s_nop 0
	v_pk_fma_f32 v[124:125], v[124:125], v[144:145], v[140:141]
	v_lshlrev_b32_e32 v140, 16, v143
	v_and_b32_e32 v141, 0xffff0000, v143
	v_mul_f32_e32 v140, 0xbfb8aa3b, v140
	v_mul_f32_e32 v141, 0xbfb8aa3b, v141
	v_exp_f32_e32 v140, v140
	v_exp_f32_e32 v141, v141
	v_lshlrev_b32_e32 v142, 16, v147
	v_and_b32_e32 v143, 0xffff0000, v147
	v_cvt_pk_bf16_f32 v138, v124, v125
	v_pk_add_f32 v[140:141], v[140:141], 1.0 op_sel_hi:[1,0]
	v_lshl_add_u64 v[124:125], s[8:9], 0, v[174:175]
	v_lshl_add_u64 v[124:125], v[124:125], 0, v[158:159]
	v_rcp_f32_e32 v141, v141
	v_rcp_f32_e32 v140, v140
	s_nop 0
	v_pk_fma_f32 v[126:127], v[126:127], v[140:141], v[142:143]
	s_nop 0
	v_cvt_pk_bf16_f32 v139, v126, v127
	v_lshlrev_b32_e32 v126, 16, v132
	v_and_b32_e32 v127, 0xffff0000, v132
	v_mul_f32_e32 v126, 0xbfb8aa3b, v126
	v_mul_f32_e32 v127, 0xbfb8aa3b, v127
	v_exp_f32_e32 v126, v126
	v_exp_f32_e32 v127, v127
	global_store_dwordx4 v[124:125], v[136:139], off
	v_pk_add_f32 v[126:127], v[126:127], 1.0 op_sel_hi:[1,0]
	s_nop 0
	v_lshlrev_b32_e32 v136, 16, v128
	v_and_b32_e32 v137, 0xffff0000, v128
	v_rcp_f32_e32 v127, v127
	v_rcp_f32_e32 v126, v126
	s_nop 0
	v_pk_fma_f32 v[120:121], v[120:121], v[126:127], v[136:137]
	v_lshlrev_b32_e32 v126, 16, v133
	v_and_b32_e32 v127, 0xffff0000, v133
	v_mul_f32_e32 v126, 0xbfb8aa3b, v126
	v_mul_f32_e32 v127, 0xbfb8aa3b, v127
	v_exp_f32_e32 v126, v126
	v_exp_f32_e32 v127, v127
	v_lshlrev_b32_e32 v128, 16, v129
	v_and_b32_e32 v129, 0xffff0000, v129
	v_pk_add_f32 v[126:127], v[126:127], 1.0 op_sel_hi:[1,0]
	s_nop 0
	v_rcp_f32_e32 v127, v127
	v_rcp_f32_e32 v126, v126
	s_nop 0
	v_pk_fma_f32 v[122:123], v[122:123], v[126:127], v[128:129]
	v_lshlrev_b32_e32 v126, 16, v134
	v_and_b32_e32 v127, 0xffff0000, v134
	v_mul_f32_e32 v126, 0xbfb8aa3b, v126
	v_mul_f32_e32 v127, 0xbfb8aa3b, v127
	v_exp_f32_e32 v126, v126
	v_exp_f32_e32 v127, v127
	v_lshlrev_b32_e32 v128, 16, v130
	v_and_b32_e32 v129, 0xffff0000, v130
	v_pk_add_f32 v[126:127], v[126:127], 1.0 op_sel_hi:[1,0]
	s_nop 0
	v_rcp_f32_e32 v127, v127
	v_rcp_f32_e32 v126, v126
	s_nop 0
	v_pk_fma_f32 v[126:127], v[116:117], v[126:127], v[128:129]
	v_lshlrev_b32_e32 v116, 16, v135
	v_and_b32_e32 v117, 0xffff0000, v135
	v_mul_f32_e32 v116, 0xbfb8aa3b, v116
	v_mul_f32_e32 v117, 0xbfb8aa3b, v117
	v_exp_f32_e32 v116, v116
	v_exp_f32_e32 v117, v117
	v_lshlrev_b32_e32 v128, 16, v131
	v_and_b32_e32 v129, 0xffff0000, v131
	v_pk_add_f32 v[116:117], v[116:117], 1.0 op_sel_hi:[1,0]
	s_nop 0
	v_rcp_f32_e32 v117, v117
	v_rcp_f32_e32 v116, v116
	s_nop 0
	v_pk_fma_f32 v[128:129], v[118:119], v[116:117], v[128:129]
	v_cvt_pk_bf16_f32 v116, v120, v121
	v_cvt_pk_bf16_f32 v117, v122, v123
	v_cvt_pk_bf16_f32 v118, v126, v127
	v_cvt_pk_bf16_f32 v119, v128, v129
	global_store_dwordx4 v[124:125], v[116:119], off offset:256
	s_nop 1
	v_or_b32_e32 v116, 16, v162
	v_mad_i64_i32 v[118:119], s[0:1], v116, s15, v[172:173]
	v_lshl_add_u64 v[118:119], v[118:119], 0, s[2:3]
	v_lshl_add_u64 v[120:121], v[118:119], 0, v[158:159]
	global_load_dwordx4 v[124:127], v[120:121], off
	v_ashrrev_i32_e32 v117, 31, v116
	v_lshlrev_b64 v[132:133], 12, v[116:117]
	v_lshl_add_u64 v[116:117], s[42:43], 0, v[132:133]
	v_lshl_add_u64 v[116:117], v[116:117], 0, v[158:159]
	global_load_dwordx4 v[128:131], v[116:117], off
	v_lshl_add_u64 v[118:119], v[118:119], 0, v[160:161]
	global_load_dwordx4 v[120:123], v[118:119], off
	s_nop 0
	global_load_dwordx4 v[116:119], v[116:117], off offset:256
	s_waitcnt vmcnt(3)
; DI unsigned pk2(float a, float b) { f32x2 v = {a, b}; bf16x2_t r = __builtin_convertvector(v, bf16x2_t); return __builtin_bit_cast(unsigned, r); }
; DI float sigmoidf_(float x) { return 1.f / (1.f + __expf(-x)); }
;     DI void operator()(const f32x4 (&acc)[2][2][4][2], const Unit& u, int wr, int wc, int fr, int fq) const {
;         const int row0 = u.pm * BM + wr * 64 + fr, col0 = u.pn * BM + wc * 32 + 8 * fq;
; #pragma unroll
;         for (int ai = 0; ai < 2; ++ai)
; #pragma unroll
;             for (int m = 0; m < 4; ++m) { const size_t row = (size_t)(row0 + ai * HALF + m * 16);
;                 u32x4 gzs[2], ts[2];
; #pragma unroll
;                 for (int bj = 0; bj < 2; ++bj) { const int col = col0 + bj * HALF; gzs[bj] = *(const u32x4*)(Zg + row * NZ + goff + col); if (add) ts[bj] = *(const u32x4*)(add + row * D + col); else ts[bj] = (u32x4){0u, 0u, 0u, 0u}; }
; #pragma unroll
;                 for (int bj = 0; bj < 2; ++bj) {
;                     const int col = col0 + bj * HALF;
;                     const u32x4 gz = gzs[bj];
;                     float a[8] = {0.f, 0.f, 0.f, 0.f, 0.f, 0.f, 0.f, 0.f};
;                     if (add) { const u32x4 t = ts[bj]; a[0] = bflo(t.x); a[1] = bfhi(t.x); a[2] = bflo(t.y); a[3] = bfhi(t.y); a[4] = bflo(t.z); a[5] = bfhi(t.z); a[6] = bflo(t.w); a[7] = bfhi(t.w); }
;                     const f32x4 v0 = acc[ai][bj][m][0], v1 = acc[ai][bj][m][1];
;                     float o[8];
;                     o[0] = a[0] + sigmoidf_(bflo(gz.x)) * v0[0]; o[1] = a[1] + sigmoidf_(bfhi(gz.x)) * v0[1];
;                     o[2] = a[2] + sigmoidf_(bflo(gz.y)) * v0[2]; o[3] = a[3] + sigmoidf_(bfhi(gz.y)) * v0[3];
;                     o[4] = a[4] + sigmoidf_(bflo(gz.z)) * v1[0]; o[5] = a[5] + sigmoidf_(bfhi(gz.z)) * v1[1];
;                     o[6] = a[6] + sigmoidf_(bflo(gz.w)) * v1[2]; o[7] = a[7] + sigmoidf_(bfhi(gz.w)) * v1[3];
;                     u32x4 w; w.x = pk2(o[0], o[1]); w.y = pk2(o[2], o[3]); w.z = pk2(o[4], o[5]); w.w = pk2(o[6], o[7]);
;                     *(u32x4*)(O + row * D + col) = w; } }
	v_lshlrev_b32_e32 v134, 16, v124
	v_and_b32_e32 v124, 0xffff0000, v124
	v_mul_f32_e32 v134, 0xbfb8aa3b, v134
	v_mul_f32_e32 v124, 0xbfb8aa3b, v124
	v_exp_f32_e32 v134, v134
	v_exp_f32_e32 v135, v124
	s_waitcnt vmcnt(2)
	v_lshlrev_b32_e32 v136, 16, v128
	v_and_b32_e32 v137, 0xffff0000, v128
	v_pk_add_f32 v[134:135], v[134:135], 1.0 op_sel_hi:[1,0]
	s_nop 0
	v_rcp_f32_e32 v135, v135
	v_rcp_f32_e32 v134, v134
	v_lshlrev_b32_e32 v124, 16, v125
	v_and_b32_e32 v125, 0xffff0000, v125
	v_mul_f32_e32 v124, 0xbfb8aa3b, v124
	v_mul_f32_e32 v125, 0xbfb8aa3b, v125
	v_exp_f32_e32 v124, v124
	v_exp_f32_e32 v125, v125
	v_pk_fma_f32 v[112:113], v[112:113], v[134:135], v[136:137]
	v_lshlrev_b32_e32 v128, 16, v129
	v_and_b32_e32 v129, 0xffff0000, v129
	v_pk_add_f32 v[124:125], v[124:125], 1.0 op_sel_hi:[1,0]
	s_nop 0
	v_rcp_f32_e32 v125, v125
	v_rcp_f32_e32 v124, v124
	s_nop 0
	v_pk_fma_f32 v[114:115], v[114:115], v[124:125], v[128:129]
	v_lshlrev_b32_e32 v124, 16, v126
	v_and_b32_e32 v125, 0xffff0000, v126
	v_mul_f32_e32 v124, 0xbfb8aa3b, v124
	v_mul_f32_e32 v125, 0xbfb8aa3b, v125
	v_exp_f32_e32 v124, v124
	v_exp_f32_e32 v125, v125
	v_lshlrev_b32_e32 v128, 16, v130
	v_and_b32_e32 v129, 0xffff0000, v130
	v_pk_add_f32 v[124:125], v[124:125], 1.0 op_sel_hi:[1,0]
	s_nop 0
	v_rcp_f32_e32 v125, v125
	v_rcp_f32_e32 v124, v124
	s_nop 0
	v_pk_fma_f32 v[108:109], v[108:109], v[124:125], v[128:129]
	v_lshlrev_b32_e32 v124, 16, v127
	v_and_b32_e32 v125, 0xffff0000, v127
	v_mul_f32_e32 v124, 0xbfb8aa3b, v124
	v_mul_f32_e32 v125, 0xbfb8aa3b, v125
	v_exp_f32_e32 v124, v124
	v_exp_f32_e32 v125, v125
	v_lshlrev_b32_e32 v126, 16, v131
	v_and_b32_e32 v127, 0xffff0000, v131
	v_pk_add_f32 v[124:125], v[124:125], 1.0 op_sel_hi:[1,0]
	s_nop 0
	v_rcp_f32_e32 v125, v125
	v_rcp_f32_e32 v124, v124
	s_nop 0
	v_pk_fma_f32 v[124:125], v[110:111], v[124:125], v[126:127]
	v_cvt_pk_bf16_f32 v110, v112, v113
	v_cvt_pk_bf16_f32 v112, v108, v109
	v_lshl_add_u64 v[108:109], s[8:9], 0, v[132:133]
	v_cvt_pk_bf16_f32 v111, v114, v115
	v_cvt_pk_bf16_f32 v113, v124, v125
	v_lshl_add_u64 v[108:109], v[108:109], 0, v[158:159]
	global_store_dwordx4 v[108:109], v[110:113], off
	s_waitcnt vmcnt(2)
	s_nop 0
	v_lshlrev_b32_e32 v110, 16, v120
	v_and_b32_e32 v111, 0xffff0000, v120
	v_mul_f32_e32 v110, 0xbfb8aa3b, v110
	v_mul_f32_e32 v111, 0xbfb8aa3b, v111
	v_exp_f32_e32 v110, v110
	v_exp_f32_e32 v111, v111
	s_waitcnt vmcnt(1)
	v_lshlrev_b32_e32 v112, 16, v116
	v_and_b32_e32 v113, 0xffff0000, v116
	v_pk_add_f32 v[110:111], v[110:111], 1.0 op_sel_hi:[1,0]
	s_nop 0
	v_rcp_f32_e32 v111, v111
	v_rcp_f32_e32 v110, v110
	s_nop 0
	v_pk_fma_f32 v[104:105], v[104:105], v[110:111], v[112:113]
	v_lshlrev_b32_e32 v110, 16, v121
	v_and_b32_e32 v111, 0xffff0000, v121
	v_mul_f32_e32 v110, 0xbfb8aa3b, v110
	v_mul_f32_e32 v111, 0xbfb8aa3b, v111
	v_exp_f32_e32 v110, v110
	v_exp_f32_e32 v111, v111
	v_lshlrev_b32_e32 v112, 16, v117
	v_and_b32_e32 v113, 0xffff0000, v117
	v_pk_add_f32 v[110:111], v[110:111], 1.0 op_sel_hi:[1,0]
	s_nop 0
	v_rcp_f32_e32 v111, v111
	v_rcp_f32_e32 v110, v110
	s_nop 0
	v_pk_fma_f32 v[106:107], v[106:107], v[110:111], v[112:113]
	v_lshlrev_b32_e32 v110, 16, v122
	v_and_b32_e32 v111, 0xffff0000, v122
	v_mul_f32_e32 v110, 0xbfb8aa3b, v110
	v_mul_f32_e32 v111, 0xbfb8aa3b, v111
	v_exp_f32_e32 v110, v110
	v_exp_f32_e32 v111, v111
	v_lshlrev_b32_e32 v112, 16, v118
	v_and_b32_e32 v113, 0xffff0000, v118
	v_pk_add_f32 v[110:111], v[110:111], 1.0 op_sel_hi:[1,0]
	s_nop 0
	v_rcp_f32_e32 v111, v111
	v_rcp_f32_e32 v110, v110
	s_nop 0
	v_pk_fma_f32 v[110:111], v[100:101], v[110:111], v[112:113]
	v_lshlrev_b32_e32 v100, 16, v123
	v_and_b32_e32 v101, 0xffff0000, v123
	v_mul_f32_e32 v100, 0xbfb8aa3b, v100
	v_mul_f32_e32 v101, 0xbfb8aa3b, v101
	v_exp_f32_e32 v100, v100
	v_exp_f32_e32 v101, v101
	v_lshlrev_b32_e32 v112, 16, v119
	v_and_b32_e32 v113, 0xffff0000, v119
	v_pk_add_f32 v[100:101], v[100:101], 1.0 op_sel_hi:[1,0]
	s_nop 0
	v_rcp_f32_e32 v101, v101
	v_rcp_f32_e32 v100, v100
	s_nop 0
	v_pk_fma_f32 v[112:113], v[102:103], v[100:101], v[112:113]
	v_cvt_pk_bf16_f32 v100, v104, v105
	v_cvt_pk_bf16_f32 v101, v106, v107
	v_cvt_pk_bf16_f32 v102, v110, v111
	v_cvt_pk_bf16_f32 v103, v112, v113
	global_store_dwordx4 v[108:109], v[100:103], off offset:256
	s_nop 1
	v_or_b32_e32 v100, 32, v162
	v_mad_i64_i32 v[102:103], s[0:1], v100, s15, v[172:173]
	v_lshl_add_u64 v[102:103], v[102:103], 0, s[2:3]
	v_lshl_add_u64 v[104:105], v[102:103], 0, v[158:159]
	global_load_dwordx4 v[108:111], v[104:105], off
	v_ashrrev_i32_e32 v101, 31, v100
	v_lshlrev_b64 v[116:117], 12, v[100:101]
	v_lshl_add_u64 v[100:101], s[42:43], 0, v[116:117]
	v_lshl_add_u64 v[100:101], v[100:101], 0, v[158:159]
	global_load_dwordx4 v[112:115], v[100:101], off
	v_lshl_add_u64 v[102:103], v[102:103], 0, v[160:161]
	global_load_dwordx4 v[104:107], v[102:103], off
	s_nop 0
	global_load_dwordx4 v[100:103], v[100:101], off offset:256
	s_waitcnt vmcnt(3)
	v_lshlrev_b32_e32 v118, 16, v108
	v_and_b32_e32 v108, 0xffff0000, v108
	v_mul_f32_e32 v118, 0xbfb8aa3b, v118
	v_mul_f32_e32 v108, 0xbfb8aa3b, v108
	v_exp_f32_e32 v118, v118
	v_exp_f32_e32 v119, v108
	s_waitcnt vmcnt(2)
; DI unsigned pk2(float a, float b) { f32x2 v = {a, b}; bf16x2_t r = __builtin_convertvector(v, bf16x2_t); return __builtin_bit_cast(unsigned, r); }
; DI float sigmoidf_(float x) { return 1.f / (1.f + __expf(-x)); }
;     DI void operator()(const f32x4 (&acc)[2][2][4][2], const Unit& u, int wr, int wc, int fr, int fq) const {
;         const int row0 = u.pm * BM + wr * 64 + fr, col0 = u.pn * BM + wc * 32 + 8 * fq;
; #pragma unroll
;         for (int ai = 0; ai < 2; ++ai)
; #pragma unroll
;             for (int m = 0; m < 4; ++m) { const size_t row = (size_t)(row0 + ai * HALF + m * 16);
;                 u32x4 gzs[2], ts[2];
; #pragma unroll
;                 for (int bj = 0; bj < 2; ++bj) { const int col = col0 + bj * HALF; gzs[bj] = *(const u32x4*)(Zg + row * NZ + goff + col); if (add) ts[bj] = *(const u32x4*)(add + row * D + col); else ts[bj] = (u32x4){0u, 0u, 0u, 0u}; }
; #pragma unroll
;                 for (int bj = 0; bj < 2; ++bj) {
;                     const int col = col0 + bj * HALF;
;                     const u32x4 gz = gzs[bj];
;                     float a[8] = {0.f, 0.f, 0.f, 0.f, 0.f, 0.f, 0.f, 0.f};
;                     if (add) { const u32x4 t = ts[bj]; a[0] = bflo(t.x); a[1] = bfhi(t.x); a[2] = bflo(t.y); a[3] = bfhi(t.y); a[4] = bflo(t.z); a[5] = bfhi(t.z); a[6] = bflo(t.w); a[7] = bfhi(t.w); }
;                     const f32x4 v0 = acc[ai][bj][m][0], v1 = acc[ai][bj][m][1];
;                     float o[8];
;                     o[0] = a[0] + sigmoidf_(bflo(gz.x)) * v0[0]; o[1] = a[1] + sigmoidf_(bfhi(gz.x)) * v0[1];
;                     o[2] = a[2] + sigmoidf_(bflo(gz.y)) * v0[2]; o[3] = a[3] + sigmoidf_(bfhi(gz.y)) * v0[3];
;                     o[4] = a[4] + sigmoidf_(bflo(gz.z)) * v1[0]; o[5] = a[5] + sigmoidf_(bfhi(gz.z)) * v1[1];
;                     o[6] = a[6] + sigmoidf_(bflo(gz.w)) * v1[2]; o[7] = a[7] + sigmoidf_(bfhi(gz.w)) * v1[3];
;                     u32x4 w; w.x = pk2(o[0], o[1]); w.y = pk2(o[2], o[3]); w.z = pk2(o[4], o[5]); w.w = pk2(o[6], o[7]);
;                     *(u32x4*)(O + row * D + col) = w; } }
	v_lshlrev_b32_e32 v120, 16, v112
	v_and_b32_e32 v121, 0xffff0000, v112
	v_pk_add_f32 v[118:119], v[118:119], 1.0 op_sel_hi:[1,0]
	s_nop 0
	v_rcp_f32_e32 v119, v119
	v_rcp_f32_e32 v118, v118
	v_lshlrev_b32_e32 v108, 16, v109
	v_and_b32_e32 v109, 0xffff0000, v109
	v_mul_f32_e32 v108, 0xbfb8aa3b, v108
	v_mul_f32_e32 v109, 0xbfb8aa3b, v109
	v_exp_f32_e32 v108, v108
	v_exp_f32_e32 v109, v109
	v_pk_fma_f32 v[96:97], v[96:97], v[118:119], v[120:121]
	v_lshlrev_b32_e32 v112, 16, v113
	v_and_b32_e32 v113, 0xffff0000, v113
	v_pk_add_f32 v[108:109], v[108:109], 1.0 op_sel_hi:[1,0]
	s_nop 0
	v_rcp_f32_e32 v109, v109
	v_rcp_f32_e32 v108, v108
	s_nop 0
	v_pk_fma_f32 v[98:99], v[98:99], v[108:109], v[112:113]
	v_lshlrev_b32_e32 v108, 16, v110
	v_and_b32_e32 v109, 0xffff0000, v110
	v_mul_f32_e32 v108, 0xbfb8aa3b, v108
	v_mul_f32_e32 v109, 0xbfb8aa3b, v109
	v_exp_f32_e32 v108, v108
	v_exp_f32_e32 v109, v109
	v_lshlrev_b32_e32 v112, 16, v114
	v_and_b32_e32 v113, 0xffff0000, v114
	v_pk_add_f32 v[108:109], v[108:109], 1.0 op_sel_hi:[1,0]
	s_nop 0
	v_rcp_f32_e32 v109, v109
	v_rcp_f32_e32 v108, v108
	s_nop 0
	v_pk_fma_f32 v[92:93], v[92:93], v[108:109], v[112:113]
	v_lshlrev_b32_e32 v108, 16, v111
	v_and_b32_e32 v109, 0xffff0000, v111
	v_mul_f32_e32 v108, 0xbfb8aa3b, v108
	v_mul_f32_e32 v109, 0xbfb8aa3b, v109
	v_exp_f32_e32 v108, v108
	v_exp_f32_e32 v109, v109
	v_lshlrev_b32_e32 v110, 16, v115
	v_and_b32_e32 v111, 0xffff0000, v115
	v_pk_add_f32 v[108:109], v[108:109], 1.0 op_sel_hi:[1,0]
	s_nop 0
	v_rcp_f32_e32 v109, v109
	v_rcp_f32_e32 v108, v108
	s_nop 0
	v_pk_fma_f32 v[108:109], v[94:95], v[108:109], v[110:111]
	v_cvt_pk_bf16_f32 v94, v96, v97
	v_cvt_pk_bf16_f32 v96, v92, v93
	v_lshl_add_u64 v[92:93], s[8:9], 0, v[116:117]
	v_cvt_pk_bf16_f32 v95, v98, v99
	v_cvt_pk_bf16_f32 v97, v108, v109
	v_lshl_add_u64 v[92:93], v[92:93], 0, v[158:159]
	global_store_dwordx4 v[92:93], v[94:97], off
	s_waitcnt vmcnt(2)
	s_nop 0
	v_lshlrev_b32_e32 v94, 16, v104
	v_and_b32_e32 v95, 0xffff0000, v104
	v_mul_f32_e32 v94, 0xbfb8aa3b, v94
	v_mul_f32_e32 v95, 0xbfb8aa3b, v95
	v_exp_f32_e32 v94, v94
	v_exp_f32_e32 v95, v95
	s_waitcnt vmcnt(1)
	v_lshlrev_b32_e32 v96, 16, v100
	v_and_b32_e32 v97, 0xffff0000, v100
	v_pk_add_f32 v[94:95], v[94:95], 1.0 op_sel_hi:[1,0]
	s_nop 0
	v_rcp_f32_e32 v95, v95
	v_rcp_f32_e32 v94, v94
	s_nop 0
	v_pk_fma_f32 v[86:87], v[86:87], v[94:95], v[96:97]
	v_lshlrev_b32_e32 v94, 16, v105
	v_and_b32_e32 v95, 0xffff0000, v105
	v_mul_f32_e32 v94, 0xbfb8aa3b, v94
	v_mul_f32_e32 v95, 0xbfb8aa3b, v95
	v_exp_f32_e32 v94, v94
	v_exp_f32_e32 v95, v95
	v_lshlrev_b32_e32 v96, 16, v101
	v_and_b32_e32 v97, 0xffff0000, v101
	v_pk_add_f32 v[94:95], v[94:95], 1.0 op_sel_hi:[1,0]
	s_nop 0
	v_rcp_f32_e32 v95, v95
	v_rcp_f32_e32 v94, v94
	s_nop 0
	v_pk_fma_f32 v[88:89], v[88:89], v[94:95], v[96:97]
	v_lshlrev_b32_e32 v94, 16, v106
	v_and_b32_e32 v95, 0xffff0000, v106
	v_mul_f32_e32 v94, 0xbfb8aa3b, v94
	v_mul_f32_e32 v95, 0xbfb8aa3b, v95
	v_exp_f32_e32 v94, v94
	v_exp_f32_e32 v95, v95
	v_lshlrev_b32_e32 v96, 16, v102
	v_and_b32_e32 v97, 0xffff0000, v102
	v_pk_add_f32 v[94:95], v[94:95], 1.0 op_sel_hi:[1,0]
	s_nop 0
	v_rcp_f32_e32 v95, v95
	v_rcp_f32_e32 v94, v94
	s_nop 0
	v_pk_fma_f32 v[94:95], v[82:83], v[94:95], v[96:97]
	v_lshlrev_b32_e32 v82, 16, v107
	v_and_b32_e32 v83, 0xffff0000, v107
	v_mul_f32_e32 v82, 0xbfb8aa3b, v82
	v_mul_f32_e32 v83, 0xbfb8aa3b, v83
	v_exp_f32_e32 v82, v82
	v_exp_f32_e32 v83, v83
	v_lshlrev_b32_e32 v96, 16, v103
	v_and_b32_e32 v97, 0xffff0000, v103
	v_pk_add_f32 v[82:83], v[82:83], 1.0 op_sel_hi:[1,0]
	s_nop 0
	v_rcp_f32_e32 v83, v83
	v_rcp_f32_e32 v82, v82
	s_nop 0
	v_pk_fma_f32 v[96:97], v[84:85], v[82:83], v[96:97]
	v_cvt_pk_bf16_f32 v82, v86, v87
	v_cvt_pk_bf16_f32 v83, v88, v89
	v_cvt_pk_bf16_f32 v84, v94, v95
	v_cvt_pk_bf16_f32 v85, v96, v97
	global_store_dwordx4 v[92:93], v[82:85], off offset:256
	s_nop 1
	v_or_b32_e32 v82, 48, v162
	v_mad_i64_i32 v[84:85], s[0:1], v82, s15, v[172:173]
	v_lshl_add_u64 v[84:85], v[84:85], 0, s[2:3]
	v_lshl_add_u64 v[86:87], v[84:85], 0, v[158:159]
	global_load_dwordx4 v[92:95], v[86:87], off
	v_ashrrev_i32_e32 v83, 31, v82
	v_lshlrev_b64 v[100:101], 12, v[82:83]
	v_lshl_add_u64 v[82:83], s[42:43], 0, v[100:101]
	v_lshl_add_u64 v[82:83], v[82:83], 0, v[158:159]
	global_load_dwordx4 v[96:99], v[82:83], off
	v_lshl_add_u64 v[84:85], v[84:85], 0, v[160:161]
	global_load_dwordx4 v[86:89], v[84:85], off
	s_nop 0
	global_load_dwordx4 v[82:85], v[82:83], off offset:256
	s_waitcnt vmcnt(3)
	v_lshlrev_b32_e32 v102, 16, v92
	v_and_b32_e32 v92, 0xffff0000, v92
	v_mul_f32_e32 v102, 0xbfb8aa3b, v102
	v_mul_f32_e32 v92, 0xbfb8aa3b, v92
	v_exp_f32_e32 v102, v102
	v_exp_f32_e32 v103, v92
	s_waitcnt vmcnt(2)
	v_lshlrev_b32_e32 v104, 16, v96
	v_and_b32_e32 v105, 0xffff0000, v96
	v_pk_add_f32 v[102:103], v[102:103], 1.0 op_sel_hi:[1,0]
	s_nop 0
	v_rcp_f32_e32 v103, v103
	v_rcp_f32_e32 v102, v102
	v_lshlrev_b32_e32 v92, 16, v93
	v_and_b32_e32 v93, 0xffff0000, v93
	v_mul_f32_e32 v92, 0xbfb8aa3b, v92
	v_mul_f32_e32 v93, 0xbfb8aa3b, v93
	v_exp_f32_e32 v92, v92
	v_exp_f32_e32 v93, v93
	v_pk_fma_f32 v[78:79], v[78:79], v[102:103], v[104:105]
	v_lshlrev_b32_e32 v96, 16, v97
	v_and_b32_e32 v97, 0xffff0000, v97
	v_pk_add_f32 v[92:93], v[92:93], 1.0 op_sel_hi:[1,0]
	s_nop 0
	v_rcp_f32_e32 v93, v93
	v_rcp_f32_e32 v92, v92
	s_nop 0
	v_pk_fma_f32 v[80:81], v[80:81], v[92:93], v[96:97]
	v_lshlrev_b32_e32 v92, 16, v94
	v_and_b32_e32 v93, 0xffff0000, v94
	v_mul_f32_e32 v92, 0xbfb8aa3b, v92
	v_mul_f32_e32 v93, 0xbfb8aa3b, v93
	v_exp_f32_e32 v92, v92
	v_exp_f32_e32 v93, v93
	v_lshlrev_b32_e32 v96, 16, v98
	v_and_b32_e32 v97, 0xffff0000, v98
	v_pk_add_f32 v[92:93], v[92:93], 1.0 op_sel_hi:[1,0]
	s_nop 0
	v_rcp_f32_e32 v93, v93
	v_rcp_f32_e32 v92, v92
	s_nop 0
	v_pk_fma_f32 v[74:75], v[74:75], v[92:93], v[96:97]
	v_lshlrev_b32_e32 v92, 16, v95
	v_and_b32_e32 v93, 0xffff0000, v95
	v_mul_f32_e32 v92, 0xbfb8aa3b, v92
	v_mul_f32_e32 v93, 0xbfb8aa3b, v93
	v_exp_f32_e32 v92, v92
	v_exp_f32_e32 v93, v93
	v_lshlrev_b32_e32 v94, 16, v99
	v_and_b32_e32 v95, 0xffff0000, v99
	v_pk_add_f32 v[92:93], v[92:93], 1.0 op_sel_hi:[1,0]
	s_nop 0
	v_rcp_f32_e32 v93, v93
	v_rcp_f32_e32 v92, v92
	s_nop 0
	v_pk_fma_f32 v[92:93], v[76:77], v[92:93], v[94:95]
	v_cvt_pk_bf16_f32 v76, v78, v79
	v_cvt_pk_bf16_f32 v78, v74, v75
	v_lshl_add_u64 v[74:75], s[8:9], 0, v[100:101]
	v_cvt_pk_bf16_f32 v77, v80, v81
	v_cvt_pk_bf16_f32 v79, v92, v93
	v_lshl_add_u64 v[74:75], v[74:75], 0, v[158:159]
	global_store_dwordx4 v[74:75], v[76:79], off
	s_waitcnt vmcnt(2)
; DI unsigned pk2(float a, float b) { f32x2 v = {a, b}; bf16x2_t r = __builtin_convertvector(v, bf16x2_t); return __builtin_bit_cast(unsigned, r); }
; DI float sigmoidf_(float x) { return 1.f / (1.f + __expf(-x)); }
;     DI void operator()(const f32x4 (&acc)[2][2][4][2], const Unit& u, int wr, int wc, int fr, int fq) const {
;         const int row0 = u.pm * BM + wr * 64 + fr, col0 = u.pn * BM + wc * 32 + 8 * fq;
; #pragma unroll
;         for (int ai = 0; ai < 2; ++ai)
; #pragma unroll
;             for (int m = 0; m < 4; ++m) { const size_t row = (size_t)(row0 + ai * HALF + m * 16);
;                 u32x4 gzs[2], ts[2];
; #pragma unroll
;                 for (int bj = 0; bj < 2; ++bj) { const int col = col0 + bj * HALF; gzs[bj] = *(const u32x4*)(Zg + row * NZ + goff + col); if (add) ts[bj] = *(const u32x4*)(add + row * D + col); else ts[bj] = (u32x4){0u, 0u, 0u, 0u}; }
; #pragma unroll
;                 for (int bj = 0; bj < 2; ++bj) {
;                     const int col = col0 + bj * HALF;
;                     const u32x4 gz = gzs[bj];
;                     float a[8] = {0.f, 0.f, 0.f, 0.f, 0.f, 0.f, 0.f, 0.f};
;                     if (add) { const u32x4 t = ts[bj]; a[0] = bflo(t.x); a[1] = bfhi(t.x); a[2] = bflo(t.y); a[3] = bfhi(t.y); a[4] = bflo(t.z); a[5] = bfhi(t.z); a[6] = bflo(t.w); a[7] = bfhi(t.w); }
;                     const f32x4 v0 = acc[ai][bj][m][0], v1 = acc[ai][bj][m][1];
;                     float o[8];
;                     o[0] = a[0] + sigmoidf_(bflo(gz.x)) * v0[0]; o[1] = a[1] + sigmoidf_(bfhi(gz.x)) * v0[1];
;                     o[2] = a[2] + sigmoidf_(bflo(gz.y)) * v0[2]; o[3] = a[3] + sigmoidf_(bfhi(gz.y)) * v0[3];
;                     o[4] = a[4] + sigmoidf_(bflo(gz.z)) * v1[0]; o[5] = a[5] + sigmoidf_(bfhi(gz.z)) * v1[1];
;                     o[6] = a[6] + sigmoidf_(bflo(gz.w)) * v1[2]; o[7] = a[7] + sigmoidf_(bfhi(gz.w)) * v1[3];
;                     u32x4 w; w.x = pk2(o[0], o[1]); w.y = pk2(o[2], o[3]); w.z = pk2(o[4], o[5]); w.w = pk2(o[6], o[7]);
;                     *(u32x4*)(O + row * D + col) = w; } }
	s_nop 0
	v_lshlrev_b32_e32 v76, 16, v86
	v_and_b32_e32 v77, 0xffff0000, v86
	v_mul_f32_e32 v76, 0xbfb8aa3b, v76
	v_mul_f32_e32 v77, 0xbfb8aa3b, v77
	v_exp_f32_e32 v76, v76
	v_exp_f32_e32 v77, v77
	s_waitcnt vmcnt(1)
	v_lshlrev_b32_e32 v78, 16, v82
	v_and_b32_e32 v79, 0xffff0000, v82
	v_pk_add_f32 v[76:77], v[76:77], 1.0 op_sel_hi:[1,0]
	s_nop 0
	v_rcp_f32_e32 v77, v77
	v_rcp_f32_e32 v76, v76
	s_nop 0
	v_pk_fma_f32 v[70:71], v[70:71], v[76:77], v[78:79]
	v_lshlrev_b32_e32 v76, 16, v87
	v_and_b32_e32 v77, 0xffff0000, v87
	v_mul_f32_e32 v76, 0xbfb8aa3b, v76
	v_mul_f32_e32 v77, 0xbfb8aa3b, v77
	v_exp_f32_e32 v76, v76
	v_exp_f32_e32 v77, v77
	v_lshlrev_b32_e32 v78, 16, v83
	v_and_b32_e32 v79, 0xffff0000, v83
	v_pk_add_f32 v[76:77], v[76:77], 1.0 op_sel_hi:[1,0]
	s_nop 0
	v_rcp_f32_e32 v77, v77
	v_rcp_f32_e32 v76, v76
	s_nop 0
	v_pk_fma_f32 v[72:73], v[72:73], v[76:77], v[78:79]
	v_lshlrev_b32_e32 v76, 16, v88
	v_and_b32_e32 v77, 0xffff0000, v88
	v_mul_f32_e32 v76, 0xbfb8aa3b, v76
	v_mul_f32_e32 v77, 0xbfb8aa3b, v77
	v_exp_f32_e32 v76, v76
	v_exp_f32_e32 v77, v77
	v_lshlrev_b32_e32 v78, 16, v84
	v_and_b32_e32 v79, 0xffff0000, v84
	v_pk_add_f32 v[76:77], v[76:77], 1.0 op_sel_hi:[1,0]
	s_nop 0
	v_rcp_f32_e32 v77, v77
	v_rcp_f32_e32 v76, v76
	s_nop 0
	v_pk_fma_f32 v[76:77], v[66:67], v[76:77], v[78:79]
	v_lshlrev_b32_e32 v66, 16, v89
	v_and_b32_e32 v67, 0xffff0000, v89
	v_mul_f32_e32 v66, 0xbfb8aa3b, v66
	v_mul_f32_e32 v67, 0xbfb8aa3b, v67
	v_exp_f32_e32 v66, v66
	v_exp_f32_e32 v67, v67
	v_lshlrev_b32_e32 v78, 16, v85
	v_and_b32_e32 v79, 0xffff0000, v85
	v_pk_add_f32 v[66:67], v[66:67], 1.0 op_sel_hi:[1,0]
	s_nop 0
	v_rcp_f32_e32 v67, v67
	v_rcp_f32_e32 v66, v66
	s_nop 0
	v_pk_fma_f32 v[78:79], v[68:69], v[66:67], v[78:79]
	v_cvt_pk_bf16_f32 v66, v70, v71
	v_cvt_pk_bf16_f32 v67, v72, v73
	v_cvt_pk_bf16_f32 v68, v76, v77
	v_cvt_pk_bf16_f32 v69, v78, v79
	global_store_dwordx4 v[74:75], v[66:69], off offset:256
	s_nop 1
	v_add_u32_e32 v66, 0x80, v162
	v_mad_i64_i32 v[68:69], s[0:1], v66, s15, v[172:173]
	v_lshl_add_u64 v[68:69], v[68:69], 0, s[2:3]
	v_lshl_add_u64 v[70:71], v[68:69], 0, v[158:159]
	global_load_dwordx4 v[74:77], v[70:71], off
	v_ashrrev_i32_e32 v67, 31, v66
	v_lshlrev_b64 v[82:83], 12, v[66:67]
	v_lshl_add_u64 v[66:67], s[42:43], 0, v[82:83]
	v_lshl_add_u64 v[66:67], v[66:67], 0, v[158:159]
	global_load_dwordx4 v[78:81], v[66:67], off
	v_lshl_add_u64 v[68:69], v[68:69], 0, v[160:161]
	global_load_dwordx4 v[70:73], v[68:69], off
	s_nop 0
	global_load_dwordx4 v[66:69], v[66:67], off offset:256
	s_waitcnt vmcnt(3)
	v_lshlrev_b32_e32 v84, 16, v74
	v_and_b32_e32 v74, 0xffff0000, v74
	v_mul_f32_e32 v84, 0xbfb8aa3b, v84
	v_mul_f32_e32 v74, 0xbfb8aa3b, v74
	v_exp_f32_e32 v84, v84
	v_exp_f32_e32 v85, v74
	s_waitcnt vmcnt(2)
	v_lshlrev_b32_e32 v86, 16, v78
	v_and_b32_e32 v87, 0xffff0000, v78
	v_pk_add_f32 v[84:85], v[84:85], 1.0 op_sel_hi:[1,0]
	s_nop 0
	v_rcp_f32_e32 v85, v85
	v_rcp_f32_e32 v84, v84
	v_lshlrev_b32_e32 v74, 16, v75
	v_and_b32_e32 v75, 0xffff0000, v75
	v_mul_f32_e32 v74, 0xbfb8aa3b, v74
	v_mul_f32_e32 v75, 0xbfb8aa3b, v75
	v_exp_f32_e32 v74, v74
	v_exp_f32_e32 v75, v75
	v_pk_fma_f32 v[62:63], v[62:63], v[84:85], v[86:87]
	v_lshlrev_b32_e32 v78, 16, v79
	v_and_b32_e32 v79, 0xffff0000, v79
	v_pk_add_f32 v[74:75], v[74:75], 1.0 op_sel_hi:[1,0]
	s_nop 0
	v_rcp_f32_e32 v75, v75
	v_rcp_f32_e32 v74, v74
	s_nop 0
	v_pk_fma_f32 v[64:65], v[64:65], v[74:75], v[78:79]
	v_lshlrev_b32_e32 v74, 16, v76
	v_and_b32_e32 v75, 0xffff0000, v76
	v_mul_f32_e32 v74, 0xbfb8aa3b, v74
	v_mul_f32_e32 v75, 0xbfb8aa3b, v75
	v_exp_f32_e32 v74, v74
	v_exp_f32_e32 v75, v75
	v_lshlrev_b32_e32 v78, 16, v80
	v_and_b32_e32 v79, 0xffff0000, v80
	v_pk_add_f32 v[74:75], v[74:75], 1.0 op_sel_hi:[1,0]
	s_nop 0
	v_rcp_f32_e32 v75, v75
	v_rcp_f32_e32 v74, v74
	s_nop 0
	v_pk_fma_f32 v[58:59], v[58:59], v[74:75], v[78:79]
	v_lshlrev_b32_e32 v74, 16, v77
	v_and_b32_e32 v75, 0xffff0000, v77
	v_mul_f32_e32 v74, 0xbfb8aa3b, v74
	v_mul_f32_e32 v75, 0xbfb8aa3b, v75
	v_exp_f32_e32 v74, v74
	v_exp_f32_e32 v75, v75
	v_lshlrev_b32_e32 v76, 16, v81
	v_and_b32_e32 v77, 0xffff0000, v81
	v_pk_add_f32 v[74:75], v[74:75], 1.0 op_sel_hi:[1,0]
	s_nop 0
	v_rcp_f32_e32 v75, v75
	v_rcp_f32_e32 v74, v74
	s_nop 0
	v_pk_fma_f32 v[74:75], v[60:61], v[74:75], v[76:77]
	v_cvt_pk_bf16_f32 v60, v62, v63
	v_cvt_pk_bf16_f32 v62, v58, v59
	v_lshl_add_u64 v[58:59], s[8:9], 0, v[82:83]
	v_cvt_pk_bf16_f32 v61, v64, v65
	v_cvt_pk_bf16_f32 v63, v74, v75
	v_lshl_add_u64 v[58:59], v[58:59], 0, v[158:159]
	global_store_dwordx4 v[58:59], v[60:63], off
	s_waitcnt vmcnt(2)
	s_nop 0
	v_lshlrev_b32_e32 v60, 16, v70
	v_and_b32_e32 v61, 0xffff0000, v70
	v_mul_f32_e32 v60, 0xbfb8aa3b, v60
	v_mul_f32_e32 v61, 0xbfb8aa3b, v61
	v_exp_f32_e32 v60, v60
	v_exp_f32_e32 v61, v61
	s_waitcnt vmcnt(1)
; DI unsigned pk2(float a, float b) { f32x2 v = {a, b}; bf16x2_t r = __builtin_convertvector(v, bf16x2_t); return __builtin_bit_cast(unsigned, r); }
; DI float sigmoidf_(float x) { return 1.f / (1.f + __expf(-x)); }
;     DI void operator()(const f32x4 (&acc)[2][2][4][2], const Unit& u, int wr, int wc, int fr, int fq) const {
;     ...
;                 for (int bj = 0; bj < 2; ++bj) { const int col = col0 + bj * HALF; gzs[bj] = *(const u32x4*)(Zg + row * NZ + goff + col); if (add) ts[bj] = *(const u32x4*)(add + row * D + col); else ts[bj] = (u32x4){0u, 0u, 0u, 0u}; }
; #pragma unroll
;                 for (int bj = 0; bj < 2; ++bj) {
;                     const int col = col0 + bj * HALF;
;                     const u32x4 gz = gzs[bj];
;                     float a[8] = {0.f, 0.f, 0.f, 0.f, 0.f, 0.f, 0.f, 0.f};
;                     if (add) { const u32x4 t = ts[bj]; a[0] = bflo(t.x); a[1] = bfhi(t.x); a[2] = bflo(t.y); a[3] = bfhi(t.y); a[4] = bflo(t.z); a[5] = bfhi(t.z); a[6] = bflo(t.w); a[7] = bfhi(t.w); }
;                     const f32x4 v0 = acc[ai][bj][m][0], v1 = acc[ai][bj][m][1];
;                     float o[8];
;                     o[0] = a[0] + sigmoidf_(bflo(gz.x)) * v0[0]; o[1] = a[1] + sigmoidf_(bfhi(gz.x)) * v0[1];
;                     o[2] = a[2] + sigmoidf_(bflo(gz.y)) * v0[2]; o[3] = a[3] + sigmoidf_(bfhi(gz.y)) * v0[3];
;                     o[4] = a[4] + sigmoidf_(bflo(gz.z)) * v1[0]; o[5] = a[5] + sigmoidf_(bfhi(gz.z)) * v1[1];
;                     o[6] = a[6] + sigmoidf_(bflo(gz.w)) * v1[2]; o[7] = a[7] + sigmoidf_(bfhi(gz.w)) * v1[3];
;                     u32x4 w; w.x = pk2(o[0], o[1]); w.y = pk2(o[2], o[3]); w.z = pk2(o[4], o[5]); w.w = pk2(o[6], o[7]);
;                     *(u32x4*)(O + row * D + col) = w; } }
	v_lshlrev_b32_e32 v62, 16, v66
	v_and_b32_e32 v63, 0xffff0000, v66
	v_pk_add_f32 v[60:61], v[60:61], 1.0 op_sel_hi:[1,0]
	s_nop 0
	v_rcp_f32_e32 v61, v61
	v_rcp_f32_e32 v60, v60
	s_nop 0
	v_pk_fma_f32 v[54:55], v[54:55], v[60:61], v[62:63]
	v_lshlrev_b32_e32 v60, 16, v71
	v_and_b32_e32 v61, 0xffff0000, v71
	v_mul_f32_e32 v60, 0xbfb8aa3b, v60
	v_mul_f32_e32 v61, 0xbfb8aa3b, v61
	v_exp_f32_e32 v60, v60
	v_exp_f32_e32 v61, v61
	v_lshlrev_b32_e32 v62, 16, v67
	v_and_b32_e32 v63, 0xffff0000, v67
	v_pk_add_f32 v[60:61], v[60:61], 1.0 op_sel_hi:[1,0]
	s_nop 0
	v_rcp_f32_e32 v61, v61
	v_rcp_f32_e32 v60, v60
	s_nop 0
	v_pk_fma_f32 v[56:57], v[56:57], v[60:61], v[62:63]
	v_lshlrev_b32_e32 v60, 16, v72
	v_and_b32_e32 v61, 0xffff0000, v72
	v_mul_f32_e32 v60, 0xbfb8aa3b, v60
	v_mul_f32_e32 v61, 0xbfb8aa3b, v61
	v_exp_f32_e32 v60, v60
	v_exp_f32_e32 v61, v61
	v_lshlrev_b32_e32 v62, 16, v68
	v_and_b32_e32 v63, 0xffff0000, v68
	v_pk_add_f32 v[60:61], v[60:61], 1.0 op_sel_hi:[1,0]
	s_nop 0
	v_rcp_f32_e32 v61, v61
	v_rcp_f32_e32 v60, v60
	s_nop 0
	v_pk_fma_f32 v[60:61], v[50:51], v[60:61], v[62:63]
	v_lshlrev_b32_e32 v50, 16, v73
	v_and_b32_e32 v51, 0xffff0000, v73
	v_mul_f32_e32 v50, 0xbfb8aa3b, v50
	v_mul_f32_e32 v51, 0xbfb8aa3b, v51
	v_exp_f32_e32 v50, v50
	v_exp_f32_e32 v51, v51
	v_lshlrev_b32_e32 v62, 16, v69
	v_and_b32_e32 v63, 0xffff0000, v69
	v_pk_add_f32 v[50:51], v[50:51], 1.0 op_sel_hi:[1,0]
	s_nop 0
	v_rcp_f32_e32 v51, v51
	v_rcp_f32_e32 v50, v50
	s_nop 0
	v_pk_fma_f32 v[62:63], v[52:53], v[50:51], v[62:63]
	v_cvt_pk_bf16_f32 v50, v54, v55
	v_cvt_pk_bf16_f32 v51, v56, v57
	v_cvt_pk_bf16_f32 v52, v60, v61
	v_cvt_pk_bf16_f32 v53, v62, v63
	global_store_dwordx4 v[58:59], v[50:53], off offset:256
	s_nop 1
	v_add_u32_e32 v50, 0x90, v162
	v_mad_i64_i32 v[52:53], s[0:1], v50, s15, v[172:173]
	v_lshl_add_u64 v[52:53], v[52:53], 0, s[2:3]
	v_lshl_add_u64 v[54:55], v[52:53], 0, v[158:159]
	global_load_dwordx4 v[58:61], v[54:55], off
	v_ashrrev_i32_e32 v51, 31, v50
	v_lshlrev_b64 v[66:67], 12, v[50:51]
	v_lshl_add_u64 v[50:51], s[42:43], 0, v[66:67]
	v_lshl_add_u64 v[50:51], v[50:51], 0, v[158:159]
	global_load_dwordx4 v[62:65], v[50:51], off
	v_lshl_add_u64 v[52:53], v[52:53], 0, v[160:161]
	global_load_dwordx4 v[54:57], v[52:53], off
	s_nop 0
	global_load_dwordx4 v[50:53], v[50:51], off offset:256
	s_waitcnt vmcnt(3)
	v_lshlrev_b32_e32 v68, 16, v58
	v_and_b32_e32 v58, 0xffff0000, v58
	v_mul_f32_e32 v68, 0xbfb8aa3b, v68
	v_mul_f32_e32 v58, 0xbfb8aa3b, v58
	v_exp_f32_e32 v68, v68
	v_exp_f32_e32 v69, v58
	s_waitcnt vmcnt(2)
	v_lshlrev_b32_e32 v70, 16, v62
	v_and_b32_e32 v71, 0xffff0000, v62
	v_pk_add_f32 v[68:69], v[68:69], 1.0 op_sel_hi:[1,0]
	s_nop 0
	v_rcp_f32_e32 v69, v69
	v_rcp_f32_e32 v68, v68
	v_lshlrev_b32_e32 v58, 16, v59
	v_and_b32_e32 v59, 0xffff0000, v59
	v_mul_f32_e32 v58, 0xbfb8aa3b, v58
	v_mul_f32_e32 v59, 0xbfb8aa3b, v59
	v_exp_f32_e32 v58, v58
	v_exp_f32_e32 v59, v59
	v_pk_fma_f32 v[46:47], v[46:47], v[68:69], v[70:71]
	v_lshlrev_b32_e32 v62, 16, v63
	v_and_b32_e32 v63, 0xffff0000, v63
	v_pk_add_f32 v[58:59], v[58:59], 1.0 op_sel_hi:[1,0]
	s_nop 0
	v_rcp_f32_e32 v59, v59
	v_rcp_f32_e32 v58, v58
	s_nop 0
	v_pk_fma_f32 v[48:49], v[48:49], v[58:59], v[62:63]
	v_lshlrev_b32_e32 v58, 16, v60
	v_and_b32_e32 v59, 0xffff0000, v60
	v_mul_f32_e32 v58, 0xbfb8aa3b, v58
	v_mul_f32_e32 v59, 0xbfb8aa3b, v59
	v_exp_f32_e32 v58, v58
	v_exp_f32_e32 v59, v59
	v_lshlrev_b32_e32 v62, 16, v64
	v_and_b32_e32 v63, 0xffff0000, v64
	v_pk_add_f32 v[58:59], v[58:59], 1.0 op_sel_hi:[1,0]
	s_nop 0
	v_rcp_f32_e32 v59, v59
	v_rcp_f32_e32 v58, v58
	s_nop 0
	v_pk_fma_f32 v[42:43], v[42:43], v[58:59], v[62:63]
	v_lshlrev_b32_e32 v58, 16, v61
	v_and_b32_e32 v59, 0xffff0000, v61
	v_mul_f32_e32 v58, 0xbfb8aa3b, v58
	v_mul_f32_e32 v59, 0xbfb8aa3b, v59
	v_exp_f32_e32 v58, v58
	v_exp_f32_e32 v59, v59
	v_lshlrev_b32_e32 v60, 16, v65
	v_and_b32_e32 v61, 0xffff0000, v65
	v_pk_add_f32 v[58:59], v[58:59], 1.0 op_sel_hi:[1,0]
	s_nop 0
	v_rcp_f32_e32 v59, v59
	v_rcp_f32_e32 v58, v58
	s_nop 0
	v_pk_fma_f32 v[58:59], v[44:45], v[58:59], v[60:61]
	v_cvt_pk_bf16_f32 v44, v46, v47
	v_cvt_pk_bf16_f32 v46, v42, v43
	v_lshl_add_u64 v[42:43], s[8:9], 0, v[66:67]
	v_cvt_pk_bf16_f32 v45, v48, v49
	v_cvt_pk_bf16_f32 v47, v58, v59
	v_lshl_add_u64 v[42:43], v[42:43], 0, v[158:159]
	global_store_dwordx4 v[42:43], v[44:47], off
	s_waitcnt vmcnt(2)
	s_nop 0
	v_lshlrev_b32_e32 v44, 16, v54
	v_and_b32_e32 v45, 0xffff0000, v54
	v_mul_f32_e32 v44, 0xbfb8aa3b, v44
	v_mul_f32_e32 v45, 0xbfb8aa3b, v45
	v_exp_f32_e32 v44, v44
	v_exp_f32_e32 v45, v45
	s_waitcnt vmcnt(1)
; DI unsigned pk2(float a, float b) { f32x2 v = {a, b}; bf16x2_t r = __builtin_convertvector(v, bf16x2_t); return __builtin_bit_cast(unsigned, r); }
; DI float sigmoidf_(float x) { return 1.f / (1.f + __expf(-x)); }
;     DI void operator()(const f32x4 (&acc)[2][2][4][2], const Unit& u, int wr, int wc, int fr, int fq) const {
;     ...
;                 for (int bj = 0; bj < 2; ++bj) { const int col = col0 + bj * HALF; gzs[bj] = *(const u32x4*)(Zg + row * NZ + goff + col); if (add) ts[bj] = *(const u32x4*)(add + row * D + col); else ts[bj] = (u32x4){0u, 0u, 0u, 0u}; }
; #pragma unroll
;                 for (int bj = 0; bj < 2; ++bj) {
;                     const int col = col0 + bj * HALF;
;                     const u32x4 gz = gzs[bj];
;                     float a[8] = {0.f, 0.f, 0.f, 0.f, 0.f, 0.f, 0.f, 0.f};
;                     if (add) { const u32x4 t = ts[bj]; a[0] = bflo(t.x); a[1] = bfhi(t.x); a[2] = bflo(t.y); a[3] = bfhi(t.y); a[4] = bflo(t.z); a[5] = bfhi(t.z); a[6] = bflo(t.w); a[7] = bfhi(t.w); }
;                     const f32x4 v0 = acc[ai][bj][m][0], v1 = acc[ai][bj][m][1];
;                     float o[8];
;                     o[0] = a[0] + sigmoidf_(bflo(gz.x)) * v0[0]; o[1] = a[1] + sigmoidf_(bfhi(gz.x)) * v0[1];
;                     o[2] = a[2] + sigmoidf_(bflo(gz.y)) * v0[2]; o[3] = a[3] + sigmoidf_(bfhi(gz.y)) * v0[3];
;                     o[4] = a[4] + sigmoidf_(bflo(gz.z)) * v1[0]; o[5] = a[5] + sigmoidf_(bfhi(gz.z)) * v1[1];
;                     o[6] = a[6] + sigmoidf_(bflo(gz.w)) * v1[2]; o[7] = a[7] + sigmoidf_(bfhi(gz.w)) * v1[3];
;                     u32x4 w; w.x = pk2(o[0], o[1]); w.y = pk2(o[2], o[3]); w.z = pk2(o[4], o[5]); w.w = pk2(o[6], o[7]);
;                     *(u32x4*)(O + row * D + col) = w; } }
	v_lshlrev_b32_e32 v46, 16, v50
	v_and_b32_e32 v47, 0xffff0000, v50
	v_pk_add_f32 v[44:45], v[44:45], 1.0 op_sel_hi:[1,0]
	s_nop 0
	v_rcp_f32_e32 v45, v45
	v_rcp_f32_e32 v44, v44
	s_nop 0
	v_pk_fma_f32 v[38:39], v[38:39], v[44:45], v[46:47]
	v_lshlrev_b32_e32 v44, 16, v55
	v_and_b32_e32 v45, 0xffff0000, v55
	v_mul_f32_e32 v44, 0xbfb8aa3b, v44
	v_mul_f32_e32 v45, 0xbfb8aa3b, v45
	v_exp_f32_e32 v44, v44
	v_exp_f32_e32 v45, v45
	v_lshlrev_b32_e32 v46, 16, v51
	v_and_b32_e32 v47, 0xffff0000, v51
	v_pk_add_f32 v[44:45], v[44:45], 1.0 op_sel_hi:[1,0]
	s_nop 0
	v_rcp_f32_e32 v45, v45
	v_rcp_f32_e32 v44, v44
	s_nop 0
	v_pk_fma_f32 v[40:41], v[40:41], v[44:45], v[46:47]
	v_lshlrev_b32_e32 v44, 16, v56
	v_and_b32_e32 v45, 0xffff0000, v56
	v_mul_f32_e32 v44, 0xbfb8aa3b, v44
	v_mul_f32_e32 v45, 0xbfb8aa3b, v45
	v_exp_f32_e32 v44, v44
	v_exp_f32_e32 v45, v45
	v_lshlrev_b32_e32 v46, 16, v52
	v_and_b32_e32 v47, 0xffff0000, v52
	v_pk_add_f32 v[44:45], v[44:45], 1.0 op_sel_hi:[1,0]
	s_nop 0
	v_rcp_f32_e32 v45, v45
	v_rcp_f32_e32 v44, v44
	s_nop 0
	v_pk_fma_f32 v[44:45], v[34:35], v[44:45], v[46:47]
	v_lshlrev_b32_e32 v34, 16, v57
	v_and_b32_e32 v35, 0xffff0000, v57
	v_mul_f32_e32 v34, 0xbfb8aa3b, v34
	v_mul_f32_e32 v35, 0xbfb8aa3b, v35
	v_exp_f32_e32 v34, v34
	v_exp_f32_e32 v35, v35
	v_lshlrev_b32_e32 v46, 16, v53
	v_and_b32_e32 v47, 0xffff0000, v53
	v_pk_add_f32 v[34:35], v[34:35], 1.0 op_sel_hi:[1,0]
	s_nop 0
	v_rcp_f32_e32 v35, v35
	v_rcp_f32_e32 v34, v34
	s_nop 0
	v_pk_fma_f32 v[46:47], v[36:37], v[34:35], v[46:47]
	v_cvt_pk_bf16_f32 v34, v38, v39
	v_cvt_pk_bf16_f32 v35, v40, v41
	v_cvt_pk_bf16_f32 v36, v44, v45
	v_cvt_pk_bf16_f32 v37, v46, v47
	global_store_dwordx4 v[42:43], v[34:37], off offset:256
	s_nop 1
	v_add_u32_e32 v34, 0xa0, v162
	v_mad_i64_i32 v[36:37], s[0:1], v34, s15, v[172:173]
	v_lshl_add_u64 v[36:37], v[36:37], 0, s[2:3]
	v_lshl_add_u64 v[38:39], v[36:37], 0, v[158:159]
	global_load_dwordx4 v[42:45], v[38:39], off
	v_ashrrev_i32_e32 v35, 31, v34
	v_lshlrev_b64 v[50:51], 12, v[34:35]
	v_lshl_add_u64 v[34:35], s[42:43], 0, v[50:51]
	v_lshl_add_u64 v[34:35], v[34:35], 0, v[158:159]
	global_load_dwordx4 v[46:49], v[34:35], off
	v_lshl_add_u64 v[36:37], v[36:37], 0, v[160:161]
	global_load_dwordx4 v[38:41], v[36:37], off
	s_nop 0
	global_load_dwordx4 v[34:37], v[34:35], off offset:256
	s_waitcnt vmcnt(3)
	v_lshlrev_b32_e32 v52, 16, v42
	v_and_b32_e32 v42, 0xffff0000, v42
	v_mul_f32_e32 v52, 0xbfb8aa3b, v52
	v_mul_f32_e32 v42, 0xbfb8aa3b, v42
	v_exp_f32_e32 v52, v52
	v_exp_f32_e32 v53, v42
	s_waitcnt vmcnt(2)
	v_lshlrev_b32_e32 v54, 16, v46
	v_and_b32_e32 v55, 0xffff0000, v46
	v_pk_add_f32 v[52:53], v[52:53], 1.0 op_sel_hi:[1,0]
	s_nop 0
	v_rcp_f32_e32 v53, v53
	v_rcp_f32_e32 v52, v52
	v_lshlrev_b32_e32 v42, 16, v43
	v_and_b32_e32 v43, 0xffff0000, v43
	v_mul_f32_e32 v42, 0xbfb8aa3b, v42
	v_mul_f32_e32 v43, 0xbfb8aa3b, v43
	v_exp_f32_e32 v42, v42
	v_exp_f32_e32 v43, v43
	v_pk_fma_f32 v[30:31], v[30:31], v[52:53], v[54:55]
	v_lshlrev_b32_e32 v46, 16, v47
	v_and_b32_e32 v47, 0xffff0000, v47
	v_pk_add_f32 v[42:43], v[42:43], 1.0 op_sel_hi:[1,0]
	s_nop 0
	v_rcp_f32_e32 v43, v43
	v_rcp_f32_e32 v42, v42
	s_nop 0
	v_pk_fma_f32 v[32:33], v[32:33], v[42:43], v[46:47]
	v_lshlrev_b32_e32 v42, 16, v44
	v_and_b32_e32 v43, 0xffff0000, v44
	v_mul_f32_e32 v42, 0xbfb8aa3b, v42
	v_mul_f32_e32 v43, 0xbfb8aa3b, v43
	v_exp_f32_e32 v42, v42
	v_exp_f32_e32 v43, v43
	v_lshlrev_b32_e32 v46, 16, v48
	v_and_b32_e32 v47, 0xffff0000, v48
	v_pk_add_f32 v[42:43], v[42:43], 1.0 op_sel_hi:[1,0]
	s_nop 0
	v_rcp_f32_e32 v43, v43
	v_rcp_f32_e32 v42, v42
	s_nop 0
	v_pk_fma_f32 v[26:27], v[26:27], v[42:43], v[46:47]
	v_lshlrev_b32_e32 v42, 16, v45
	v_and_b32_e32 v43, 0xffff0000, v45
	v_mul_f32_e32 v42, 0xbfb8aa3b, v42
	v_mul_f32_e32 v43, 0xbfb8aa3b, v43
	v_exp_f32_e32 v42, v42
	v_exp_f32_e32 v43, v43
	v_lshlrev_b32_e32 v44, 16, v49
	v_and_b32_e32 v45, 0xffff0000, v49
	v_pk_add_f32 v[42:43], v[42:43], 1.0 op_sel_hi:[1,0]
	s_nop 0
	v_rcp_f32_e32 v43, v43
	v_rcp_f32_e32 v42, v42
	s_nop 0
	v_pk_fma_f32 v[42:43], v[28:29], v[42:43], v[44:45]
	v_cvt_pk_bf16_f32 v28, v30, v31
	v_cvt_pk_bf16_f32 v30, v26, v27
	v_lshl_add_u64 v[26:27], s[8:9], 0, v[50:51]
	v_cvt_pk_bf16_f32 v29, v32, v33
	v_cvt_pk_bf16_f32 v31, v42, v43
	v_lshl_add_u64 v[26:27], v[26:27], 0, v[158:159]
	global_store_dwordx4 v[26:27], v[28:31], off
	s_waitcnt vmcnt(2)
	s_nop 0
	v_lshlrev_b32_e32 v28, 16, v38
	v_and_b32_e32 v29, 0xffff0000, v38
	v_mul_f32_e32 v28, 0xbfb8aa3b, v28
	v_mul_f32_e32 v29, 0xbfb8aa3b, v29
	v_exp_f32_e32 v28, v28
	v_exp_f32_e32 v29, v29
	s_waitcnt vmcnt(1)
; DI float sigmoidf_(float x) { return 1.f / (1.f + __expf(-x)); }
; #define PG8_BAR __builtin_amdgcn_s_barrier()
; template <class Epi, class Sched, bool ALIGN_EPI = true, bool SP2 = true>
; __device__ __forceinline__ void gemm_phase(LAS unsigned char* lds, const Dims g, const Sched& S, const Epi& E) {
;     ...
;         if constexpr (ALIGN_EPI) { if (wr == 0) PG8_BAR; }
;         E(acc, cur, wr, wc, fr, fq);
;         if (!has_next) break;
; #pragma unroll
;         for (int a = 0; a < 2; ++a)
; #pragma unroll
;             for (int b = 0; b < 2; ++b)
; #pragma unroll
;                 for (int m = 0; m < 4; ++m)
; #pragma unroll
;                     for (int n = 0; n < 2; ++n) acc[a][b][m][n] = (f32x4){0.f, 0.f, 0.f, 0.f};
;         cur = nxt; cA = nA; cB = nB; ++ui;
;         if constexpr (ALIGN_EPI) { if (wr == 1) PG8_BAR; }
;     DI void operator()(const f32x4 (&acc)[2][2][4][2], const Unit& u, int wr, int wc, int fr, int fq) const {
;     ...
;                 for (int bj = 0; bj < 2; ++bj) { const int col = col0 + bj * HALF; gzs[bj] = *(const u32x4*)(Zg + row * NZ + goff + col); if (add) ts[bj] = *(const u32x4*)(add + row * D + col); else ts[bj] = (u32x4){0u, 0u, 0u, 0u}; }
; #pragma unroll
;                 for (int bj = 0; bj < 2; ++bj) {
;                     const int col = col0 + bj * HALF;
;                     const u32x4 gz = gzs[bj];
;                     float a[8] = {0.f, 0.f, 0.f, 0.f, 0.f, 0.f, 0.f, 0.f};
;                     if (add) { const u32x4 t = ts[bj]; a[0] = bflo(t.x); a[1] = bfhi(t.x); a[2] = bflo(t.y); a[3] = bfhi(t.y); a[4] = bflo(t.z); a[5] = bfhi(t.z); a[6] = bflo(t.w); a[7] = bfhi(t.w); }
;                     const f32x4 v0 = acc[ai][bj][m][0], v1 = acc[ai][bj][m][1];
;                     float o[8];
;                     o[0] = a[0] + sigmoidf_(bflo(gz.x)) * v0[0]; o[1] = a[1] + sigmoidf_(bfhi(gz.x)) * v0[1];
;                     o[2] = a[2] + sigmoidf_(bflo(gz.y)) * v0[2]; o[3] = a[3] + sigmoidf_(bfhi(gz.y)) * v0[3];
;                     o[4] = a[4] + sigmoidf_(bflo(gz.z)) * v1[0]; o[5] = a[5] + sigmoidf_(bfhi(gz.z)) * v1[1];
;                     o[6] = a[6] + sigmoidf_(bflo(gz.w)) * v1[2]; o[7] = a[7] + sigmoidf_(bfhi(gz.w)) * v1[3];
;                     u32x4 w; w.x = pk2(o[0], o[1]); w.y = pk2(o[2], o[3]); w.z = pk2(o[4], o[5]); w.w = pk2(o[6], o[7]);
;                     *(u32x4*)(O + row * D + col) = w; } }
	v_lshlrev_b32_e32 v30, 16, v34
	v_and_b32_e32 v31, 0xffff0000, v34
	v_pk_add_f32 v[28:29], v[28:29], 1.0 op_sel_hi:[1,0]
	s_nop 0
	v_rcp_f32_e32 v29, v29
	v_rcp_f32_e32 v28, v28
	s_nop 0
	v_pk_fma_f32 v[22:23], v[22:23], v[28:29], v[30:31]
	v_lshlrev_b32_e32 v28, 16, v39
	v_and_b32_e32 v29, 0xffff0000, v39
	v_mul_f32_e32 v28, 0xbfb8aa3b, v28
	v_mul_f32_e32 v29, 0xbfb8aa3b, v29
	v_exp_f32_e32 v28, v28
	v_exp_f32_e32 v29, v29
	v_lshlrev_b32_e32 v30, 16, v35
	v_and_b32_e32 v31, 0xffff0000, v35
	v_pk_add_f32 v[28:29], v[28:29], 1.0 op_sel_hi:[1,0]
	s_nop 0
	v_rcp_f32_e32 v29, v29
	v_rcp_f32_e32 v28, v28
	s_nop 0
	v_pk_fma_f32 v[24:25], v[24:25], v[28:29], v[30:31]
	v_lshlrev_b32_e32 v28, 16, v40
	v_and_b32_e32 v29, 0xffff0000, v40
	v_mul_f32_e32 v28, 0xbfb8aa3b, v28
	v_mul_f32_e32 v29, 0xbfb8aa3b, v29
	v_exp_f32_e32 v28, v28
	v_exp_f32_e32 v29, v29
	v_lshlrev_b32_e32 v30, 16, v36
	v_and_b32_e32 v31, 0xffff0000, v36
	v_pk_add_f32 v[28:29], v[28:29], 1.0 op_sel_hi:[1,0]
	s_nop 0
	v_rcp_f32_e32 v29, v29
	v_rcp_f32_e32 v28, v28
	s_nop 0
	v_pk_fma_f32 v[28:29], v[18:19], v[28:29], v[30:31]
	v_lshlrev_b32_e32 v18, 16, v41
	v_and_b32_e32 v19, 0xffff0000, v41
	v_mul_f32_e32 v18, 0xbfb8aa3b, v18
	v_mul_f32_e32 v19, 0xbfb8aa3b, v19
	v_exp_f32_e32 v18, v18
	v_exp_f32_e32 v19, v19
	v_lshlrev_b32_e32 v30, 16, v37
	v_and_b32_e32 v31, 0xffff0000, v37
	v_pk_add_f32 v[18:19], v[18:19], 1.0 op_sel_hi:[1,0]
	s_nop 0
	v_rcp_f32_e32 v19, v19
	v_rcp_f32_e32 v18, v18
	s_nop 0
	v_pk_fma_f32 v[30:31], v[20:21], v[18:19], v[30:31]
	v_cvt_pk_bf16_f32 v18, v22, v23
	v_cvt_pk_bf16_f32 v19, v24, v25
	v_cvt_pk_bf16_f32 v20, v28, v29
	v_cvt_pk_bf16_f32 v21, v30, v31
	global_store_dwordx4 v[26:27], v[18:21], off offset:256
	s_nop 1
	v_add_u32_e32 v18, 0xb0, v162
	v_mad_i64_i32 v[20:21], s[0:1], v18, s15, v[172:173]
	v_lshl_add_u64 v[20:21], v[20:21], 0, s[2:3]
	v_lshl_add_u64 v[22:23], v[20:21], 0, v[158:159]
	global_load_dwordx4 v[26:29], v[22:23], off
	v_ashrrev_i32_e32 v19, 31, v18
	v_lshlrev_b64 v[34:35], 12, v[18:19]
	v_lshl_add_u64 v[18:19], s[42:43], 0, v[34:35]
	v_lshl_add_u64 v[18:19], v[18:19], 0, v[158:159]
	global_load_dwordx4 v[30:33], v[18:19], off
	v_lshl_add_u64 v[20:21], v[20:21], 0, v[160:161]
	global_load_dwordx4 v[22:25], v[20:21], off
	s_nop 0
	global_load_dwordx4 v[18:21], v[18:19], off offset:256
	s_mov_b64 s[2:3], -1
	s_waitcnt vmcnt(3)
	v_lshlrev_b32_e32 v36, 16, v26
	v_and_b32_e32 v26, 0xffff0000, v26
	v_mul_f32_e32 v36, 0xbfb8aa3b, v36
	v_mul_f32_e32 v26, 0xbfb8aa3b, v26
	v_exp_f32_e32 v36, v36
	v_exp_f32_e32 v37, v26
	s_waitcnt vmcnt(2)
	v_lshlrev_b32_e32 v38, 16, v30
	v_and_b32_e32 v39, 0xffff0000, v30
	v_pk_add_f32 v[36:37], v[36:37], 1.0 op_sel_hi:[1,0]
	s_nop 0
	v_rcp_f32_e32 v37, v37
	v_rcp_f32_e32 v36, v36
	v_lshlrev_b32_e32 v26, 16, v27
	v_and_b32_e32 v27, 0xffff0000, v27
	v_mul_f32_e32 v26, 0xbfb8aa3b, v26
	v_mul_f32_e32 v27, 0xbfb8aa3b, v27
	v_exp_f32_e32 v26, v26
	v_exp_f32_e32 v27, v27
	v_pk_fma_f32 v[14:15], v[14:15], v[36:37], v[38:39]
	v_lshlrev_b32_e32 v30, 16, v31
	v_and_b32_e32 v31, 0xffff0000, v31
	v_pk_add_f32 v[26:27], v[26:27], 1.0 op_sel_hi:[1,0]
	s_nop 0
	v_rcp_f32_e32 v27, v27
	v_rcp_f32_e32 v26, v26
	s_nop 0
	v_pk_fma_f32 v[16:17], v[16:17], v[26:27], v[30:31]
	v_lshlrev_b32_e32 v26, 16, v28
	v_and_b32_e32 v27, 0xffff0000, v28
	v_mul_f32_e32 v26, 0xbfb8aa3b, v26
	v_mul_f32_e32 v27, 0xbfb8aa3b, v27
	v_exp_f32_e32 v26, v26
	v_exp_f32_e32 v27, v27
	v_lshlrev_b32_e32 v30, 16, v32
	v_and_b32_e32 v31, 0xffff0000, v32
	v_pk_add_f32 v[26:27], v[26:27], 1.0 op_sel_hi:[1,0]
	s_nop 0
	v_rcp_f32_e32 v27, v27
	v_rcp_f32_e32 v26, v26
	s_nop 0
	v_pk_fma_f32 v[10:11], v[10:11], v[26:27], v[30:31]
	v_lshlrev_b32_e32 v26, 16, v29
	v_and_b32_e32 v27, 0xffff0000, v29
	v_mul_f32_e32 v26, 0xbfb8aa3b, v26
	v_mul_f32_e32 v27, 0xbfb8aa3b, v27
	v_exp_f32_e32 v26, v26
	v_exp_f32_e32 v27, v27
	v_lshlrev_b32_e32 v28, 16, v33
	v_and_b32_e32 v29, 0xffff0000, v33
	v_pk_add_f32 v[26:27], v[26:27], 1.0 op_sel_hi:[1,0]
	s_nop 0
	v_rcp_f32_e32 v27, v27
	v_rcp_f32_e32 v26, v26
	s_nop 0
	v_pk_fma_f32 v[26:27], v[12:13], v[26:27], v[28:29]
	v_cvt_pk_bf16_f32 v12, v14, v15
	v_cvt_pk_bf16_f32 v14, v10, v11
	v_lshl_add_u64 v[10:11], s[8:9], 0, v[34:35]
	v_cvt_pk_bf16_f32 v13, v16, v17
	v_cvt_pk_bf16_f32 v15, v26, v27
	v_lshl_add_u64 v[10:11], v[10:11], 0, v[158:159]
	global_store_dwordx4 v[10:11], v[12:15], off
	s_waitcnt vmcnt(2)
	s_nop 0
	v_lshlrev_b32_e32 v12, 16, v22
	v_and_b32_e32 v13, 0xffff0000, v22
	v_mul_f32_e32 v12, 0xbfb8aa3b, v12
	v_mul_f32_e32 v13, 0xbfb8aa3b, v13
	v_exp_f32_e32 v12, v12
	v_exp_f32_e32 v13, v13
	s_waitcnt vmcnt(1)
	v_lshlrev_b32_e32 v14, 16, v18
	v_and_b32_e32 v15, 0xffff0000, v18
	v_pk_add_f32 v[12:13], v[12:13], 1.0 op_sel_hi:[1,0]
	s_nop 0
	v_rcp_f32_e32 v13, v13
	v_rcp_f32_e32 v12, v12
	s_nop 0
	v_pk_fma_f32 v[6:7], v[6:7], v[12:13], v[14:15]
	v_lshlrev_b32_e32 v12, 16, v23
	v_and_b32_e32 v13, 0xffff0000, v23
	v_mul_f32_e32 v12, 0xbfb8aa3b, v12
	v_mul_f32_e32 v13, 0xbfb8aa3b, v13
	v_exp_f32_e32 v12, v12
	v_exp_f32_e32 v13, v13
	v_lshlrev_b32_e32 v14, 16, v19
	v_and_b32_e32 v15, 0xffff0000, v19
	v_pk_add_f32 v[12:13], v[12:13], 1.0 op_sel_hi:[1,0]
	s_nop 0
	v_rcp_f32_e32 v13, v13
	v_rcp_f32_e32 v12, v12
	s_nop 0
	v_pk_fma_f32 v[8:9], v[8:9], v[12:13], v[14:15]
	v_lshlrev_b32_e32 v12, 16, v24
	v_and_b32_e32 v13, 0xffff0000, v24
	v_mul_f32_e32 v12, 0xbfb8aa3b, v12
	v_mul_f32_e32 v13, 0xbfb8aa3b, v13
	v_exp_f32_e32 v12, v12
	v_exp_f32_e32 v13, v13
	v_lshlrev_b32_e32 v14, 16, v20
	v_and_b32_e32 v15, 0xffff0000, v20
	v_pk_add_f32 v[12:13], v[12:13], 1.0 op_sel_hi:[1,0]
	s_nop 0
	v_rcp_f32_e32 v13, v13
	v_rcp_f32_e32 v12, v12
	s_nop 0
	v_pk_fma_f32 v[12:13], v[2:3], v[12:13], v[14:15]
	v_lshlrev_b32_e32 v2, 16, v25
	v_and_b32_e32 v3, 0xffff0000, v25
	v_mul_f32_e32 v2, 0xbfb8aa3b, v2
	v_mul_f32_e32 v3, 0xbfb8aa3b, v3
	v_exp_f32_e32 v2, v2
	v_exp_f32_e32 v3, v3
	v_lshlrev_b32_e32 v14, 16, v21
	v_and_b32_e32 v15, 0xffff0000, v21
	v_pk_add_f32 v[2:3], v[2:3], 1.0 op_sel_hi:[1,0]
	s_nop 0
	v_rcp_f32_e32 v3, v3
	v_rcp_f32_e32 v2, v2
	s_nop 0
	v_pk_fma_f32 v[14:15], v[4:5], v[2:3], v[14:15]
	v_cvt_pk_bf16_f32 v2, v6, v7
	v_cvt_pk_bf16_f32 v3, v8, v9
	v_cvt_pk_bf16_f32 v4, v12, v13
	v_cvt_pk_bf16_f32 v5, v14, v15
	s_andn2_b64 vcc, exec, s[38:39]
	global_store_dwordx4 v[10:11], v[2:5], off offset:256
	s_cbranch_vccnz .LBB0_1421
	s_andn2_b64 vcc, exec, s[48:49]
	s_cbranch_vccnz .LBB0_1420
	s_barrier
	s_branch .LBB0_1420

; template <class Epi>
; DI void skinny64(const bf16* A, int lda, const bf16* Bt, int ldb, int N, int K, int r0, LAS unsigned char* lds, const Epi& epi, int wave, int lane, int bid, int G) {
;     ...
;         const bf16* wp = Bt + (size_t)(16 * nt + n16) * ldb + 8 * q + wave * ksw * 32; const bf16* ap = A + (size_t)(r0 + 32 * mh + n16) * lda + 8 * q + wave * ksw * 32;
; #pragma unroll 8
;         for (int ks = 0; ks < ksw; ++ks) { const bf16x8 wf = *(const bf16x8*)(wp + ks * 32);
; #pragma unroll
;             for (int mt = 0; mt < 2; ++mt) acc[mt] = __builtin_amdgcn_mfma_f32_16x16x32_bf16(wf, *(const bf16x8*)(ap + (size_t)(16 * mt) * lda + ks * 32), acc[mt], 0, 0, 0); }
;         __syncthreads();
; #pragma unroll
;         for (int mt = 0; mt < 2; ++mt) red[(wave * 2 + mt) * 64 + lane] = acc[mt];
;         __syncthreads();
;         if (wave < 2) { f32x4 s = red[wave * 64 + lane];
; #pragma unroll
;             for (int w = 1; w < 8; ++w) s = s + red[(w * 2 + wave) * 64 + lane];
;             epi(r0 + 32 * mh + 16 * wave + n16, 16 * nt + 4 * q, s); }
.LBB0_1437:
	s_and_b32 s24, s4, -16
	v_or_b32_e32 v6, s24, v18
	v_ashrrev_i32_e32 v7, 31, v6
	s_and_b32 s25, s2, 32
	v_lshlrev_b64 v[6:7], 11, v[6:7]
	s_bitset1_b32 s25, 13
	v_lshl_add_u64 v[26:27], v[2:3], 0, v[6:7]
	v_or_b32_e32 v6, s25, v18
	v_lshlrev_b32_e32 v90, 11, v6
	v_lshl_add_u64 v[28:29], v[4:5], 0, v[90:91]
	s_mov_b32 s26, 0x8000
	v_add_co_u32_e32 v30, vcc, s26, v28
	global_load_dwordx4 v[6:9], v[26:27], off
	global_load_dwordx4 v[10:13], v[28:29], off
	v_addc_co_u32_e32 v31, vcc, 0, v29, vcc
	global_load_dwordx4 v[14:17], v[30:31], off
	global_load_dwordx4 v[108:111], v[26:27], off offset:64
	global_load_dwordx4 v[112:115], v[28:29], off offset:64
	global_load_dwordx4 v[116:119], v[30:31], off offset:64
	global_load_dwordx4 v[120:123], v[26:27], off offset:128
	global_load_dwordx4 v[124:127], v[28:29], off offset:128
	global_load_dwordx4 v[128:131], v[30:31], off offset:128
	global_load_dwordx4 v[132:135], v[26:27], off offset:192
	global_load_dwordx4 v[136:139], v[28:29], off offset:192
	global_load_dwordx4 v[140:143], v[30:31], off offset:192
	s_andn2_b64 vcc, exec, s[12:13]
	s_waitcnt vmcnt(10)
	v_mfma_f32_16x16x32_bf16 v[10:13], v[6:9], v[10:13], 0
	s_waitcnt vmcnt(9)
	v_mfma_f32_16x16x32_bf16 v[6:9], v[6:9], v[14:17], 0
	s_waitcnt vmcnt(7)
	v_mfma_f32_16x16x32_bf16 v[10:13], v[108:111], v[112:115], v[10:13]
	s_waitcnt vmcnt(6)
	v_mfma_f32_16x16x32_bf16 v[6:9], v[108:111], v[116:119], v[6:9]
	s_waitcnt vmcnt(4)
	v_mfma_f32_16x16x32_bf16 v[10:13], v[120:123], v[124:127], v[10:13]
	s_waitcnt vmcnt(3)
	v_mfma_f32_16x16x32_bf16 v[6:9], v[120:123], v[128:131], v[6:9]
	s_waitcnt vmcnt(1)
	v_mfma_f32_16x16x32_bf16 v[10:13], v[132:135], v[136:139], v[10:13]
	s_barrier
	s_waitcnt vmcnt(0)
	v_mfma_f32_16x16x32_bf16 v[6:9], v[132:135], v[140:143], v[6:9]
	s_nop 0
	v_add_u32_e32 v14, s0, v19
	s_nop 2
	ds_write_b128 v14, v[10:13]
	s_nop 2
	ds_write_b128 v14, v[6:9] offset:1024
	s_waitcnt lgkmcnt(0)
	s_barrier
	s_cbranch_vccnz .LBB0_1436
	v_add_u32_e32 v16, s1, v19
	ds_read_b128 v[6:9], v16
	ds_read_b128 v[10:13], v16 offset:2048
	s_waitcnt lgkmcnt(0)
	v_pk_add_f32 v[12:13], v[8:9], v[12:13]
	v_pk_add_f32 v[10:11], v[6:7], v[10:11]
	ds_read_b128 v[6:9], v16 offset:4096
	s_waitcnt lgkmcnt(0)
	v_pk_add_f32 v[12:13], v[12:13], v[8:9]
	v_pk_add_f32 v[10:11], v[10:11], v[6:7]
	ds_read_b128 v[6:9], v16 offset:6144
	s_waitcnt lgkmcnt(0)
	v_pk_add_f32 v[12:13], v[12:13], v[8:9]
	v_pk_add_f32 v[10:11], v[10:11], v[6:7]
	ds_read_b128 v[6:9], v16 offset:8192
	s_waitcnt lgkmcnt(0)
	v_pk_add_f32 v[12:13], v[12:13], v[8:9]
	v_pk_add_f32 v[10:11], v[10:11], v[6:7]
	ds_read_b128 v[6:9], v16 offset:10240
	s_waitcnt lgkmcnt(0)
	v_pk_add_f32 v[12:13], v[12:13], v[8:9]
	v_pk_add_f32 v[10:11], v[10:11], v[6:7]
	ds_read_b128 v[6:9], v16 offset:12288
	s_waitcnt lgkmcnt(0)
	v_pk_add_f32 v[12:13], v[12:13], v[8:9]
	v_pk_add_f32 v[14:15], v[10:11], v[6:7]
	ds_read_b128 v[8:11], v16 offset:14336
	s_waitcnt lgkmcnt(0)
	v_pk_add_f32 v[16:17], v[14:15], v[8:9]
	v_or_b32_e32 v8, s24, v21
	v_pk_add_f32 v[6:7], v[12:13], v[10:11]
	v_add_u32_e32 v10, s25, v20
	v_mov_b64_e32 v[12:13], s[40:41]
	v_ashrrev_i32_e32 v9, 31, v8
	v_mad_i64_i32 v[12:13], s[24:25], v10, s15, v[12:13]
	v_lshlrev_b64 v[8:9], 1, v[8:9]
	v_lshl_add_u64 v[12:13], v[12:13], 0, v[8:9]
	s_movk_i32 s24, 0x1000
	v_add_co_u32_e32 v12, vcc, s24, v12
	v_ashrrev_i32_e32 v11, 31, v10
	s_nop 0
	v_addc_co_u32_e32 v13, vcc, 0, v13, vcc
	global_load_dwordx2 v[14:15], v[12:13], off offset:3072
	v_lshlrev_b64 v[10:11], 12, v[10:11]
	v_lshl_add_u64 v[12:13], s[42:43], 0, v[10:11]
	v_lshl_add_u64 v[12:13], v[12:13], 0, v[8:9]
	global_load_dwordx2 v[12:13], v[12:13], off
	s_waitcnt vmcnt(1)
	v_lshlrev_b32_e32 v22, 16, v14
	v_and_b32_e32 v14, 0xffff0000, v14
	v_mul_f32_e32 v22, 0xbfb8aa3b, v22
	v_mul_f32_e32 v14, 0xbfb8aa3b, v14
	v_exp_f32_e32 v22, v22
	v_exp_f32_e32 v23, v14
	s_waitcnt vmcnt(0)
	v_lshlrev_b32_e32 v24, 16, v12
	v_and_b32_e32 v25, 0xffff0000, v12
	v_pk_add_f32 v[22:23], v[22:23], 1.0 op_sel_hi:[1,0]
	s_nop 0
	v_rcp_f32_e32 v23, v23
	v_lshlrev_b32_e32 v14, 16, v15
	v_and_b32_e32 v15, 0xffff0000, v15
	v_mul_f32_e32 v14, 0xbfb8aa3b, v14
	v_mul_f32_e32 v15, 0xbfb8aa3b, v15
	v_exp_f32_e32 v14, v14
	v_exp_f32_e32 v15, v15
	v_rcp_f32_e32 v22, v22
	s_nop 0
	v_pk_fma_f32 v[16:17], v[16:17], v[22:23], v[24:25]
	v_pk_add_f32 v[14:15], v[14:15], 1.0 op_sel_hi:[1,0]
	v_cvt_pk_bf16_f32 v12, v16, v17
	v_lshlrev_b32_e32 v16, 16, v13
	v_and_b32_e32 v17, 0xffff0000, v13
	v_rcp_f32_e32 v15, v15
	v_rcp_f32_e32 v14, v14
	s_nop 0
	v_pk_fma_f32 v[6:7], v[6:7], v[14:15], v[16:17]
	s_nop 0
	v_cvt_pk_bf16_f32 v13, v6, v7
	v_lshl_add_u64 v[6:7], s[8:9], 0, v[10:11]
	v_lshl_add_u64 v[6:7], v[6:7], 0, v[8:9]
	global_store_dwordx2 v[6:7], v[12:13], off
	s_branch .LBB0_1436

.LBB0_1720:
	s_add_i32 s0, s0, 2
	s_min_u32 s1, s0, 28
	s_lshl_b32 s12, s1, 17
	s_add_i32 s12, s12, 0x60000
	s_waitcnt vmcnt(12)
	v_cvt_pk_bf16_f32 v164, v74, v78
	s_waitcnt vmcnt(10)
	v_cvt_pk_bf16_f32 v165, v82, v86
	v_cvt_pk_bf16_f32 v166, v75, v79
	v_cvt_pk_bf16_f32 v167, v83, v87
	v_cvt_pk_bf16_f32 v190, v76, v80
	v_cvt_pk_bf16_f32 v191, v84, v88
	v_cvt_pk_bf16_f32 v192, v77, v81
	v_cvt_pk_bf16_f32 v193, v85, v89
	buffer_load_dwordx4 v[74:77], v160, s[8:11], s12 offen
	buffer_load_dwordx4 v[78:81], v90, s[8:11], s12 offen
	buffer_load_dwordx4 v[82:85], v178, s[8:11], s12 offen
	buffer_load_dwordx4 v[86:89], v179, s[8:11], s12 offen
	v_add_u32_e32 v194, 0x4000, v188
	v_add_u32_e32 v195, 0x4000, v180
	v_add_u32_e32 v214, v173, v174
	ds_write2_b64 v194, v[164:165], v[166:167] offset1:16
	ds_write2_b64 v195, v[190:191], v[192:193] offset0:32 offset1:48
	v_add_u32_e32 v215, v176, v174
	ds_read_b128 v[164:167], v214 offset:32768
	ds_read_b128 v[190:193], v214 offset:34816
	ds_read_b128 v[194:197], v214 offset:36864
	ds_read_b128 v[198:201], v215
	ds_read_b128 v[202:205], v215 offset:2048
	ds_read_b128 v[206:209], v215 offset:4096
	ds_read_b128 v[210:213], v215 offset:6144
	s_waitcnt lgkmcnt(3)
	v_mfma_f32_16x16x32_bf16 v[152:155], v[198:201], v[164:167], v[152:155]
	v_mfma_f32_16x16x32_bf16 v[62:65], v[198:201], v[190:193], v[62:65]
	v_mfma_f32_16x16x32_bf16 v[30:33], v[198:201], v[194:197], v[30:33]
	s_waitcnt lgkmcnt(2)
	v_mfma_f32_16x16x32_bf16 v[120:123], v[202:205], v[164:167], v[120:123]
	v_mfma_f32_16x16x32_bf16 v[54:57], v[202:205], v[190:193], v[54:57]
	v_mfma_f32_16x16x32_bf16 v[22:25], v[202:205], v[194:197], v[22:25]
	s_waitcnt lgkmcnt(1)
	v_mfma_f32_16x16x32_bf16 v[112:115], v[206:209], v[164:167], v[112:115]
	v_mfma_f32_16x16x32_bf16 v[46:49], v[206:209], v[190:193], v[46:49]
	v_mfma_f32_16x16x32_bf16 v[14:17], v[206:209], v[194:197], v[14:17]
	s_waitcnt lgkmcnt(0)
	v_mfma_f32_16x16x32_bf16 v[70:73], v[210:213], v[164:167], v[70:73]
	v_mfma_f32_16x16x32_bf16 v[38:41], v[210:213], v[190:193], v[38:41]
	v_mfma_f32_16x16x32_bf16 v[6:9], v[210:213], v[194:197], v[6:9]
	ds_read_b128 v[198:201], v215 offset:8192
	ds_read_b128 v[202:205], v215 offset:10240
	ds_read_b128 v[206:209], v215 offset:12288
	ds_read_b128 v[210:213], v215 offset:14336
	s_waitcnt lgkmcnt(3)
	v_mfma_f32_16x16x32_bf16 v[148:151], v[198:201], v[164:167], v[148:151]
	v_mfma_f32_16x16x32_bf16 v[58:61], v[198:201], v[190:193], v[58:61]
	v_mfma_f32_16x16x32_bf16 v[26:29], v[198:201], v[194:197], v[26:29]
	s_waitcnt lgkmcnt(2)
	v_mfma_f32_16x16x32_bf16 v[116:119], v[202:205], v[164:167], v[116:119]
	v_mfma_f32_16x16x32_bf16 v[50:53], v[202:205], v[190:193], v[50:53]
	v_mfma_f32_16x16x32_bf16 v[18:21], v[202:205], v[194:197], v[18:21]
	s_waitcnt lgkmcnt(1)
	v_mfma_f32_16x16x32_bf16 v[92:95], v[206:209], v[164:167], v[92:95]
	v_mfma_f32_16x16x32_bf16 v[42:45], v[206:209], v[190:193], v[42:45]
	v_mfma_f32_16x16x32_bf16 v[10:13], v[206:209], v[194:197], v[10:13]
	s_waitcnt lgkmcnt(0)
	v_mfma_f32_16x16x32_bf16 v[66:69], v[210:213], v[164:167], v[66:69]
	v_mfma_f32_16x16x32_bf16 v[34:37], v[210:213], v[190:193], v[34:37]
	v_mfma_f32_16x16x32_bf16 v[2:5], v[210:213], v[194:197], v[2:5]
	v_add_u32_e32 v216, v173, v175
	ds_read_b128 v[164:167], v216 offset:32768
	ds_read_b128 v[190:193], v216 offset:34816
	v_add_u32_e32 v217, v176, v175
	ds_read_b128 v[194:197], v216 offset:36864
	ds_read_b128 v[198:201], v217
	ds_read_b128 v[202:205], v217 offset:2048
	ds_read_b128 v[206:209], v217 offset:4096
	ds_read_b128 v[210:213], v217 offset:6144
	s_waitcnt lgkmcnt(3)
	v_mfma_f32_16x16x32_bf16 v[152:155], v[198:201], v[164:167], v[152:155]
	v_mfma_f32_16x16x32_bf16 v[62:65], v[198:201], v[190:193], v[62:65]
	v_mfma_f32_16x16x32_bf16 v[30:33], v[198:201], v[194:197], v[30:33]
	s_waitcnt lgkmcnt(2)
	v_mfma_f32_16x16x32_bf16 v[120:123], v[202:205], v[164:167], v[120:123]
	v_mfma_f32_16x16x32_bf16 v[54:57], v[202:205], v[190:193], v[54:57]
	v_mfma_f32_16x16x32_bf16 v[22:25], v[202:205], v[194:197], v[22:25]
	s_waitcnt lgkmcnt(1)
	v_mfma_f32_16x16x32_bf16 v[112:115], v[206:209], v[164:167], v[112:115]
	v_mfma_f32_16x16x32_bf16 v[46:49], v[206:209], v[190:193], v[46:49]
	v_mfma_f32_16x16x32_bf16 v[14:17], v[206:209], v[194:197], v[14:17]
	s_waitcnt lgkmcnt(0)
	v_mfma_f32_16x16x32_bf16 v[70:73], v[210:213], v[164:167], v[70:73]
	v_mfma_f32_16x16x32_bf16 v[38:41], v[210:213], v[190:193], v[38:41]
	v_mfma_f32_16x16x32_bf16 v[6:9], v[210:213], v[194:197], v[6:9]
	ds_read_b128 v[198:201], v217 offset:8192
	ds_read_b128 v[202:205], v217 offset:10240
	ds_read_b128 v[206:209], v217 offset:12288
	ds_read_b128 v[210:213], v217 offset:14336
	s_min_u32 s12, s0, 29
	s_lshl_b32 s12, s12, 7
	s_waitcnt vmcnt(9)
	ds_write_b128 v189, v[132:135] offset:38912
	s_waitcnt vmcnt(8)
	ds_write_b128 v181, v[124:127] offset:39936
	s_waitcnt vmcnt(7)
	ds_write_b128 v189, v[140:143] offset:40960
	s_waitcnt vmcnt(6)
	ds_write_b128 v181, v[144:147] offset:41984
	s_waitcnt vmcnt(5)
	ds_write_b128 v189, v[128:131] offset:43008
	s_waitcnt vmcnt(4)
	ds_write_b128 v181, v[136:139] offset:44032
	s_addk_i32 s12, 0x100
	s_waitcnt lgkmcnt(9)
	v_mfma_f32_16x16x32_bf16 v[148:151], v[198:201], v[164:167], v[148:151]
	buffer_load_dwordx4 v[124:127], v182, s[4:7], s12 offen
	buffer_load_dwordx4 v[128:131], v183, s[4:7], s12 offen
	buffer_load_dwordx4 v[132:135], v184, s[4:7], s12 offen
	buffer_load_dwordx4 v[136:139], v185, s[4:7], s12 offen
	buffer_load_dwordx4 v[140:143], v186, s[4:7], s12 offen
	buffer_load_dwordx4 v[144:147], v187, s[4:7], s12 offen
	s_min_u32 s12, s0, 27
	s_waitcnt lgkmcnt(0)
	v_mfma_f32_16x16x32_bf16 v[116:119], v[202:205], v[164:167], v[116:119]
	s_barrier
	s_lshl_b32 s12, s12, 17
	v_mfma_f32_16x16x32_bf16 v[92:95], v[206:209], v[164:167], v[92:95]
	s_add_i32 s12, s12, 0x80000
	v_mfma_f32_16x16x32_bf16 v[66:69], v[210:213], v[164:167], v[66:69]
	v_cvt_pk_bf16_f32 v164, v96, v100
	v_cvt_pk_bf16_f32 v165, v104, v108
	v_cvt_pk_bf16_f32 v96, v97, v101
	v_cvt_pk_bf16_f32 v97, v105, v109
	ds_write2_b64 v188, v[164:165], v[96:97] offset1:16
	v_cvt_pk_bf16_f32 v96, v98, v102
	v_cvt_pk_bf16_f32 v97, v106, v110
	v_cvt_pk_bf16_f32 v98, v99, v103
	v_cvt_pk_bf16_f32 v99, v107, v111
	ds_write2_b64 v180, v[96:97], v[98:99] offset0:32 offset1:48
	buffer_load_dwordx4 v[96:99], v160, s[8:11], s12 offen
	buffer_load_dwordx4 v[100:103], v90, s[8:11], s12 offen
	buffer_load_dwordx4 v[104:107], v178, s[8:11], s12 offen
	buffer_load_dwordx4 v[108:111], v179, s[8:11], s12 offen
	v_mfma_f32_16x16x32_bf16 v[58:61], v[198:201], v[190:193], v[58:61]
	v_mfma_f32_16x16x32_bf16 v[26:29], v[198:201], v[194:197], v[26:29]
	v_mfma_f32_16x16x32_bf16 v[50:53], v[202:205], v[190:193], v[50:53]
	v_mfma_f32_16x16x32_bf16 v[18:21], v[202:205], v[194:197], v[18:21]
	v_mfma_f32_16x16x32_bf16 v[42:45], v[206:209], v[190:193], v[42:45]
	v_mfma_f32_16x16x32_bf16 v[10:13], v[206:209], v[194:197], v[10:13]
	v_mfma_f32_16x16x32_bf16 v[34:37], v[210:213], v[190:193], v[34:37]
	v_mfma_f32_16x16x32_bf16 v[2:5], v[210:213], v[194:197], v[2:5]
	ds_read_b128 v[164:167], v214 offset:38912
	ds_read_b128 v[190:193], v214 offset:40960
	ds_read_b128 v[194:197], v214 offset:43008
	ds_read_b128 v[198:201], v215 offset:16384
	ds_read_b128 v[202:205], v215 offset:18432
	ds_read_b128 v[206:209], v215 offset:20480
	ds_read_b128 v[210:213], v215 offset:22528
	s_waitcnt lgkmcnt(3)
	v_mfma_f32_16x16x32_bf16 v[152:155], v[198:201], v[164:167], v[152:155]
	v_mfma_f32_16x16x32_bf16 v[62:65], v[198:201], v[190:193], v[62:65]
	v_mfma_f32_16x16x32_bf16 v[30:33], v[198:201], v[194:197], v[30:33]
	s_waitcnt lgkmcnt(2)
	v_mfma_f32_16x16x32_bf16 v[120:123], v[202:205], v[164:167], v[120:123]
	v_mfma_f32_16x16x32_bf16 v[54:57], v[202:205], v[190:193], v[54:57]
	v_mfma_f32_16x16x32_bf16 v[22:25], v[202:205], v[194:197], v[22:25]
	s_waitcnt lgkmcnt(1)
	v_mfma_f32_16x16x32_bf16 v[112:115], v[206:209], v[164:167], v[112:115]
	v_mfma_f32_16x16x32_bf16 v[46:49], v[206:209], v[190:193], v[46:49]
	v_mfma_f32_16x16x32_bf16 v[14:17], v[206:209], v[194:197], v[14:17]
	s_waitcnt lgkmcnt(0)
	v_mfma_f32_16x16x32_bf16 v[70:73], v[210:213], v[164:167], v[70:73]
	v_mfma_f32_16x16x32_bf16 v[38:41], v[210:213], v[190:193], v[38:41]
	v_mfma_f32_16x16x32_bf16 v[6:9], v[210:213], v[194:197], v[6:9]
	ds_read_b128 v[198:201], v215 offset:24576
	ds_read_b128 v[202:205], v215 offset:26624
	ds_read_b128 v[206:209], v215 offset:28672
	ds_read_b128 v[210:213], v215 offset:30720
	s_waitcnt lgkmcnt(3)
	v_mfma_f32_16x16x32_bf16 v[148:151], v[198:201], v[164:167], v[148:151]
	v_mfma_f32_16x16x32_bf16 v[58:61], v[198:201], v[190:193], v[58:61]
	v_mfma_f32_16x16x32_bf16 v[26:29], v[198:201], v[194:197], v[26:29]
	s_waitcnt lgkmcnt(2)
	v_mfma_f32_16x16x32_bf16 v[116:119], v[202:205], v[164:167], v[116:119]
	v_mfma_f32_16x16x32_bf16 v[50:53], v[202:205], v[190:193], v[50:53]
	v_mfma_f32_16x16x32_bf16 v[18:21], v[202:205], v[194:197], v[18:21]
	s_waitcnt lgkmcnt(1)
	v_mfma_f32_16x16x32_bf16 v[92:95], v[206:209], v[164:167], v[92:95]
	v_mfma_f32_16x16x32_bf16 v[42:45], v[206:209], v[190:193], v[42:45]
	v_mfma_f32_16x16x32_bf16 v[10:13], v[206:209], v[194:197], v[10:13]
	s_waitcnt lgkmcnt(0)
	v_mfma_f32_16x16x32_bf16 v[66:69], v[210:213], v[164:167], v[66:69]
	v_mfma_f32_16x16x32_bf16 v[34:37], v[210:213], v[190:193], v[34:37]
	v_mfma_f32_16x16x32_bf16 v[2:5], v[210:213], v[194:197], v[2:5]
	ds_read_b128 v[164:167], v216 offset:38912
	ds_read_b128 v[190:193], v216 offset:40960
	ds_read_b128 v[194:197], v216 offset:43008
	ds_read_b128 v[198:201], v217 offset:16384
	ds_read_b128 v[202:205], v217 offset:18432
	ds_read_b128 v[206:209], v217 offset:20480
	ds_read_b128 v[210:213], v217 offset:22528
	s_waitcnt lgkmcnt(3)
	v_mfma_f32_16x16x32_bf16 v[152:155], v[198:201], v[164:167], v[152:155]
	v_mfma_f32_16x16x32_bf16 v[62:65], v[198:201], v[190:193], v[62:65]
	v_mfma_f32_16x16x32_bf16 v[30:33], v[198:201], v[194:197], v[30:33]
	s_waitcnt lgkmcnt(2)
	v_mfma_f32_16x16x32_bf16 v[120:123], v[202:205], v[164:167], v[120:123]
	v_mfma_f32_16x16x32_bf16 v[54:57], v[202:205], v[190:193], v[54:57]
	v_mfma_f32_16x16x32_bf16 v[22:25], v[202:205], v[194:197], v[22:25]
	s_waitcnt lgkmcnt(1)
	v_mfma_f32_16x16x32_bf16 v[112:115], v[206:209], v[164:167], v[112:115]
	v_mfma_f32_16x16x32_bf16 v[46:49], v[206:209], v[190:193], v[46:49]
	v_mfma_f32_16x16x32_bf16 v[14:17], v[206:209], v[194:197], v[14:17]
	s_waitcnt lgkmcnt(0)
	v_mfma_f32_16x16x32_bf16 v[70:73], v[210:213], v[164:167], v[70:73]
	v_mfma_f32_16x16x32_bf16 v[38:41], v[210:213], v[190:193], v[38:41]
	v_mfma_f32_16x16x32_bf16 v[6:9], v[210:213], v[194:197], v[6:9]
	ds_read_b128 v[198:201], v217 offset:24576
	ds_read_b128 v[202:205], v217 offset:26624
	ds_read_b128 v[206:209], v217 offset:28672
	ds_read_b128 v[210:213], v217 offset:30720
	s_lshl_b32 s1, s1, 7
	s_waitcnt vmcnt(9)
	ds_write_b128 v189, v[124:127] offset:32768
	s_waitcnt vmcnt(8)
	ds_write_b128 v181, v[128:131] offset:33792
	s_waitcnt vmcnt(7)
	ds_write_b128 v189, v[132:135] offset:34816
	s_waitcnt vmcnt(6)
	ds_write_b128 v181, v[136:139] offset:35840
	s_waitcnt vmcnt(5)
	ds_write_b128 v189, v[140:143] offset:36864
	s_waitcnt vmcnt(4)
	ds_write_b128 v181, v[144:147] offset:37888
	s_addk_i32 s1, 0x180
	buffer_load_dwordx4 v[132:135], v182, s[4:7], s1 offen
	buffer_load_dwordx4 v[124:127], v183, s[4:7], s1 offen
	buffer_load_dwordx4 v[140:143], v184, s[4:7], s1 offen
	buffer_load_dwordx4 v[144:147], v185, s[4:7], s1 offen
	buffer_load_dwordx4 v[128:131], v186, s[4:7], s1 offen
	buffer_load_dwordx4 v[136:139], v187, s[4:7], s1 offen
	s_waitcnt lgkmcnt(9)
	v_mfma_f32_16x16x32_bf16 v[148:151], v[198:201], v[164:167], v[148:151]
	s_cmp_gt_u32 s0, 29
	s_waitcnt lgkmcnt(0)
	s_barrier
; #define LAS __attribute__((address_space(3)))
; DI unsigned pk2(float a, float b) { f32x2 v = {a, b}; bf16x2_t r = __builtin_convertvector(v, bf16x2_t); return __builtin_bit_cast(unsigned, r); }
; DI float sigmoidf_(float x) { return 1.f / (1.f + __expf(-x)); }
; #define MS_WLOAD(set, t) do { _Pragma("unroll") for (int r_ = 0; r_ < 4; ++r_) wr[set][r_] = __builtin_bit_cast(f32x4, __builtin_amdgcn_raw_buffer_load_b128(wrs, (int)wvo + r_ * LDW * 4, MS_CL(t) * (64 * LDW * 4), 0)); } while (0)
; #define MS_WCOMMIT(set, bufi) do { LAS unsigned char* wb_ = lds + (bufi) * MS_TILE; _Pragma("unroll") for (int i_ = 0; i_ < 4; ++i_) { \
;             u32x2 p_; p_.x = pk2(wr[set][0][i_], wr[set][1][i_]); p_.y = pk2(wr[set][2][i_], wr[set][3][i_]); \
;             *(LAS u32x2*)(wb_ + ((i_ < 2) ? lw0 : lw1) + i_ * 128) = p_; } } while (0)
; #define MS_XSLOAD(t) do { _Pragma("unroll") for (int i_ = 0; i_ < 6; ++i_) xs[i_] = __builtin_bit_cast(bf16x8, __builtin_amdgcn_raw_buffer_load_b128(xrs, (int)xso[i_], MS_CL(t) * 128, 0)); } while (0)
; #define MS_XSWRITE(bufi) do { _Pragma("unroll") for (int i_ = 0; i_ < 6; ++i_) *(LAS bf16x8*)(xw + (bufi) * MS_XBUF + i_ * 1024 + ((i_ & 1) ? (xwo ^ 64) : xwo)) = xs[i_]; } while (0)
;     ...
;             const LAS unsigned char* xr1 = lds + MS_XOFF + wave * MS_XWAVE + tk * 128 + (((4 + q) ^ rd_g) << 4);
;             __syncthreads();
;             MS_XSLOAD(0); MS_WLOAD(0, 0); MS_WLOAD(1, 1);
;             MS_WCOMMIT(0, 0); MS_WLOAD(0, 2);
;             MS_XSWRITE(0); MS_XSLOAD(1);
;             __syncthreads();
; #pragma unroll 1
;             for (int t = 0; t < NT; t += 2) { MS_STEP(0, 1, t); MS_STEP(1, 0, t + 1); }
; #pragma unroll
;             for (int mt = 0; mt < 3; ++mt) { const int tok = rp + wave * 48 + mt * 16 + tk;
;                 if (tok < M) {
;                     if (MODE == 0) { bf16* o = (bf16*)(ws + o_hid) + (size_t)(row0 + tok) * DEXP + slab * 64 + 4 * q;
; #pragma unroll
;                         for (int j = 0; j < 4; ++j) { float h[4];
; #pragma unroll
;                             for (int i = 0; i < 4; ++i) { const float gt = acc[mt][j][i]; h[i] = gt * sigmoidf_(gt) * acc[mt][j + 4][i]; }
;                             *(u32x2*)(o + 16 * j) = (u32x2){pk2(h[0], h[1]), pk2(h[2], h[3])}; }
	v_mfma_f32_16x16x32_bf16 v[58:61], v[198:201], v[190:193], v[58:61]
	v_mfma_f32_16x16x32_bf16 v[26:29], v[198:201], v[194:197], v[26:29]
	v_mfma_f32_16x16x32_bf16 v[116:119], v[202:205], v[164:167], v[116:119]
	v_mfma_f32_16x16x32_bf16 v[50:53], v[202:205], v[190:193], v[50:53]
	v_mfma_f32_16x16x32_bf16 v[18:21], v[202:205], v[194:197], v[18:21]
	v_mfma_f32_16x16x32_bf16 v[92:95], v[206:209], v[164:167], v[92:95]
	v_mfma_f32_16x16x32_bf16 v[42:45], v[206:209], v[190:193], v[42:45]
	v_mfma_f32_16x16x32_bf16 v[10:13], v[206:209], v[194:197], v[10:13]
	v_mfma_f32_16x16x32_bf16 v[66:69], v[210:213], v[164:167], v[66:69]
	v_mfma_f32_16x16x32_bf16 v[34:37], v[210:213], v[190:193], v[34:37]
	v_mfma_f32_16x16x32_bf16 v[2:5], v[210:213], v[194:197], v[2:5]
	s_cbranch_scc0 .LBB0_1720
	v_add_u32_e32 v76, s31, v177
	v_cmp_gt_i32_e32 vcc, s28, v76
	s_and_saveexec_b64 s[12:13], vcc
	s_cbranch_execz .LBB0_1723
	v_mul_f32_e32 v77, 0xbfb8aa3b, v152
	v_exp_f32_e32 v78, v77
	v_mul_f32_e32 v77, 0xbfb8aa3b, v153
	v_exp_f32_e32 v79, v77
	v_add_u32_e32 v74, s29, v76
	v_ashrrev_i32_e32 v75, 31, v74
	v_lshlrev_b64 v[74:75], 10, v[74:75]
	v_pk_add_f32 v[78:79], v[78:79], 1.0 op_sel_hi:[1,0]
	v_lshl_add_u64 v[74:75], v[158:159], 0, v[74:75]
	v_rcp_f32_e32 v79, v79
	v_rcp_f32_e32 v78, v78
	v_mul_f32_e32 v77, 0xbfb8aa3b, v154
	v_exp_f32_e32 v80, v77
	v_mul_f32_e32 v77, 0xbfb8aa3b, v155
	v_exp_f32_e32 v81, v77
	v_pk_mul_f32 v[78:79], v[152:153], v[78:79]
	v_pk_add_f32 v[80:81], v[80:81], 1.0 op_sel_hi:[1,0]
	s_nop 0
	v_pk_mul_f32 v[78:79], v[78:79], v[148:149]
	v_rcp_f32_e32 v81, v81
	v_cvt_pk_bf16_f32 v78, v78, v79
	v_rcp_f32_e32 v80, v80
	s_nop 0
	v_pk_mul_f32 v[80:81], v[154:155], v[80:81]
	v_mul_f32_e32 v77, 0xbfb8aa3b, v120
	v_pk_mul_f32 v[80:81], v[80:81], v[150:151]
	s_nop 0
	v_cvt_pk_bf16_f32 v79, v80, v81
	global_store_dwordx2 v[74:75], v[78:79], off
	v_exp_f32_e32 v78, v77
	v_mul_f32_e32 v77, 0xbfb8aa3b, v121
	v_exp_f32_e32 v79, v77
	s_nop 0
	v_pk_add_f32 v[78:79], v[78:79], 1.0 op_sel_hi:[1,0]
	s_nop 0
	v_rcp_f32_e32 v79, v79
	v_rcp_f32_e32 v78, v78
	v_mul_f32_e32 v77, 0xbfb8aa3b, v122
	v_exp_f32_e32 v80, v77
	v_mul_f32_e32 v77, 0xbfb8aa3b, v123
	v_exp_f32_e32 v81, v77
	v_pk_mul_f32 v[78:79], v[120:121], v[78:79]
	v_pk_add_f32 v[80:81], v[80:81], 1.0 op_sel_hi:[1,0]
	s_nop 0
	v_pk_mul_f32 v[78:79], v[78:79], v[116:117]
	v_rcp_f32_e32 v81, v81
	v_cvt_pk_bf16_f32 v78, v78, v79
	v_rcp_f32_e32 v80, v80
	s_nop 0
	v_pk_mul_f32 v[80:81], v[122:123], v[80:81]
	v_mul_f32_e32 v77, 0xbfb8aa3b, v112
	v_pk_mul_f32 v[80:81], v[80:81], v[118:119]
	s_nop 0
	v_cvt_pk_bf16_f32 v79, v80, v81
	global_store_dwordx2 v[74:75], v[78:79], off offset:32
	v_exp_f32_e32 v78, v77
	v_mul_f32_e32 v77, 0xbfb8aa3b, v113
	v_exp_f32_e32 v79, v77
	s_nop 0
	v_pk_add_f32 v[78:79], v[78:79], 1.0 op_sel_hi:[1,0]
	s_nop 0
	v_rcp_f32_e32 v79, v79
	v_rcp_f32_e32 v78, v78
	v_mul_f32_e32 v77, 0xbfb8aa3b, v114
	v_exp_f32_e32 v80, v77
	v_mul_f32_e32 v77, 0xbfb8aa3b, v115
	v_exp_f32_e32 v81, v77
	v_pk_mul_f32 v[78:79], v[112:113], v[78:79]
	v_pk_add_f32 v[80:81], v[80:81], 1.0 op_sel_hi:[1,0]
	s_nop 0
	v_pk_mul_f32 v[78:79], v[78:79], v[92:93]
	v_rcp_f32_e32 v81, v81
	v_cvt_pk_bf16_f32 v78, v78, v79
	v_rcp_f32_e32 v80, v80
	s_nop 0
	v_pk_mul_f32 v[80:81], v[114:115], v[80:81]
	v_mul_f32_e32 v77, 0xbfb8aa3b, v70
	v_pk_mul_f32 v[80:81], v[80:81], v[94:95]
	s_nop 0
	v_cvt_pk_bf16_f32 v79, v80, v81
	global_store_dwordx2 v[74:75], v[78:79], off offset:64
	v_exp_f32_e32 v78, v77
	v_mul_f32_e32 v77, 0xbfb8aa3b, v71
	v_exp_f32_e32 v79, v77
	s_nop 0
	v_pk_add_f32 v[78:79], v[78:79], 1.0 op_sel_hi:[1,0]
	s_nop 0
	v_rcp_f32_e32 v79, v79
	v_rcp_f32_e32 v78, v78
	s_nop 0
	v_pk_mul_f32 v[70:71], v[70:71], v[78:79]
	s_nop 0
	v_pk_mul_f32 v[66:67], v[70:71], v[66:67]
	v_mul_f32_e32 v70, 0xbfb8aa3b, v72
	v_mul_f32_e32 v71, 0xbfb8aa3b, v73
	v_exp_f32_e32 v70, v70
	v_exp_f32_e32 v71, v71
	v_cvt_pk_bf16_f32 v66, v66, v67
	v_pk_add_f32 v[70:71], v[70:71], 1.0 op_sel_hi:[1,0]
	s_nop 0
	v_rcp_f32_e32 v71, v71
	v_rcp_f32_e32 v70, v70
	s_nop 0
	v_pk_mul_f32 v[70:71], v[72:73], v[70:71]
	s_nop 0
	v_pk_mul_f32 v[68:69], v[70:71], v[68:69]
	s_nop 0
	v_cvt_pk_bf16_f32 v67, v68, v69
	global_store_dwordx2 v[74:75], v[66:67], off offset:96
; DI unsigned pk2(float a, float b) { f32x2 v = {a, b}; bf16x2_t r = __builtin_convertvector(v, bf16x2_t); return __builtin_bit_cast(unsigned, r); }
; DI float sigmoidf_(float x) { return 1.f / (1.f + __expf(-x)); }
;     ...
;             for (int mt = 0; mt < 3; ++mt) { const int tok = rp + wave * 48 + mt * 16 + tk;
;                 if (tok < M) {
;                     if (MODE == 0) { bf16* o = (bf16*)(ws + o_hid) + (size_t)(row0 + tok) * DEXP + slab * 64 + 4 * q;
; #pragma unroll
;                         for (int j = 0; j < 4; ++j) { float h[4];
; #pragma unroll
;                             for (int i = 0; i < 4; ++i) { const float gt = acc[mt][j][i]; h[i] = gt * sigmoidf_(gt) * acc[mt][j + 4][i]; }
;                             *(u32x2*)(o + 16 * j) = (u32x2){pk2(h[0], h[1]), pk2(h[2], h[3])}; }
.LBB0_1723:
	s_or_b64 exec, exec, s[12:13]
	v_add_u32_e32 v66, 16, v76
	v_cmp_gt_i32_e32 vcc, s28, v66
	s_and_saveexec_b64 s[12:13], vcc
	s_cbranch_execz .LBB0_1725
	v_mul_f32_e32 v68, 0xbfb8aa3b, v62
	v_mul_f32_e32 v69, 0xbfb8aa3b, v63
	v_exp_f32_e32 v68, v68
	v_exp_f32_e32 v69, v69
	v_add_u32_e32 v66, s29, v66
	v_ashrrev_i32_e32 v67, 31, v66
	v_lshlrev_b64 v[66:67], 10, v[66:67]
	v_pk_add_f32 v[68:69], v[68:69], 1.0 op_sel_hi:[1,0]
	v_lshl_add_u64 v[66:67], v[158:159], 0, v[66:67]
	v_rcp_f32_e32 v69, v69
	v_rcp_f32_e32 v68, v68
	s_nop 0
	v_pk_mul_f32 v[62:63], v[62:63], v[68:69]
	s_nop 0
	v_pk_mul_f32 v[58:59], v[62:63], v[58:59]
	v_mul_f32_e32 v62, 0xbfb8aa3b, v64
	v_mul_f32_e32 v63, 0xbfb8aa3b, v65
	v_exp_f32_e32 v62, v62
	v_exp_f32_e32 v63, v63
	v_cvt_pk_bf16_f32 v58, v58, v59
	v_pk_add_f32 v[62:63], v[62:63], 1.0 op_sel_hi:[1,0]
	s_nop 0
	v_rcp_f32_e32 v63, v63
	v_rcp_f32_e32 v62, v62
	s_nop 0
	v_pk_mul_f32 v[62:63], v[64:65], v[62:63]
	s_nop 0
	v_pk_mul_f32 v[60:61], v[62:63], v[60:61]
	s_nop 0
	v_cvt_pk_bf16_f32 v59, v60, v61
	global_store_dwordx2 v[66:67], v[58:59], off
	v_mul_f32_e32 v58, 0xbfb8aa3b, v54
	v_mul_f32_e32 v59, 0xbfb8aa3b, v55
	v_exp_f32_e32 v58, v58
	v_exp_f32_e32 v59, v59
	s_nop 0
	v_pk_add_f32 v[58:59], v[58:59], 1.0 op_sel_hi:[1,0]
	s_nop 0
	v_rcp_f32_e32 v59, v59
	v_rcp_f32_e32 v58, v58
	s_nop 0
	v_pk_mul_f32 v[54:55], v[54:55], v[58:59]
	s_nop 0
	v_pk_mul_f32 v[50:51], v[54:55], v[50:51]
	v_mul_f32_e32 v54, 0xbfb8aa3b, v56
	v_mul_f32_e32 v55, 0xbfb8aa3b, v57
	v_exp_f32_e32 v54, v54
	v_exp_f32_e32 v55, v55
	v_cvt_pk_bf16_f32 v50, v50, v51
	v_pk_add_f32 v[54:55], v[54:55], 1.0 op_sel_hi:[1,0]
	s_nop 0
	v_rcp_f32_e32 v55, v55
	v_rcp_f32_e32 v54, v54
	s_nop 0
	v_pk_mul_f32 v[54:55], v[56:57], v[54:55]
	s_nop 0
	v_pk_mul_f32 v[52:53], v[54:55], v[52:53]
	s_nop 0
	v_cvt_pk_bf16_f32 v51, v52, v53
	global_store_dwordx2 v[66:67], v[50:51], off offset:32
	v_mul_f32_e32 v50, 0xbfb8aa3b, v46
	v_mul_f32_e32 v51, 0xbfb8aa3b, v47
	v_exp_f32_e32 v50, v50
	v_exp_f32_e32 v51, v51
	s_nop 0
	v_pk_add_f32 v[50:51], v[50:51], 1.0 op_sel_hi:[1,0]
	s_nop 0
	v_rcp_f32_e32 v51, v51
	v_rcp_f32_e32 v50, v50
	s_nop 0
	v_pk_mul_f32 v[46:47], v[46:47], v[50:51]
	s_nop 0
	v_pk_mul_f32 v[42:43], v[46:47], v[42:43]
	v_mul_f32_e32 v46, 0xbfb8aa3b, v48
	v_mul_f32_e32 v47, 0xbfb8aa3b, v49
	v_exp_f32_e32 v46, v46
	v_exp_f32_e32 v47, v47
	v_cvt_pk_bf16_f32 v42, v42, v43
	v_pk_add_f32 v[46:47], v[46:47], 1.0 op_sel_hi:[1,0]
	s_nop 0
	v_rcp_f32_e32 v47, v47
	v_rcp_f32_e32 v46, v46
	s_nop 0
	v_pk_mul_f32 v[46:47], v[48:49], v[46:47]
	s_nop 0
	v_pk_mul_f32 v[44:45], v[46:47], v[44:45]
	s_nop 0
	v_cvt_pk_bf16_f32 v43, v44, v45
	global_store_dwordx2 v[66:67], v[42:43], off offset:64
	v_mul_f32_e32 v42, 0xbfb8aa3b, v38
	v_mul_f32_e32 v43, 0xbfb8aa3b, v39
	v_exp_f32_e32 v42, v42
	v_exp_f32_e32 v43, v43
	s_nop 0
	v_pk_add_f32 v[42:43], v[42:43], 1.0 op_sel_hi:[1,0]
	s_nop 0
	v_rcp_f32_e32 v43, v43
	v_rcp_f32_e32 v42, v42
	s_nop 0
	v_pk_mul_f32 v[38:39], v[38:39], v[42:43]
	s_nop 0
	v_pk_mul_f32 v[34:35], v[38:39], v[34:35]
	v_mul_f32_e32 v38, 0xbfb8aa3b, v40
	v_mul_f32_e32 v39, 0xbfb8aa3b, v41
	v_exp_f32_e32 v38, v38
	v_exp_f32_e32 v39, v39
	v_cvt_pk_bf16_f32 v34, v34, v35
	v_pk_add_f32 v[38:39], v[38:39], 1.0 op_sel_hi:[1,0]
	s_nop 0
	v_rcp_f32_e32 v39, v39
	v_rcp_f32_e32 v38, v38
	s_nop 0
	v_pk_mul_f32 v[38:39], v[40:41], v[38:39]
	s_nop 0
	v_pk_mul_f32 v[36:37], v[38:39], v[36:37]
	s_nop 0
	v_cvt_pk_bf16_f32 v35, v36, v37
	global_store_dwordx2 v[66:67], v[34:35], off offset:96
.LBB0_1725:
	s_or_b64 exec, exec, s[12:13]
	v_add_u32_e32 v34, 32, v76
	v_cmp_gt_i32_e32 vcc, s28, v34
	s_and_saveexec_b64 s[12:13], vcc
	s_cbranch_execz .LBB0_1718
	v_mul_f32_e32 v36, 0xbfb8aa3b, v30
	v_mul_f32_e32 v37, 0xbfb8aa3b, v31
	v_exp_f32_e32 v36, v36
	v_exp_f32_e32 v37, v37
	v_add_u32_e32 v34, s29, v34
	v_ashrrev_i32_e32 v35, 31, v34
	v_lshlrev_b64 v[34:35], 10, v[34:35]
	v_pk_add_f32 v[36:37], v[36:37], 1.0 op_sel_hi:[1,0]
	v_lshl_add_u64 v[34:35], v[158:159], 0, v[34:35]
	v_rcp_f32_e32 v37, v37
	v_rcp_f32_e32 v36, v36
	s_nop 0
	v_pk_mul_f32 v[30:31], v[30:31], v[36:37]
	s_nop 0
	v_pk_mul_f32 v[26:27], v[30:31], v[26:27]
	v_mul_f32_e32 v30, 0xbfb8aa3b, v32
	v_mul_f32_e32 v31, 0xbfb8aa3b, v33
	v_exp_f32_e32 v30, v30
	v_exp_f32_e32 v31, v31
	v_cvt_pk_bf16_f32 v26, v26, v27
	v_pk_add_f32 v[30:31], v[30:31], 1.0 op_sel_hi:[1,0]
	s_nop 0
	v_rcp_f32_e32 v31, v31
	v_rcp_f32_e32 v30, v30
	s_nop 0
	v_pk_mul_f32 v[30:31], v[32:33], v[30:31]
	s_nop 0
	v_pk_mul_f32 v[28:29], v[30:31], v[28:29]
	s_nop 0
	v_cvt_pk_bf16_f32 v27, v28, v29
	global_store_dwordx2 v[34:35], v[26:27], off
	v_mul_f32_e32 v26, 0xbfb8aa3b, v22
	v_mul_f32_e32 v27, 0xbfb8aa3b, v23
	v_exp_f32_e32 v26, v26
	v_exp_f32_e32 v27, v27
	s_nop 0
	v_pk_add_f32 v[26:27], v[26:27], 1.0 op_sel_hi:[1,0]
	s_nop 0
	v_rcp_f32_e32 v27, v27
	v_rcp_f32_e32 v26, v26
	s_nop 0
	v_pk_mul_f32 v[22:23], v[22:23], v[26:27]
	s_nop 0
	v_pk_mul_f32 v[18:19], v[22:23], v[18:19]
	v_mul_f32_e32 v22, 0xbfb8aa3b, v24
	v_mul_f32_e32 v23, 0xbfb8aa3b, v25
	v_exp_f32_e32 v22, v22
	v_exp_f32_e32 v23, v23
	v_cvt_pk_bf16_f32 v18, v18, v19
	v_pk_add_f32 v[22:23], v[22:23], 1.0 op_sel_hi:[1,0]
	s_nop 0
	v_rcp_f32_e32 v23, v23
	v_rcp_f32_e32 v22, v22
	s_nop 0
	v_pk_mul_f32 v[22:23], v[24:25], v[22:23]
	s_nop 0
	v_pk_mul_f32 v[20:21], v[22:23], v[20:21]
	s_nop 0
	v_cvt_pk_bf16_f32 v19, v20, v21
	global_store_dwordx2 v[34:35], v[18:19], off offset:32
	v_mul_f32_e32 v18, 0xbfb8aa3b, v14
	v_mul_f32_e32 v19, 0xbfb8aa3b, v15
	v_exp_f32_e32 v18, v18
	v_exp_f32_e32 v19, v19
	s_nop 0
	v_pk_add_f32 v[18:19], v[18:19], 1.0 op_sel_hi:[1,0]
	s_nop 0
	v_rcp_f32_e32 v19, v19
	v_rcp_f32_e32 v18, v18
	s_nop 0
	v_pk_mul_f32 v[14:15], v[14:15], v[18:19]
	s_nop 0
	v_pk_mul_f32 v[10:11], v[14:15], v[10:11]
	v_mul_f32_e32 v14, 0xbfb8aa3b, v16
	v_mul_f32_e32 v15, 0xbfb8aa3b, v17
	v_exp_f32_e32 v14, v14
	v_exp_f32_e32 v15, v15
	v_cvt_pk_bf16_f32 v10, v10, v11
	v_pk_add_f32 v[14:15], v[14:15], 1.0 op_sel_hi:[1,0]
	s_nop 0
	v_rcp_f32_e32 v15, v15
	v_rcp_f32_e32 v14, v14
	s_nop 0
	v_pk_mul_f32 v[14:15], v[16:17], v[14:15]
	s_nop 0
	v_pk_mul_f32 v[12:13], v[14:15], v[12:13]
	s_nop 0
	v_cvt_pk_bf16_f32 v11, v12, v13
	global_store_dwordx2 v[34:35], v[10:11], off offset:64
	v_mul_f32_e32 v10, 0xbfb8aa3b, v6
	v_mul_f32_e32 v11, 0xbfb8aa3b, v7
	v_exp_f32_e32 v10, v10
	v_exp_f32_e32 v11, v11
	s_nop 0
	v_pk_add_f32 v[10:11], v[10:11], 1.0 op_sel_hi:[1,0]
	s_nop 0
	v_rcp_f32_e32 v11, v11
	v_rcp_f32_e32 v10, v10
	s_nop 0
	v_pk_mul_f32 v[6:7], v[6:7], v[10:11]
	s_nop 0
	v_pk_mul_f32 v[2:3], v[6:7], v[2:3]
	v_mul_f32_e32 v6, 0xbfb8aa3b, v8
	v_mul_f32_e32 v7, 0xbfb8aa3b, v9
	v_exp_f32_e32 v6, v6
	v_exp_f32_e32 v7, v7
	v_cvt_pk_bf16_f32 v2, v2, v3
	v_pk_add_f32 v[6:7], v[6:7], 1.0 op_sel_hi:[1,0]
	s_nop 0
	v_rcp_f32_e32 v7, v7
	v_rcp_f32_e32 v6, v6
	s_nop 0
	v_pk_mul_f32 v[6:7], v[8:9], v[6:7]
	s_nop 0
	v_pk_mul_f32 v[4:5], v[6:7], v[4:5]
	s_nop 0
	v_cvt_pk_bf16_f32 v3, v4, v5
	global_store_dwordx2 v[34:35], v[2:3], off offset:96
	s_branch .LBB0_1718
